# speedup vs baseline: 1.0260x; 1.0209x over previous
_Z4ln_kPKfS0_S0_S0_PfPDF16_:
	v_lshlrev_b32_e32 v64, 4, v0
	s_getpc_b64 s[92:93]
	s_add_u32 s92, s92, 0xa2f8
	s_addc_u32 s93, s93, 0x0
	global_load_dwordx4 v[60:63], v64, s[92:93]
	v_add_u32_e32 v64, 0x1000, v64
	global_load_dwordx4 v[60:63], v64, s[92:93]
	v_add_u32_e32 v64, 0x1000, v64
	global_load_dwordx4 v[60:63], v64, s[92:93]
	v_add_u32_e32 v64, 0x1000, v64
	global_load_dwordx4 v[60:63], v64, s[92:93]
	v_lshlrev_b32_e32 v64, 4, v0
	s_load_dwordx8 s[4:11], s[0:1], 0x0
	v_lshrrev_b32_e32 v1, 6, v0
	v_lshl_or_b32 v54, s2, 2, v1
	s_movk_i32 s12, 0xc00
	v_and_b32_e32 v55, 63, v0
	s_waitcnt lgkmcnt(0)
	v_mov_b64_e32 v[2:3], s[4:5]
	v_mad_i64_i32 v[4:5], s[2:3], v54, s12, v[2:3]
	v_mov_b64_e32 v[2:3], s[6:7]
	v_mad_i64_i32 v[6:7], s[2:3], v54, s12, v[2:3]
	v_lshlrev_b32_e32 v2, 4, v55
	v_mov_b32_e32 v3, 0
	v_lshl_add_u64 v[30:31], v[6:7], 0, v[2:3]
	v_lshl_add_u64 v[28:29], v[4:5], 0, v[2:3]
	global_load_dwordx4 v[4:7], v[30:31], off
	global_load_dwordx4 v[8:11], v[28:29], off
	global_load_dwordx4 v[12:15], v[28:29], off offset:1024
	global_load_dwordx4 v[16:19], v[30:31], off offset:1024
	global_load_dwordx4 v[20:23], v[28:29], off offset:2048
	global_load_dwordx4 v[24:27], v[30:31], off offset:2048
	s_nop 0
	global_load_dwordx4 v[28:31], v2, s[8:9]
	global_load_dwordx4 v[32:35], v2, s[10:11]
	global_load_dwordx4 v[36:39], v2, s[8:9] offset:1024
	global_load_dwordx4 v[40:43], v2, s[10:11] offset:1024
	s_load_dwordx4 s[4:7], s[0:1], 0x20
	v_and_b32_e32 v50, 16, v0
	v_cmp_eq_u32_e32 vcc, 0, v50
	v_and_b32_e32 v51, 32, v0
	v_mov_b32_e32 v56, 0x2b8cbccc
	s_waitcnt lgkmcnt(0)
	v_mov_b64_e32 v[0:1], s[4:5]
	v_mad_i64_i32 v[0:1], s[0:1], v54, s12, v[0:1]
	v_cmp_eq_u32_e64 s[0:1], 0, v51
	s_mov_b32 s3, 0xf800000
	s_movk_i32 s2, 0x680
	v_mov_b64_e32 v[44:45], s[6:7]
	v_mov_b32_e32 v57, 0x260
	s_waitcnt vmcnt(8)
	v_pk_add_f32 v[46:47], v[8:9], v[4:5]
	v_pk_add_f32 v[48:49], v[10:11], v[6:7]
	global_load_dwordx4 v[4:7], v2, s[8:9] offset:2048
	global_load_dwordx4 v[8:11], v2, s[10:11] offset:2048
	s_waitcnt vmcnt(8)
	v_pk_add_f32 v[12:13], v[12:13], v[16:17]
	s_waitcnt vmcnt(6)
	v_pk_add_f32 v[16:17], v[20:21], v[24:25]
	v_pk_add_f32 v[14:15], v[14:15], v[18:19]
	v_pk_add_f32 v[18:19], v[22:23], v[26:27]
	v_add_f32_e32 v52, v46, v47
	v_mov_b32_e32 v20, v12
	v_mov_b32_e32 v21, v16
	v_mov_b32_e32 v22, v13
	v_mov_b32_e32 v23, v17
	v_mov_b32_e32 v24, v14
	v_mov_b32_e32 v25, v18
	v_add_f32_e32 v52, v52, v48
	v_pk_add_f32 v[20:21], v[20:21], v[22:23]
	v_mov_b32_e32 v26, v15
	v_mov_b32_e32 v27, v19
	v_add_f32_e32 v22, v52, v49
	v_pk_add_f32 v[20:21], v[20:21], v[24:25]
	v_add_f32_e32 v22, 0, v22
	v_pk_add_f32 v[20:21], v[20:21], v[26:27]
	s_nop 0
	v_add_f32_e32 v20, v22, v20
	v_add_f32_e32 v20, v20, v21
	s_nop 1
	v_add_f32_dpp v20, v20, v20 quad_perm:[1,0,3,2] row_mask:0xf bank_mask:0xf bound_ctrl:1
	s_nop 1
	v_add_f32_dpp v20, v20, v20 quad_perm:[2,3,0,1] row_mask:0xf bank_mask:0xf bound_ctrl:1
	s_nop 1
	v_add_f32_dpp v20, v20, v20 row_half_mirror row_mask:0xf bank_mask:0xf bound_ctrl:1
	s_nop 1
	v_add_f32_dpp v20, v20, v20 row_mirror row_mask:0xf bank_mask:0xf bound_ctrl:1
	v_mov_b32_e32 v21, v20
	v_mov_b32_e32 v22, v20
	s_nop 1
	v_permlane16_swap_b32_e32 v21, v22
	v_cndmask_b32_e32 v21, v21, v22, vcc
	v_add_f32_e32 v20, v20, v21
	v_mov_b32_e32 v21, v20
	v_mov_b32_e32 v22, v20
	s_nop 1
	v_permlane32_swap_b32_e32 v21, v22
	v_cndmask_b32_e64 v21, v21, v22, s[0:1]
	v_add_f32_e32 v20, v20, v21
	v_mul_f32_e32 v20, 0x3aaaaaab, v20
	v_pk_add_f32 v[22:23], v[46:47], v[20:21] op_sel_hi:[1,0] neg_lo:[0,1] neg_hi:[0,1]
	v_pk_add_f32 v[16:17], v[16:17], v[20:21] op_sel_hi:[1,0] neg_lo:[0,1] neg_hi:[0,1]
	v_pk_add_f32 v[24:25], v[48:49], v[20:21] op_sel_hi:[1,0] neg_lo:[0,1] neg_hi:[0,1]
	v_pk_add_f32 v[12:13], v[12:13], v[20:21] op_sel_hi:[1,0] neg_lo:[0,1] neg_hi:[0,1]
	v_mov_b32_e32 v48, v17
	v_mov_b32_e32 v49, v23
	v_pk_add_f32 v[14:15], v[14:15], v[20:21] op_sel_hi:[1,0] neg_lo:[0,1] neg_hi:[0,1]
	v_pk_add_f32 v[18:19], v[18:19], v[20:21] op_sel_hi:[1,0] neg_lo:[0,1] neg_hi:[0,1]
	v_pk_mul_f32 v[20:21], v[12:13], v[12:13]
	v_mov_b32_e32 v46, v16
	v_mov_b32_e32 v47, v22
	v_pk_mul_f32 v[48:49], v[48:49], v[48:49]
	v_pk_mul_f32 v[26:27], v[14:15], v[14:15]
	v_mov_b32_e32 v50, v18
	v_mov_b32_e32 v51, v24
	v_add_f32_e32 v58, v20, v21
	v_pk_fma_f32 v[20:21], v[46:47], v[46:47], v[48:49]
	v_mov_b32_e32 v52, v19
	v_mov_b32_e32 v53, v25
	v_add_f32_e32 v26, v26, v58
	v_pk_fma_f32 v[20:21], v[50:51], v[50:51], v[20:21]
	v_add_f32_e32 v26, v27, v26
	v_pk_fma_f32 v[20:21], v[52:53], v[52:53], v[20:21]
	s_nop 0
	v_add_f32_e32 v21, v21, v26
	v_add_f32_e32 v20, v20, v21
	s_nop 1
	v_add_f32_dpp v20, v20, v20 quad_perm:[1,0,3,2] row_mask:0xf bank_mask:0xf bound_ctrl:1
	s_nop 1
	v_add_f32_dpp v20, v20, v20 quad_perm:[2,3,0,1] row_mask:0xf bank_mask:0xf bound_ctrl:1
	s_nop 1
	v_add_f32_dpp v20, v20, v20 row_half_mirror row_mask:0xf bank_mask:0xf bound_ctrl:1
	s_nop 1
	v_add_f32_dpp v20, v20, v20 row_mirror row_mask:0xf bank_mask:0xf bound_ctrl:1
	v_mov_b32_e32 v21, v20
	v_mov_b32_e32 v26, v20
	s_nop 1
	v_permlane16_swap_b32_e32 v21, v26
	v_cndmask_b32_e32 v21, v21, v26, vcc
	v_add_f32_e32 v20, v20, v21
	v_mov_b32_e32 v21, v20
	v_mov_b32_e32 v26, v20
	s_nop 1
	v_permlane32_swap_b32_e32 v21, v26
	v_cndmask_b32_e64 v21, v21, v26, s[0:1]
	v_add_f32_e32 v20, v20, v21
	v_fmac_f32_e32 v56, 0x3aaaaaab, v20
	v_mul_f32_e32 v20, 0x4f800000, v56
	v_cmp_gt_f32_e32 vcc, s3, v56
	v_lshl_add_u64 v[26:27], v[0:1], 0, v[2:3]
	s_nop 0
	v_cndmask_b32_e32 v46, v56, v20, vcc
	v_sqrt_f32_e32 v47, v46
	v_mad_i64_i32 v[20:21], s[0:1], v54, s2, v[44:45]
	v_add_u32_e32 v0, -1, v47
	v_add_u32_e32 v1, 1, v47
	v_fma_f32 v2, -v0, v47, v46
	v_fma_f32 v44, -v1, v47, v46
	v_cmp_ge_f32_e64 s[0:1], 0, v2
	v_lshlrev_b32_e32 v2, 3, v55
	v_lshl_add_u64 v[20:21], v[20:21], 0, v[2:3]
	v_cndmask_b32_e64 v0, v47, v0, s[0:1]
	v_cmp_lt_f32_e64 s[0:1], 0, v44
	s_nop 1
	v_cndmask_b32_e64 v0, v0, v1, s[0:1]
	v_mul_f32_e32 v1, 0x37800000, v0
	v_cndmask_b32_e32 v0, v0, v1, vcc
	v_cmp_class_f32_e32 vcc, v46, v57
	s_nop 1
	v_cndmask_b32_e32 v0, v0, v46, vcc
	v_div_scale_f32 v1, s[0:1], v0, v0, 1.0
	v_rcp_f32_e32 v44, v1
	s_nop 0
	v_fma_f32 v2, -v1, v44, 1.0
	v_fmac_f32_e32 v44, v2, v44
	v_div_scale_f32 v2, vcc, 1.0, v0, 1.0
	v_mul_f32_e32 v3, v2, v44
	v_fma_f32 v45, -v1, v3, v2
	v_fmac_f32_e32 v3, v45, v44
	v_fma_f32 v1, -v1, v3, v2
	v_div_fmas_f32 v1, v1, v44, v3
	v_div_fixup_f32 v44, v1, v0, 1.0
	v_pk_mul_f32 v[0:1], v[22:23], v[44:45] op_sel_hi:[1,0]
	v_pk_mul_f32 v[2:3], v[24:25], v[44:45] op_sel_hi:[1,0]
	v_pk_mul_f32 v[12:13], v[12:13], v[44:45] op_sel_hi:[1,0]
	v_pk_mul_f32 v[14:15], v[14:15], v[44:45] op_sel_hi:[1,0]
	v_pk_mul_f32 v[16:17], v[16:17], v[44:45] op_sel_hi:[1,0]
	s_waitcnt vmcnt(4)
	v_pk_fma_f32 v[0:1], v[28:29], v[0:1], v[32:33]
	v_pk_fma_f32 v[2:3], v[30:31], v[2:3], v[34:35]
	s_waitcnt vmcnt(2)
	v_pk_fma_f32 v[12:13], v[12:13], v[36:37], v[40:41]
	v_pk_fma_f32 v[14:15], v[14:15], v[38:39], v[42:43]
	s_waitcnt vmcnt(0)
	v_pk_fma_f32 v[4:5], v[16:17], v[4:5], v[8:9]
	v_pk_mul_f32 v[8:9], v[18:19], v[44:45] op_sel_hi:[1,0]
	global_store_dwordx4 v[26:27], v[0:3], off sc1
	v_pk_fma_f32 v[6:7], v[8:9], v[6:7], v[10:11]
	s_nop 0
	v_cvt_pk_f16_f32 v3, v2, v3
	v_cvt_pk_f16_f32 v2, v0, v1
	v_cvt_pk_f16_f32 v1, v14, v15
	v_cvt_pk_f16_f32 v0, v12, v13
	global_store_dwordx2 v[20:21], v[2:3], off sc1
	global_store_dwordx4 v[26:27], v[12:15], off offset:1024 sc1
	global_store_dwordx2 v[20:21], v[0:1], off offset:512 sc1
	global_store_dwordx4 v[26:27], v[4:7], off offset:2048 sc1
	v_cvt_pk_f16_f32 v1, v6, v7
	v_cvt_pk_f16_f32 v0, v4, v5
	global_store_dwordx2 v[20:21], v[0:1], off offset:1024 sc1
	s_endpgm

.LBB2_1:
	global_load_dwordx4 v[24:27], v[18:19], off offset:-8
	v_and_b32_e32 v23, 4, v22
	v_mad_u32_u24 v23, v23, s6, v17
	v_cmp_gt_u32_e32 vcc, 0x200, v0
	s_and_saveexec_b64 s[2:3], vcc
	v_lshl_add_u64 v[28:29], v[18:19], 0, s[4:5]
	v_add_u32_e32 v35, 0x800, v17
	global_load_dwordx4 v[30:33], v[28:29], off offset:-8
	v_and_b32_e32 v34, 4, v22
	v_mad_u32_u24 v34, v34, s6, v35
	s_mov_b64 exec, s[2:3]
	s_waitcnt vmcnt(0)
	ds_write_b32 v23, v24
	ds_write_b32 v23, v25 offset:3088
	ds_write_b32 v23, v26 offset:6176
	ds_write_b32 v23, v27 offset:9264
	s_and_saveexec_b64 s[2:3], vcc
	ds_write_b32 v34, v30
	ds_write_b32 v34, v31 offset:3088
	ds_write_b32 v34, v32 offset:6176
	ds_write_b32 v34, v33 offset:9264
	s_mov_b64 exec, s[2:3]
	s_or_b64 exec, exec, s[2:3]
	v_add_f32_e32 v17, v10, v11
	v_mov_b32_e32 v18, v6
	v_mov_b32_e32 v19, v2
	v_mov_b32_e32 v22, v7
	v_mov_b32_e32 v23, v3
	v_add_f32_e32 v17, v17, v12
	v_pk_add_f32 v[18:19], v[18:19], v[22:23]
	v_mov_b32_e32 v22, v8
	v_mov_b32_e32 v23, v4
	v_add_f32_e32 v17, v17, v13
	v_pk_add_f32 v[18:19], v[18:19], v[22:23]
	v_mov_b32_e32 v22, v9
	v_mov_b32_e32 v23, v5
	v_add_f32_e32 v17, 0, v17
	v_pk_add_f32 v[18:19], v[18:19], v[22:23]
	v_and_b32_e32 v22, 16, v0
	v_add_f32_e32 v17, v17, v18
	v_add_f32_e32 v17, v17, v19
	v_cmp_eq_u32_e64 s[4:5], 0, v22
	v_and_b32_e32 v22, 32, v0
	v_add_f32_dpp v17, v17, v17 quad_perm:[1,0,3,2] row_mask:0xf bank_mask:0xf bound_ctrl:1
	v_cmp_eq_u32_e64 s[2:3], 0, v22
	v_lshrrev_b32_e32 v1, 1, v0
	v_add_f32_dpp v17, v17, v17 quad_perm:[2,3,0,1] row_mask:0xf bank_mask:0xf bound_ctrl:1
	v_and_b32_e32 v1, 28, v1
	s_waitcnt lgkmcnt(0)
	v_add_f32_dpp v17, v17, v17 row_half_mirror row_mask:0xf bank_mask:0xf bound_ctrl:1
	s_barrier
	s_nop 0
	v_add_f32_dpp v17, v17, v17 row_mirror row_mask:0xf bank_mask:0xf bound_ctrl:1
	v_mov_b32_e32 v18, v17
	v_mov_b32_e32 v19, v17
	s_nop 1
	v_permlane16_swap_b32_e32 v18, v19
	v_cndmask_b32_e64 v18, v18, v19, s[4:5]
	v_add_f32_e32 v17, v17, v18
	v_mov_b32_e32 v18, v17
	v_mov_b32_e32 v19, v17
	s_nop 1
	v_permlane32_swap_b32_e32 v18, v19
	v_cndmask_b32_e64 v18, v18, v19, s[2:3]
	v_add_f32_e32 v17, v17, v18
	v_lshlrev_b32_e32 v18, 4, v16
	global_load_dword v1, v1, s[8:9]
	s_nop 0
	global_load_dwordx4 v[22:25], v18, s[18:19]
	global_load_dwordx4 v[26:29], v18, s[20:21]
	global_load_dwordx4 v[30:33], v18, s[18:19] offset:1024
	global_load_dwordx4 v[34:37], v18, s[20:21] offset:1024
	global_load_dwordx4 v[38:41], v18, s[18:19] offset:2048
	global_load_dwordx4 v[42:45], v18, s[20:21] offset:2048
	v_mul_f32_e32 v46, 0x3aaaaaab, v17
	v_pk_add_f32 v[10:11], v[10:11], v[46:47] op_sel_hi:[1,0] neg_lo:[0,1] neg_hi:[0,1]
	v_pk_add_f32 v[2:3], v[2:3], v[46:47] op_sel_hi:[1,0] neg_lo:[0,1] neg_hi:[0,1]
	v_pk_add_f32 v[6:7], v[6:7], v[46:47] op_sel_hi:[1,0] neg_lo:[0,1] neg_hi:[0,1]
	v_mov_b32_e32 v52, v3
	v_mov_b32_e32 v53, v11
	v_pk_add_f32 v[12:13], v[12:13], v[46:47] op_sel_hi:[1,0] neg_lo:[0,1] neg_hi:[0,1]
	v_pk_mul_f32 v[48:49], v[6:7], v[6:7]
	v_pk_add_f32 v[8:9], v[8:9], v[46:47] op_sel_hi:[1,0] neg_lo:[0,1] neg_hi:[0,1]
	v_pk_add_f32 v[4:5], v[4:5], v[46:47] op_sel_hi:[1,0] neg_lo:[0,1] neg_hi:[0,1]
	v_mov_b32_e32 v46, v2
	v_mov_b32_e32 v47, v10
	v_pk_mul_f32 v[52:53], v[52:53], v[52:53]
	v_pk_mul_f32 v[50:51], v[8:9], v[8:9]
	v_pk_fma_f32 v[46:47], v[46:47], v[46:47], v[52:53]
	v_mov_b32_e32 v52, v4
	v_mov_b32_e32 v53, v12
	v_add_f32_e32 v17, v48, v49
	v_mov_b32_e32 v54, v5
	v_mov_b32_e32 v55, v13
	v_pk_fma_f32 v[46:47], v[52:53], v[52:53], v[46:47]
	v_add_f32_e32 v17, v50, v17
	v_pk_fma_f32 v[46:47], v[54:55], v[54:55], v[46:47]
	v_add_f32_e32 v17, v51, v17
	v_add_f32_e32 v17, v47, v17
	v_add_f32_e32 v17, v46, v17
	s_mov_b32 s6, 0xf800000
	s_load_dword s0, s[0:1], 0x48
	v_add_f32_dpp v17, v17, v17 quad_perm:[1,0,3,2] row_mask:0xf bank_mask:0xf bound_ctrl:1
	s_waitcnt lgkmcnt(0)
	s_cmp_lg_u32 s0, 0
	v_add_f32_dpp v17, v17, v17 quad_perm:[2,3,0,1] row_mask:0xf bank_mask:0xf bound_ctrl:1
	s_nop 1
	v_add_f32_dpp v17, v17, v17 row_half_mirror row_mask:0xf bank_mask:0xf bound_ctrl:1
	s_nop 1
	v_add_f32_dpp v17, v17, v17 row_mirror row_mask:0xf bank_mask:0xf bound_ctrl:1
	v_mov_b32_e32 v19, v17
	v_mov_b32_e32 v46, v17
	s_nop 1
	v_permlane16_swap_b32_e32 v19, v46
	v_cndmask_b32_e64 v19, v19, v46, s[4:5]
	v_add_f32_e32 v17, v17, v19
	v_mov_b32_e32 v19, v17
	v_mov_b32_e32 v46, v17
	s_nop 1
	v_permlane32_swap_b32_e32 v19, v46
	v_cndmask_b32_e64 v19, v19, v46, s[2:3]
	v_add_f32_e32 v17, v17, v19
	v_mov_b32_e32 v19, 0x2b8cbccc
	v_fmac_f32_e32 v19, 0x3aaaaaab, v17
	v_mul_f32_e32 v17, 0x4f800000, v19
	v_cmp_gt_f32_e32 vcc, s6, v19
	s_nop 1
	v_cndmask_b32_e32 v17, v19, v17, vcc
	v_sqrt_f32_e32 v19, v17
	s_nop 0
	v_add_u32_e32 v46, -1, v19
	v_fma_f32 v47, -v46, v19, v17
	v_cmp_ge_f32_e64 s[6:7], 0, v47
	v_add_u32_e32 v47, 1, v19
	s_nop 0
	v_cndmask_b32_e64 v46, v19, v46, s[6:7]
	v_fma_f32 v19, -v47, v19, v17
	v_cmp_lt_f32_e64 s[6:7], 0, v19
	s_nop 1
	v_cndmask_b32_e64 v19, v46, v47, s[6:7]
	v_mul_f32_e32 v46, 0x37800000, v19
	v_cndmask_b32_e32 v19, v19, v46, vcc
	v_mov_b32_e32 v46, 0x260
	v_cmp_class_f32_e32 vcc, v17, v46
	s_nop 1
	v_cndmask_b32_e32 v17, v19, v17, vcc
	v_div_scale_f32 v19, s[6:7], v17, v17, 1.0
	v_rcp_f32_e32 v46, v19
	s_nop 0
	v_fma_f32 v47, -v19, v46, 1.0
	v_fmac_f32_e32 v46, v47, v46
	v_div_scale_f32 v47, vcc, 1.0, v17, 1.0
	v_mul_f32_e32 v48, v47, v46
	v_fma_f32 v49, -v19, v48, v47
	v_fmac_f32_e32 v48, v49, v46
	v_fma_f32 v19, -v19, v48, v47
	v_div_fmas_f32 v19, v19, v46, v48
	v_div_fixup_f32 v46, v19, v17, 1.0
	v_pk_mul_f32 v[10:11], v[10:11], v[46:47] op_sel_hi:[1,0]
	v_pk_mul_f32 v[12:13], v[12:13], v[46:47] op_sel_hi:[1,0]
	v_pk_mul_f32 v[6:7], v[6:7], v[46:47] op_sel_hi:[1,0]
	v_pk_mul_f32 v[8:9], v[8:9], v[46:47] op_sel_hi:[1,0]
	v_pk_mul_f32 v[2:3], v[2:3], v[46:47] op_sel_hi:[1,0]
	v_pk_mul_f32 v[4:5], v[4:5], v[46:47] op_sel_hi:[1,0]
	s_waitcnt vmcnt(4)
	v_pk_fma_f32 v[10:11], v[22:23], v[10:11], v[26:27]
	v_pk_fma_f32 v[12:13], v[24:25], v[12:13], v[28:29]
	s_waitcnt vmcnt(2)
	v_pk_fma_f32 v[6:7], v[6:7], v[30:31], v[34:35]
	v_pk_fma_f32 v[8:9], v[8:9], v[32:33], v[36:37]
	s_waitcnt vmcnt(0)
	v_pk_fma_f32 v[2:3], v[2:3], v[38:39], v[42:43]
	v_pk_fma_f32 v[4:5], v[4:5], v[40:41], v[44:45]
	s_cbranch_scc0 .LBB2_10
	v_and_b32_e32 v17, 0x1ff, v14
	v_cmp_eq_u32_e32 vcc, 0, v17
	s_and_saveexec_b64 s[0:1], vcc
	s_cbranch_execz .LBB2_5
	v_lshl_add_u64 v[22:23], s[10:11], 0, v[20:21]
	v_mov_b32_e32 v19, 0
	v_lshl_add_u64 v[22:23], v[22:23], 0, v[18:19]
	global_store_dwordx4 v[22:23], v[10:13], off sc1
	global_store_dwordx4 v[22:23], v[6:9], off offset:1024 sc1
	global_store_dwordx4 v[22:23], v[2:5], off offset:2048 sc1

.LBB2_6:
	s_movk_i32 s0, 0x680
	v_mov_b64_e32 v[22:23], s[12:13]
	v_mov_b32_e32 v19, 0
	v_lshl_add_u64 v[20:21], s[10:11], 0, v[20:21]
	v_mad_i64_i32 v[22:23], s[0:1], v14, s0, v[22:23]
	v_lshlrev_b32_e32 v26, 3, v16
	v_mov_b32_e32 v27, v19
	v_lshl_add_u64 v[20:21], v[20:21], 0, v[18:19]
	v_cvt_pk_f16_f32 v25, v12, v13
	v_cvt_pk_f16_f32 v24, v10, v11
	v_lshl_add_u64 v[22:23], v[22:23], 0, v[26:27]
	global_store_dwordx4 v[20:21], v[10:13], off sc1
	global_store_dwordx2 v[22:23], v[24:25], off sc1
	global_store_dwordx4 v[20:21], v[6:9], off offset:1024 sc1
	v_cvt_pk_f16_f32 v25, v8, v9
	v_cvt_pk_f16_f32 v24, v6, v7
	global_store_dwordx2 v[22:23], v[24:25], off offset:512 sc1
	global_store_dwordx4 v[20:21], v[2:5], off offset:2048 sc1
	v_cvt_pk_f16_f32 v21, v4, v5
	v_cvt_pk_f16_f32 v20, v2, v3
	global_store_dwordx2 v[22:23], v[20:21], off offset:1024 sc1
.LBB2_7:
	ds_read_b128 v[20:23], v18
	ds_read_b128 v[24:27], v18 offset:1024
	ds_read_b128 v[28:31], v18 offset:2048
	v_and_b32_e32 v0, 8, v0
	v_cmp_eq_u32_e32 vcc, 0, v0
	s_waitcnt lgkmcnt(2)
	v_mul_f32_e32 v17, v21, v11
	s_waitcnt lgkmcnt(1)
	v_mul_f32_e32 v19, v25, v7
	v_fmac_f32_e32 v17, v20, v10
	v_fmac_f32_e32 v19, v24, v6
	v_fmac_f32_e32 v17, v22, v12
	v_fmac_f32_e32 v17, v23, v13
	v_fmac_f32_e32 v19, v26, v8
	v_add_f32_e32 v17, 0, v17
	v_fmac_f32_e32 v19, v27, v9
	ds_read_b128 v[20:23], v18 offset:3088
	ds_read_b128 v[24:27], v18 offset:4112
	v_add_f32_e32 v17, v17, v19
	s_waitcnt lgkmcnt(2)
	v_mul_f32_e32 v19, v29, v3
	v_fmac_f32_e32 v19, v28, v2
	v_fmac_f32_e32 v19, v30, v4
	v_fmac_f32_e32 v19, v31, v5
	v_add_f32_e32 v17, v17, v19
	s_waitcnt lgkmcnt(1)
	v_mul_f32_e32 v19, v21, v11
	v_fmac_f32_e32 v19, v20, v10
	v_fmac_f32_e32 v19, v22, v12
	v_fmac_f32_e32 v19, v23, v13
	ds_read_b128 v[20:23], v18 offset:5136
	s_waitcnt lgkmcnt(1)
	v_mul_f32_e32 v25, v25, v7
	v_fmac_f32_e32 v25, v24, v6
	v_fmac_f32_e32 v25, v26, v8
	v_add_f32_e32 v19, 0, v19
	v_fmac_f32_e32 v25, v27, v9
	v_add_f32_e32 v19, v19, v25
	ds_read_b128 v[24:27], v18 offset:6176
	s_waitcnt lgkmcnt(1)
	v_mul_f32_e32 v21, v21, v3
	v_fmac_f32_e32 v21, v20, v2
	v_fmac_f32_e32 v21, v22, v4
	v_fmac_f32_e32 v21, v23, v5
	v_add_f32_e32 v19, v19, v21
	ds_read_b128 v[20:23], v18 offset:7200
	s_waitcnt lgkmcnt(1)
	v_mul_f32_e32 v25, v25, v11
	v_fmac_f32_e32 v25, v24, v10
	v_fmac_f32_e32 v25, v26, v12
	v_fmac_f32_e32 v25, v27, v13
	v_add_f32_e32 v28, 0, v25
	ds_read_b128 v[24:27], v18 offset:8224
	s_waitcnt lgkmcnt(1)
	v_mul_f32_e32 v21, v21, v7
	v_fmac_f32_e32 v21, v20, v6
	v_fmac_f32_e32 v21, v22, v8
	v_fmac_f32_e32 v21, v23, v9
	v_add_f32_e32 v28, v28, v21
	ds_read_b128 v[20:23], v18 offset:9264
	s_waitcnt lgkmcnt(1)
	v_mul_f32_e32 v25, v25, v3
	v_fmac_f32_e32 v25, v24, v2
	v_fmac_f32_e32 v25, v26, v4
	v_fmac_f32_e32 v25, v27, v5
	v_add_f32_e32 v28, v28, v25
	ds_read_b128 v[24:27], v18 offset:10288
	s_waitcnt lgkmcnt(1)
	v_mul_f32_e32 v21, v21, v11
	v_fmac_f32_e32 v21, v20, v10
	v_fmac_f32_e32 v21, v22, v12
	v_fmac_f32_e32 v21, v23, v13
	v_add_f32_e32 v29, 0, v21
	ds_read_b128 v[20:23], v18 offset:11312
	s_waitcnt lgkmcnt(1)
	v_mul_f32_e32 v25, v25, v7
	v_fmac_f32_e32 v25, v24, v6
	v_fmac_f32_e32 v25, v26, v8
	v_fmac_f32_e32 v25, v27, v9
	v_add_f32_e32 v29, v29, v25
	ds_read_b128 v[24:27], v18 offset:12352
	s_waitcnt lgkmcnt(1)
	v_mul_f32_e32 v21, v21, v3
	v_fmac_f32_e32 v21, v20, v2
	v_fmac_f32_e32 v21, v22, v4
	v_fmac_f32_e32 v21, v23, v5
	v_add_f32_e32 v29, v29, v21
	ds_read_b128 v[20:23], v18 offset:13376
	s_waitcnt lgkmcnt(1)
	v_mul_f32_e32 v25, v25, v11
	v_fmac_f32_e32 v25, v24, v10
	v_fmac_f32_e32 v25, v26, v12
	v_fmac_f32_e32 v25, v27, v13
	v_add_f32_e32 v30, 0, v25
	ds_read_b128 v[24:27], v18 offset:14400
	s_waitcnt lgkmcnt(1)
	v_mul_f32_e32 v21, v21, v7
	v_fmac_f32_e32 v21, v20, v6
	v_fmac_f32_e32 v21, v22, v8
	v_fmac_f32_e32 v21, v23, v9
	v_add_f32_e32 v30, v30, v21
	ds_read_b128 v[20:23], v18 offset:15440
	s_waitcnt lgkmcnt(1)
	v_mul_f32_e32 v25, v25, v3
	v_fmac_f32_e32 v25, v24, v2
	v_fmac_f32_e32 v25, v26, v4
	v_fmac_f32_e32 v25, v27, v5
	v_add_f32_e32 v30, v30, v25
	ds_read_b128 v[24:27], v18 offset:16464
	s_waitcnt lgkmcnt(1)
	v_mul_f32_e32 v21, v21, v11
	v_fmac_f32_e32 v21, v20, v10
	v_fmac_f32_e32 v21, v22, v12
	v_fmac_f32_e32 v21, v23, v13
	v_add_f32_e32 v31, 0, v21
	ds_read_b128 v[20:23], v18 offset:17488
	s_waitcnt lgkmcnt(1)
	v_mul_f32_e32 v25, v25, v7
	v_fmac_f32_e32 v25, v24, v6
	v_fmac_f32_e32 v25, v26, v8
	v_fmac_f32_e32 v25, v27, v9
	v_add_f32_e32 v31, v31, v25
	ds_read_b128 v[24:27], v18 offset:18528
	s_waitcnt lgkmcnt(1)
	v_mul_f32_e32 v21, v21, v3
	v_fmac_f32_e32 v21, v20, v2
	v_fmac_f32_e32 v21, v22, v4
	v_fmac_f32_e32 v21, v23, v5
	v_add_f32_e32 v31, v31, v21
	ds_read_b128 v[20:23], v18 offset:19552
	s_waitcnt lgkmcnt(1)
	v_mul_f32_e32 v25, v25, v11
	v_fmac_f32_e32 v25, v24, v10
	v_fmac_f32_e32 v25, v26, v12
	v_fmac_f32_e32 v25, v27, v13
	v_add_f32_e32 v32, 0, v25
	ds_read_b128 v[24:27], v18 offset:20576
	s_waitcnt lgkmcnt(1)
	v_mul_f32_e32 v21, v21, v7
	v_fmac_f32_e32 v21, v20, v6
	v_fmac_f32_e32 v21, v22, v8
	v_fmac_f32_e32 v21, v23, v9
	v_add_f32_e32 v32, v32, v21
	ds_read_b128 v[20:23], v18 offset:21616
	s_waitcnt lgkmcnt(1)
	v_mul_f32_e32 v25, v25, v3
	v_fmac_f32_e32 v25, v24, v2
	v_fmac_f32_e32 v25, v26, v4
	v_fmac_f32_e32 v25, v27, v5
	v_add_f32_e32 v32, v32, v25
	ds_read_b128 v[24:27], v18 offset:22640
	s_waitcnt lgkmcnt(1)
	v_mul_f32_e32 v11, v21, v11
	v_fmac_f32_e32 v11, v20, v10
	v_fmac_f32_e32 v11, v22, v12
	v_fmac_f32_e32 v11, v23, v13
	v_add_f32_e32 v20, 0, v11
	ds_read_b128 v[10:13], v18 offset:23664
	s_waitcnt lgkmcnt(1)
	v_mul_f32_e32 v7, v25, v7
	v_fmac_f32_e32 v7, v24, v6
	v_fmac_f32_e32 v7, v26, v8
	v_fmac_f32_e32 v7, v27, v9
	s_waitcnt lgkmcnt(0)
	v_mul_f32_e32 v3, v11, v3
	v_fmac_f32_e32 v3, v10, v2
	v_fmac_f32_e32 v3, v12, v4
	v_add_f32_e32 v6, v20, v7
	v_fmac_f32_e32 v3, v13, v5
	v_add_f32_e32 v2, v6, v3
	v_cndmask_b32_e64 v3, v17, v30, s[2:3]
	v_mov_b32_e32 v5, v3
	s_nop 1
	v_permlane32_swap_b32_e32 v3, v5
	v_cndmask_b32_e64 v4, v30, v17, s[2:3]
	v_cndmask_b32_e64 v3, v3, v5, s[2:3]
	v_add_f32_e32 v3, v4, v3
	v_cndmask_b32_e64 v4, v19, v31, s[2:3]
	v_mov_b32_e32 v6, v4
	s_nop 1
	v_permlane32_swap_b32_e32 v4, v6
	v_cndmask_b32_e64 v5, v31, v19, s[2:3]
	v_cndmask_b32_e64 v4, v4, v6, s[2:3]
	v_add_f32_e32 v4, v5, v4
	v_cndmask_b32_e64 v5, v28, v32, s[2:3]
	v_mov_b32_e32 v7, v5
	s_nop 1
	v_permlane32_swap_b32_e32 v5, v7
	v_cndmask_b32_e64 v6, v32, v28, s[2:3]
	v_cndmask_b32_e64 v5, v5, v7, s[2:3]
	v_add_f32_e32 v5, v6, v5
	v_cndmask_b32_e64 v6, v29, v2, s[2:3]
	v_mov_b32_e32 v7, v6
	s_nop 1
	v_permlane32_swap_b32_e32 v6, v7
	v_cndmask_b32_e64 v2, v2, v29, s[2:3]
	v_cndmask_b32_e64 v6, v6, v7, s[2:3]
	v_add_f32_e32 v2, v2, v6
	v_cndmask_b32_e64 v6, v3, v5, s[4:5]
	v_cndmask_b32_e64 v3, v5, v3, s[4:5]
	v_mov_b32_e32 v5, v6
	s_nop 1
	v_permlane16_swap_b32_e32 v6, v5
	v_cndmask_b32_e64 v5, v6, v5, s[4:5]
	v_add_f32_e32 v3, v3, v5
	v_cndmask_b32_e64 v5, v4, v2, s[4:5]
	v_cndmask_b32_e64 v2, v2, v4, s[4:5]
	v_mov_b32_e32 v4, v5
	s_nop 1
	v_permlane16_swap_b32_e32 v5, v4
	v_cndmask_b32_e64 v4, v5, v4, s[4:5]
	v_add_f32_e32 v2, v2, v4
	v_cndmask_b32_e32 v0, v3, v2, vcc
	v_cndmask_b32_e32 v2, v2, v3, vcc
	v_cmp_eq_u32_e32 vcc, 0, v16
	s_nop 0
	v_add_f32_dpp v0, v0, v2 row_ror:8 row_mask:0xf bank_mask:0xf bound_ctrl:1
	s_nop 1
	v_add_f32_dpp v0, v0, v0 quad_perm:[1,0,3,2] row_mask:0xf bank_mask:0xf bound_ctrl:1
	s_nop 1
	v_add_f32_dpp v0, v0, v0 quad_perm:[2,3,0,1] row_mask:0xf bank_mask:0xf bound_ctrl:1
	s_nop 1
	v_add_f32_dpp v0, v0, v0 row_half_mirror row_mask:0xf bank_mask:0xf bound_ctrl:1
	v_add_f32_e32 v0, v1, v0
	s_nop 0
	v_readlane_b32 s12, v0, 0
	v_readlane_b32 s24, v0, 8
	v_readlane_b32 s23, v0, 16
	v_readlane_b32 s22, v0, 24
	v_readlane_b32 s21, v0, 32
	v_readlane_b32 s20, v0, 40
	v_readlane_b32 s19, v0, 48
	v_readlane_b32 s18, v0, 56
	s_and_saveexec_b64 s[0:1], vcc
	s_cbranch_execz .LBB2_9
	v_mov_b32_e32 v0, s12
	v_mov_b32_e32 v1, s24
	v_cmp_gt_f32_e32 vcc, s24, v0
	s_mov_b32 s25, 0x3fb8aa3b
	s_mov_b32 s26, 0xc2ce8ed0
	v_cndmask_b32_e32 v0, v0, v1, vcc
	v_mov_b32_e32 v1, s23
	v_cmp_gt_f32_e64 s[0:1], s23, v0
	s_mov_b32 s27, 0x42b17218
	s_nop 0
	v_cndmask_b32_e64 v0, v0, v1, s[0:1]
	v_mov_b32_e32 v1, s22
	v_cmp_gt_f32_e64 s[2:3], s22, v0
	s_and_b64 s[0:1], s[0:1], exec
	s_nop 0
	v_cndmask_b32_e64 v0, v0, v1, s[2:3]
	v_mov_b32_e32 v1, s21
	v_cmp_gt_f32_e64 s[4:5], s21, v0
	s_nop 1
	v_cndmask_b32_e64 v0, v0, v1, s[4:5]
	v_mov_b32_e32 v1, s20
	v_cmp_gt_f32_e64 s[6:7], s20, v0
	s_nop 1
	v_cndmask_b32_e64 v0, v0, v1, s[6:7]
	v_mov_b32_e32 v1, s19
	v_cmp_gt_f32_e64 s[8:9], s19, v0
	s_nop 1
	v_cndmask_b32_e64 v0, v0, v1, s[8:9]
	v_mov_b32_e32 v1, s18
	v_cmp_gt_f32_e64 s[10:11], s18, v0
	s_nop 1
	v_cndmask_b32_e64 v0, v0, v1, s[10:11]
	v_sub_f32_e32 v1, s12, v0
	v_mul_f32_e32 v2, 0x3fb8aa3b, v1
	v_fma_f32 v3, v1, s25, -v2
	v_rndne_f32_e32 v4, v2
	v_fmac_f32_e32 v3, 0x32a5705f, v1
	v_sub_f32_e32 v2, v2, v4
	v_add_f32_e32 v2, v2, v3
	v_exp_f32_e32 v2, v2
	v_cvt_i32_f32_e32 v3, v4
	v_cmp_ngt_f32_e64 s[12:13], s26, v1
	v_ldexp_f32 v2, v2, v3
	v_sub_f32_e32 v3, s24, v0
	v_mul_f32_e32 v4, 0x3fb8aa3b, v3
	v_fma_f32 v5, v3, s25, -v4
	v_rndne_f32_e32 v6, v4
	v_fmac_f32_e32 v5, 0x32a5705f, v3
	v_sub_f32_e32 v4, v4, v6
	v_add_f32_e32 v4, v4, v5
	v_exp_f32_e32 v4, v4
	v_cvt_i32_f32_e32 v5, v6
	v_cndmask_b32_e64 v2, 0, v2, s[12:13]
	v_mov_b32_e32 v6, 0x7f800000
	v_cmp_nlt_f32_e64 s[12:13], s27, v1
	s_nop 1
	v_cndmask_b32_e64 v1, v6, v2, s[12:13]
	v_ldexp_f32 v2, v4, v5
	v_sub_f32_e32 v4, s23, v0
	v_mul_f32_e32 v5, 0x3fb8aa3b, v4
	v_fma_f32 v7, v4, s25, -v5
	v_rndne_f32_e32 v8, v5
	v_fmac_f32_e32 v7, 0x32a5705f, v4
	v_sub_f32_e32 v5, v5, v8
	v_add_f32_e32 v5, v5, v7
	v_exp_f32_e32 v5, v5
	v_cvt_i32_f32_e32 v7, v8
	v_cmp_ngt_f32_e64 s[12:13], s26, v3
	s_nop 1
	v_cndmask_b32_e64 v2, 0, v2, s[12:13]
	v_cmp_nlt_f32_e64 s[12:13], s27, v3
	v_sub_f32_e32 v3, s22, v0
	s_nop 0
	v_cndmask_b32_e64 v2, v6, v2, s[12:13]
	v_add_f32_e32 v1, v1, v2
	v_ldexp_f32 v2, v5, v7
	v_mul_f32_e32 v5, 0x3fb8aa3b, v3
	v_fma_f32 v7, v3, s25, -v5
	v_rndne_f32_e32 v8, v5
	v_fmac_f32_e32 v7, 0x32a5705f, v3
	v_sub_f32_e32 v5, v5, v8
	v_add_f32_e32 v5, v5, v7
	v_exp_f32_e32 v5, v5
	v_cvt_i32_f32_e32 v7, v8
	v_cmp_ngt_f32_e64 s[12:13], s26, v4
	s_nop 1
	v_cndmask_b32_e64 v2, 0, v2, s[12:13]
	v_cmp_nlt_f32_e64 s[12:13], s27, v4
	v_sub_f32_e32 v4, s21, v0
	s_nop 0
	v_cndmask_b32_e64 v2, v6, v2, s[12:13]
	v_add_f32_e32 v1, v1, v2
	v_ldexp_f32 v2, v5, v7
	v_mul_f32_e32 v5, 0x3fb8aa3b, v4
	v_fma_f32 v7, v4, s25, -v5
	v_rndne_f32_e32 v8, v5
	v_fmac_f32_e32 v7, 0x32a5705f, v4
	v_sub_f32_e32 v5, v5, v8
	v_add_f32_e32 v5, v5, v7
	v_exp_f32_e32 v5, v5
	v_cvt_i32_f32_e32 v7, v8
	v_cmp_ngt_f32_e64 s[12:13], s26, v3
	s_nop 1
	v_cndmask_b32_e64 v2, 0, v2, s[12:13]
	v_cmp_nlt_f32_e64 s[12:13], s27, v3
	v_sub_f32_e32 v3, s20, v0
	s_nop 0
	v_cndmask_b32_e64 v2, v6, v2, s[12:13]
	v_add_f32_e32 v1, v1, v2
	v_ldexp_f32 v2, v5, v7
	v_mul_f32_e32 v5, 0x3fb8aa3b, v3
	v_fma_f32 v7, v3, s25, -v5
	v_rndne_f32_e32 v8, v5
	v_fmac_f32_e32 v7, 0x32a5705f, v3
	v_sub_f32_e32 v5, v5, v8
	v_add_f32_e32 v5, v5, v7
	v_exp_f32_e32 v5, v5
	v_cvt_i32_f32_e32 v7, v8
	v_cmp_ngt_f32_e64 s[12:13], s26, v4
	s_nop 1
	v_cndmask_b32_e64 v2, 0, v2, s[12:13]
	v_cmp_nlt_f32_e64 s[12:13], s27, v4
	v_sub_f32_e32 v4, s19, v0
	v_sub_f32_e32 v0, s18, v0
	v_cndmask_b32_e64 v2, v6, v2, s[12:13]
	v_add_f32_e32 v1, v1, v2
	v_ldexp_f32 v2, v5, v7
	v_mul_f32_e32 v5, 0x3fb8aa3b, v4
	v_fma_f32 v7, v4, s25, -v5
	v_rndne_f32_e32 v8, v5
	v_fmac_f32_e32 v7, 0x32a5705f, v4
	v_sub_f32_e32 v5, v5, v8
	v_add_f32_e32 v5, v5, v7
	v_exp_f32_e32 v5, v5
	v_cvt_i32_f32_e32 v7, v8
	v_cmp_ngt_f32_e64 s[12:13], s26, v3
	s_nop 1
	v_cndmask_b32_e64 v2, 0, v2, s[12:13]
	v_cmp_nlt_f32_e64 s[12:13], s27, v3
	v_mul_f32_e32 v3, 0x3fb8aa3b, v0
	s_nop 0
	v_cndmask_b32_e64 v2, v6, v2, s[12:13]
	v_add_f32_e32 v1, v1, v2
	v_ldexp_f32 v2, v5, v7
	v_fma_f32 v5, v0, s25, -v3
	v_rndne_f32_e32 v7, v3
	v_fmac_f32_e32 v5, 0x32a5705f, v0
	v_sub_f32_e32 v3, v3, v7
	v_add_f32_e32 v3, v3, v5
	v_exp_f32_e32 v3, v3
	v_cvt_i32_f32_e32 v5, v7
	v_cmp_ngt_f32_e64 s[12:13], s26, v4
	s_nop 1
	v_cndmask_b32_e64 v2, 0, v2, s[12:13]
	v_cmp_nlt_f32_e64 s[12:13], s27, v4
	s_nop 1
	v_cndmask_b32_e64 v2, v6, v2, s[12:13]
	v_add_f32_e32 v1, v1, v2
	v_ldexp_f32 v2, v3, v5
	v_cmp_ngt_f32_e64 s[12:13], s26, v0
	s_nop 1
	v_cndmask_b32_e64 v2, 0, v2, s[12:13]
	v_cmp_nlt_f32_e64 s[12:13], s27, v0
	s_nop 1
	v_cndmask_b32_e64 v0, v6, v2, s[12:13]
	v_add_f32_e32 v4, v1, v0
	v_cndmask_b32_e64 v0, 0, 1, vcc
	s_nop 0
	v_readfirstlane_b32 s0, v0
	s_cselect_b32 s12, 2, s0
	s_and_b64 s[0:1], s[2:3], exec
	s_cselect_b32 s2, 3, s12
	s_and_b64 s[0:1], s[4:5], exec
	s_cselect_b32 s2, 4, s2
	s_and_b64 s[0:1], s[6:7], exec
	v_div_scale_f32 v5, s[0:1], v4, v4, 1.0
	s_cselect_b32 s2, 5, s2
	s_and_b64 s[0:1], s[8:9], exec
	v_rcp_f32_e32 v6, v5
	s_cselect_b32 s2, 6, s2
	s_and_b64 s[0:1], s[10:11], exec
	s_cselect_b32 s2, 7, s2
	v_lshlrev_b64 v[0:1], 2, v[14:15]
	v_lshl_add_u64 v[2:3], s[14:15], 0, v[0:1]
	v_mov_b32_e32 v7, s2
	global_store_dword v[2:3], v7, off sc1
	v_fma_f32 v2, -v5, v6, 1.0
	v_fmac_f32_e32 v6, v2, v6
	v_div_scale_f32 v2, vcc, 1.0, v4, 1.0
	v_mul_f32_e32 v3, v2, v6
	v_fma_f32 v7, -v5, v3, v2
	v_fmac_f32_e32 v3, v7, v6
	v_fma_f32 v2, -v5, v3, v2
	v_div_fmas_f32 v2, v2, v6, v3
	v_div_fixup_f32 v2, v2, v4, 1.0
	v_lshl_add_u64 v[0:1], s[16:17], 0, v[0:1]
	global_store_dword v[0:1], v2, off sc1

.LBB4_7:
	s_lshr_b32 s5, s3, 6
	v_cvt_f32_i32_e32 v1, s5
	s_sext_i32_i16 s6, s9
	v_cvt_f32_i32_e32 v2, s6
	s_ashr_i32 s6, s6, 30
	v_rcp_iflag_f32_e32 v3, v1
	s_or_b32 s10, s6, 1
	v_mov_b32_e32 v19, 0
	v_lshrrev_b32_e32 v20, 3, v0
	v_mul_f32_e32 v3, v2, v3
	v_trunc_f32_e32 v3, v3
	v_fma_f32 v2, -v3, v1, v2
	v_cvt_i32_f32_e32 v3, v3
	v_cmp_ge_f32_e64 s[6:7], |v2|, v1
	s_and_b64 s[6:7], s[6:7], exec
	s_cselect_b32 s6, s10, 0
	v_readfirstlane_b32 s7, v3
	s_add_i32 s6, s7, s6
	s_mul_i32 s5, s6, s5
	s_sub_i32 s5, s9, s5
	s_sext_i32_i16 s7, s6
	s_sext_i32_i16 s5, s5
	s_ashr_i32 s9, s8, 31
	s_lshl_b32 s6, s7, 6
	s_lshl_b32 s10, s5, 6
	s_lshl_b64 s[8:9], s[8:9], 3
	s_add_u32 s12, s0, s8
	s_addc_u32 s13, s1, s9
	s_load_dwordx2 s[14:15], s[12:13], 0x0
	s_load_dwordx2 s[8:9], s[12:13], 0x88
	s_ashr_i32 s11, s10, 31
	s_lshl_b64 s[12:13], s[10:11], 2
	v_lshrrev_b32_e32 v1, 4, v0
	s_waitcnt lgkmcnt(0)
	s_add_u32 s12, s14, s12
	v_lshlrev_b32_e32 v2, 4, v0
	s_addc_u32 s13, s15, s13
	v_and_b32_e32 v18, 0xf0, v2
	v_or_b32_e32 v16, s6, v1
	v_lshl_add_u64 v[14:15], s[12:13], 0, v[18:19]
	v_mul_hi_i32_i24_e32 v3, s3, v16
	v_mul_i32_i24_e32 v2, s3, v16
	v_lshl_add_u64 v[10:11], v[2:3], 2, v[14:15]
	v_or_b32_e32 v2, 16, v16
	v_mul_hi_i32_i24_e32 v3, s3, v2
	v_mul_i32_i24_e32 v2, s3, v2
	v_lshl_add_u64 v[12:13], v[2:3], 2, v[14:15]
	global_load_dwordx4 v[2:5], v[10:11], off
	global_load_dwordx4 v[6:9], v[12:13], off
	v_or_b32_e32 v10, 32, v16
	v_mul_hi_i32_i24_e32 v11, s3, v10
	v_mul_i32_i24_e32 v10, s3, v10
	v_lshl_add_u64 v[10:11], v[10:11], 2, v[14:15]
	v_or_b32_e32 v16, 48, v16
	global_load_dwordx4 v[10:13], v[10:11], off
	v_mul_hi_i32_i24_e32 v17, s3, v16
	v_mul_i32_i24_e32 v16, s3, v16
	v_lshl_add_u64 v[14:15], v[16:17], 2, v[14:15]
	global_load_dwordx4 v[14:17], v[14:15], off
	s_movk_i32 s3, 0x104
	v_and_b32_e32 v24, 7, v0
	s_movk_i32 s5, 0x820
	v_lshlrev_b32_e32 v21, 2, v20
	v_mad_u32_u24 v1, v1, s3, v18
	v_or_b32_e32 v18, s10, v20
	v_mad_u32_u24 v26, v24, s5, v21
	v_add_u32_e32 v25, 0x1040, v1
	v_add_u32_e32 v27, 0x1048, v1
	v_mul_hi_i32_i24_e32 v21, s4, v18
	v_mul_i32_i24_e32 v20, s4, v18
	v_or_b32_e32 v18, 32, v18
	v_add_u32_e32 v28, 0x2080, v1
	v_add_u32_e32 v29, 0x2088, v1
	v_add_u32_e32 v30, 0x30c0, v1
	v_add_u32_e32 v31, 0x30c8, v1
	v_add_u32_e32 v32, 0x400, v26
	v_mul_hi_i32_i24_e32 v23, s4, v18
	v_mul_i32_i24_e32 v22, s4, v18
	s_ashr_i32 s7, s6, 31
	v_lshlrev_b32_e32 v18, 4, v24
	s_lshl_b64 s[4:5], s[6:7], 1
	s_add_u32 s4, s8, s4
	s_addc_u32 s5, s9, s5
	v_lshl_add_u64 v[18:19], s[4:5], 0, v[18:19]
	v_lshl_add_u64 v[20:21], v[20:21], 1, v[18:19]
	s_mov_b64 s[4:5], 0
	v_lshl_add_u64 v[18:19], v[22:23], 1, v[18:19]
	s_waitcnt vmcnt(3)
	ds_write2_b32 v1, v2, v3 offset1:1
	ds_write2_b32 v1, v4, v5 offset0:2 offset1:3
	s_waitcnt vmcnt(2)
	ds_write2_b32 v25, v6, v7 offset1:1
	ds_write2_b32 v27, v8, v9 offset1:1
	s_waitcnt vmcnt(1)
	ds_write2_b32 v28, v10, v11 offset1:1
	ds_write2_b32 v29, v12, v13 offset1:1
	s_waitcnt vmcnt(0)
	ds_write2_b32 v30, v14, v15 offset1:1
	ds_write2_b32 v31, v16, v17 offset1:1
	s_waitcnt lgkmcnt(0)
	s_barrier
	ds_read2_b32 v[10:11], v26 offset1:32
	ds_read2_b32 v[6:7], v26 offset0:130 offset1:162
	ds_read2_b32 v[12:13], v32 offset0:4 offset1:36
	ds_read2_b32 v[8:9], v32 offset0:134 offset1:166
	ds_read2_b32 v[14:15], v32 offset0:199 offset1:231
	ds_read2_b32 v[16:17], v32 offset0:69 offset1:101
	ds_read2_b32 v[24:25], v26 offset0:195 offset1:227
	ds_read2_b32 v[26:27], v26 offset0:65 offset1:97
	s_waitcnt lgkmcnt(3)
	v_cvt_pk_f16_f32 v5, v8, v14
	s_waitcnt lgkmcnt(2)
	v_cvt_pk_f16_f32 v4, v12, v16
	s_waitcnt lgkmcnt(1)
	v_cvt_pk_f16_f32 v3, v6, v24
	s_waitcnt lgkmcnt(0)
	v_cvt_pk_f16_f32 v2, v10, v26
	v_cvt_pk_f16_f32 v9, v9, v15
	v_cvt_pk_f16_f32 v8, v13, v17
	v_cvt_pk_f16_f32 v7, v7, v25
	v_cvt_pk_f16_f32 v6, v11, v27
	global_store_dwordx4 v[20:21], v[2:5], off sc1
	global_store_dwordx4 v[18:19], v[6:9], off sc1
.LBB4_8:
	s_and_b64 vcc, exec, s[4:5]
	s_cbranch_vccz .LBB4_11
	s_load_dwordx2 s[4:5], s[0:1], 0x110
	s_lshl_b32 s2, s2, 2
	v_lshrrev_b32_e32 v1, 6, v0
	v_mov_b32_e32 v11, 0
	v_or_b32_e32 v10, s2, v1
	s_waitcnt lgkmcnt(0)
	v_lshl_add_u64 v[2:3], v[10:11], 2, s[4:5]
	global_load_dword v6, v[2:3], off
	s_load_dwordx8 s[4:11], s[0:1], 0x120
	v_mov_b32_e32 v2, 0x1ff
	v_bitop3_b32 v1, s2, v2, v1 bitop3:0xc8
	v_mul_u32_u24_e32 v1, 0x300, v1
	v_and_b32_e32 v62, 63, v0
	v_mov_b32_e32 v3, v11
	v_lshlrev_b32_e32 v2, 2, v1
	s_movk_i32 s12, 0xc00
	v_lshlrev_b32_e32 v12, 4, v62
	v_mov_b32_e32 v13, v11
	s_waitcnt lgkmcnt(0)
	v_mov_b64_e32 v[4:5], s[4:5]
	v_lshl_add_u64 v[2:3], s[6:7], 0, v[2:3]
	v_lshl_add_u64 v[50:51], v[2:3], 0, v[12:13]
	v_and_b32_e32 v63, 16, v0
	v_cmp_eq_u32_e32 vcc, 0, v63
	v_and_b32_e32 v64, 32, v0
	v_mov_b32_e32 v65, 0x2b8cbccc
	v_mov_b32_e32 v66, 0x260
	v_lshlrev_b32_e32 v0, 3, v62
	v_mov_b32_e32 v1, v11
	s_waitcnt vmcnt(0)
	v_mad_i64_i32 v[2:3], s[2:3], v6, s12, v[4:5]
	v_lshl_add_u64 v[52:53], v[2:3], 0, v[12:13]
	global_load_dwordx4 v[14:17], v[52:53], off
	global_load_dwordx4 v[18:21], v[50:51], off
	global_load_dwordx4 v[22:25], v[50:51], off offset:1024
	global_load_dwordx4 v[26:29], v[52:53], off offset:1024
	global_load_dwordx4 v[30:33], v[50:51], off offset:2048
	global_load_dwordx4 v[34:37], v[52:53], off offset:2048
	global_load_dwordx4 v[38:41], v12, s[8:9]
	global_load_dwordx4 v[42:45], v12, s[8:9] offset:1024
	global_load_dwordx4 v[46:49], v12, s[8:9] offset:2048
	global_load_dwordx4 v[6:9], v12, s[10:11]
	global_load_dwordx4 v[2:5], v12, s[10:11] offset:1024
	s_load_dwordx2 s[2:3], s[0:1], 0x150
	s_load_dwordx4 s[4:7], s[0:1], 0x140
	s_mov_b32 s9, 0xf800000
	s_movk_i32 s8, 0x680
	s_waitcnt lgkmcnt(0)
	v_mov_b64_e32 v[56:57], s[2:3]
	v_mov_b64_e32 v[50:51], s[6:7]
	s_waitcnt vmcnt(9)
	v_pk_add_f32 v[52:53], v[14:15], v[18:19]
	v_pk_add_f32 v[54:55], v[16:17], v[20:21]
	s_waitcnt vmcnt(7)
	v_pk_add_f32 v[58:59], v[26:27], v[22:23]
	v_pk_add_f32 v[60:61], v[28:29], v[24:25]
	global_load_dwordx4 v[14:17], v12, s[4:5]
	global_load_dwordx4 v[18:21], v12, s[4:5] offset:1024
	global_load_dwordx4 v[22:25], v12, s[4:5] offset:2048
	global_load_dwordx4 v[26:29], v12, s[10:11] offset:2048
	s_waitcnt vmcnt(9)
	v_pk_add_f32 v[30:31], v[34:35], v[30:31]
	v_pk_add_f32 v[32:33], v[36:37], v[32:33]
	s_waitcnt vmcnt(8)
	v_pk_add_f32 v[34:35], v[52:53], v[38:39]
	v_pk_add_f32 v[36:37], v[54:55], v[40:41]
	s_waitcnt vmcnt(7)
	v_pk_add_f32 v[40:41], v[58:59], v[42:43]
	s_waitcnt vmcnt(6)
	v_pk_add_f32 v[30:31], v[30:31], v[46:47]
	v_pk_add_f32 v[42:43], v[60:61], v[44:45]
	v_pk_add_f32 v[32:33], v[32:33], v[48:49]
	v_add_f32_e32 v52, v34, v35
	v_mov_b32_e32 v44, v40
	v_mov_b32_e32 v45, v30
	v_mov_b32_e32 v46, v41
	v_mov_b32_e32 v47, v31
	v_mov_b32_e32 v48, v42
	v_mov_b32_e32 v49, v32
	v_add_f32_e32 v52, v52, v36
	v_pk_add_f32 v[44:45], v[44:45], v[46:47]
	v_mad_u64_u32 v[38:39], s[2:3], v10, s12, v[50:51]
	v_mov_b32_e32 v50, v43
	v_mov_b32_e32 v51, v33
	v_add_f32_e32 v46, v52, v37
	v_pk_add_f32 v[44:45], v[44:45], v[48:49]
	v_add_f32_e32 v46, 0, v46
	v_pk_add_f32 v[44:45], v[44:45], v[50:51]
	v_cmp_eq_u32_e64 s[2:3], 0, v64
	v_add_f32_e32 v44, v46, v44
	v_add_f32_e32 v44, v44, v45
	v_lshl_add_u64 v[38:39], v[38:39], 0, v[12:13]
	s_nop 0
	v_add_f32_dpp v44, v44, v44 quad_perm:[1,0,3,2] row_mask:0xf bank_mask:0xf bound_ctrl:1
	s_nop 1
	v_add_f32_dpp v44, v44, v44 quad_perm:[2,3,0,1] row_mask:0xf bank_mask:0xf bound_ctrl:1
	s_nop 1
	v_add_f32_dpp v44, v44, v44 row_half_mirror row_mask:0xf bank_mask:0xf bound_ctrl:1
	s_nop 1
	v_add_f32_dpp v44, v44, v44 row_mirror row_mask:0xf bank_mask:0xf bound_ctrl:1
	v_mov_b32_e32 v45, v44
	v_mov_b32_e32 v46, v44
	s_nop 1
	v_permlane16_swap_b32_e32 v45, v46
	v_cndmask_b32_e32 v45, v45, v46, vcc
	v_add_f32_e32 v44, v44, v45
	v_mov_b32_e32 v45, v44
	v_mov_b32_e32 v46, v44
	s_nop 1
	v_permlane32_swap_b32_e32 v45, v46
	v_cndmask_b32_e64 v45, v45, v46, s[2:3]
	v_add_f32_e32 v44, v44, v45
	v_mul_f32_e32 v44, 0x3aaaaaab, v44
	v_pk_add_f32 v[34:35], v[34:35], v[44:45] op_sel_hi:[1,0] neg_lo:[0,1] neg_hi:[0,1]
	v_pk_add_f32 v[30:31], v[30:31], v[44:45] op_sel_hi:[1,0] neg_lo:[0,1] neg_hi:[0,1]
	v_pk_add_f32 v[40:41], v[40:41], v[44:45] op_sel_hi:[1,0] neg_lo:[0,1] neg_hi:[0,1]
	v_mov_b32_e32 v50, v31
	v_mov_b32_e32 v51, v35
	v_pk_add_f32 v[36:37], v[36:37], v[44:45] op_sel_hi:[1,0] neg_lo:[0,1] neg_hi:[0,1]
	v_pk_add_f32 v[42:43], v[42:43], v[44:45] op_sel_hi:[1,0] neg_lo:[0,1] neg_hi:[0,1]
	v_pk_add_f32 v[32:33], v[32:33], v[44:45] op_sel_hi:[1,0] neg_lo:[0,1] neg_hi:[0,1]
	v_pk_mul_f32 v[44:45], v[40:41], v[40:41]
	v_mov_b32_e32 v48, v30
	v_mov_b32_e32 v49, v34
	v_pk_mul_f32 v[50:51], v[50:51], v[50:51]
	v_pk_mul_f32 v[46:47], v[42:43], v[42:43]
	v_mov_b32_e32 v52, v32
	v_mov_b32_e32 v53, v36
	v_add_f32_e32 v54, v44, v45
	v_pk_fma_f32 v[48:49], v[48:49], v[48:49], v[50:51]
	v_mov_b32_e32 v44, v33
	v_mov_b32_e32 v45, v37
	v_add_f32_e32 v46, v46, v54
	v_pk_fma_f32 v[48:49], v[52:53], v[52:53], v[48:49]
	v_add_f32_e32 v46, v47, v46
	v_pk_fma_f32 v[44:45], v[44:45], v[44:45], v[48:49]
	s_nop 0
	v_add_f32_e32 v45, v45, v46
	v_add_f32_e32 v44, v44, v45
	s_nop 1
	v_add_f32_dpp v44, v44, v44 quad_perm:[1,0,3,2] row_mask:0xf bank_mask:0xf bound_ctrl:1
	s_nop 1
	v_add_f32_dpp v44, v44, v44 quad_perm:[2,3,0,1] row_mask:0xf bank_mask:0xf bound_ctrl:1
	s_nop 1
	v_add_f32_dpp v44, v44, v44 row_half_mirror row_mask:0xf bank_mask:0xf bound_ctrl:1
	s_nop 1
	v_add_f32_dpp v44, v44, v44 row_mirror row_mask:0xf bank_mask:0xf bound_ctrl:1
	v_mov_b32_e32 v45, v44
	v_mov_b32_e32 v46, v44
	s_nop 1
	v_permlane16_swap_b32_e32 v45, v46
	v_cndmask_b32_e32 v45, v45, v46, vcc
	v_add_f32_e32 v44, v44, v45
	v_mov_b32_e32 v45, v44
	v_mov_b32_e32 v46, v44
	s_nop 1
	v_permlane32_swap_b32_e32 v45, v46
	v_cndmask_b32_e64 v45, v45, v46, s[2:3]
	v_add_f32_e32 v44, v44, v45
	v_fmac_f32_e32 v65, 0x3aaaaaab, v44
	v_mul_f32_e32 v44, 0x4f800000, v65
	v_cmp_gt_f32_e32 vcc, s9, v65
	s_nop 1
	v_cndmask_b32_e32 v46, v65, v44, vcc
	v_sqrt_f32_e32 v47, v46
	v_mad_u64_u32 v[44:45], s[2:3], v10, s8, v[56:57]
	v_lshl_add_u64 v[44:45], v[44:45], 0, v[0:1]
	v_add_u32_e32 v12, -1, v47
	v_add_u32_e32 v13, 1, v47
	v_fma_f32 v48, -v12, v47, v46
	v_fma_f32 v49, -v13, v47, v46
	v_cmp_ge_f32_e64 s[2:3], 0, v48
	s_nop 1
	v_cndmask_b32_e64 v12, v47, v12, s[2:3]
	v_cmp_lt_f32_e64 s[2:3], 0, v49
	s_nop 1
	v_cndmask_b32_e64 v12, v12, v13, s[2:3]
	v_mul_f32_e32 v13, 0x37800000, v12
	v_cndmask_b32_e32 v12, v12, v13, vcc
	v_cmp_class_f32_e32 vcc, v46, v66
	s_nop 1
	v_cndmask_b32_e32 v12, v12, v46, vcc
	v_div_scale_f32 v13, s[2:3], v12, v12, 1.0
	v_rcp_f32_e32 v46, v13
	v_div_scale_f32 v0, vcc, 1.0, v12, 1.0
	v_fma_f32 v1, -v13, v46, 1.0
	v_fmac_f32_e32 v46, v1, v46
	v_mul_f32_e32 v1, v0, v46
	v_fma_f32 v47, -v13, v1, v0
	v_fmac_f32_e32 v1, v47, v46
	v_fma_f32 v0, -v13, v1, v0
	v_div_fmas_f32 v0, v0, v46, v1
	v_div_fixup_f32 v0, v0, v12, 1.0
	v_pk_mul_f32 v[12:13], v[34:35], v[0:1] op_sel_hi:[1,0]
	v_pk_mul_f32 v[34:35], v[36:37], v[0:1] op_sel_hi:[1,0]
	v_pk_mul_f32 v[36:37], v[40:41], v[0:1] op_sel_hi:[1,0]
	v_pk_mul_f32 v[40:41], v[42:43], v[0:1] op_sel_hi:[1,0]
	v_pk_mul_f32 v[30:31], v[30:31], v[0:1] op_sel_hi:[1,0]
	v_pk_mul_f32 v[32:33], v[32:33], v[0:1] op_sel_hi:[1,0]
	s_waitcnt vmcnt(3)
	v_pk_fma_f32 v[6:7], v[6:7], v[12:13], v[14:15]
	v_pk_fma_f32 v[8:9], v[8:9], v[34:35], v[16:17]
	s_waitcnt vmcnt(2)
	v_pk_fma_f32 v[0:1], v[2:3], v[36:37], v[18:19]
	v_pk_fma_f32 v[2:3], v[4:5], v[40:41], v[20:21]
	s_waitcnt vmcnt(0)
	v_pk_fma_f32 v[12:13], v[30:31], v[26:27], v[22:23]
	v_pk_fma_f32 v[14:15], v[32:33], v[28:29], v[24:25]
	v_cvt_pk_f16_f32 v5, v8, v9
	v_cvt_pk_f16_f32 v4, v6, v7
	v_cmp_eq_u32_e32 vcc, 0, v62
	global_store_dwordx4 v[38:39], v[6:9], off sc1
	global_store_dwordx4 v[38:39], v[0:3], off offset:1024 sc1
	global_store_dwordx4 v[38:39], v[12:15], off offset:2048 sc1
	s_nop 0
	v_cvt_pk_f16_f32 v3, v2, v3
	v_cvt_pk_f16_f32 v2, v0, v1
	v_cvt_pk_f16_f32 v1, v14, v15
	v_cvt_pk_f16_f32 v0, v12, v13
	global_store_dwordx2 v[44:45], v[4:5], off sc1
	global_store_dwordx2 v[44:45], v[2:3], off offset:512 sc1
	global_store_dwordx2 v[44:45], v[0:1], off offset:1024 sc1
	s_and_saveexec_b64 s[2:3], vcc
	s_cbranch_execz .LBB4_11
	s_load_dwordx2 s[2:3], s[0:1], 0x118
	v_lshlrev_b64 v[0:1], 2, v[10:11]
	s_load_dwordx2 s[0:1], s[0:1], 0x158
	s_waitcnt lgkmcnt(0)
	v_lshl_add_u64 v[2:3], s[2:3], 0, v[0:1]
	global_load_dword v2, v[2:3], off
	v_lshl_add_u64 v[0:1], s[0:1], 0, v[0:1]
	s_waitcnt vmcnt(0)
	v_cvt_f32_i32_e32 v2, v2
	v_sub_f32_e32 v2, 1.0, v2
	v_mul_f32_e32 v2, 0xc61c4000, v2
	global_store_dword v[0:1], v2, off sc1

.LBB5_5:
	v_mov_b32_e32 v34, v85
	v_mov_b32_e32 v35, v85
	s_nop 1
	v_permlane32_swap_b32_e32 v34, v35
	v_cndmask_b32_e32 v34, v34, v35, vcc
	v_add_f32_e32 v34, v85, v34
	v_div_scale_f32 v35, s[4:5], v34, v34, 1.0
	v_rcp_f32_e32 v36, v35
	v_lshl_add_u32 v1, v1, 5, s8
	v_and_or_b32 v1, v0, 31, v1
	s_mul_i32 s12, s12, 12
	v_fma_f32 v37, -v35, v36, 1.0
	v_fmac_f32_e32 v36, v37, v36
	v_div_scale_f32 v37, vcc, 1.0, v34, 1.0
	v_mul_f32_e32 v38, v37, v36
	v_fma_f32 v39, -v35, v38, v37
	v_fmac_f32_e32 v38, v39, v36
	v_fma_f32 v35, -v35, v38, v37
	v_div_fmas_f32 v35, v35, v36, v38
	v_div_fixup_f32 v34, v35, v34, 1.0
	v_mul_u32_u24_e32 v36, 0x680, v1
	v_fma_mixlo_f16 v1, v34, v2, 0
	v_fma_mixlo_f16 v35, v34, v6, 0
	v_mov_b32_e32 v2, v3
	v_mov_b32_e32 v3, v4
	s_sub_i32 s3, s3, s12
	v_pk_mul_f32 v[2:3], v[34:35], v[2:3] op_sel_hi:[0,1]
	v_mov_b32_e32 v6, v7
	v_mov_b32_e32 v7, v8
	v_mov_b32_e32 v37, 0
	s_and_b32 s3, s3, 0xff
	v_cvt_pk_f16_f32 v3, v2, v3
	v_pk_mul_f32 v[6:7], v[34:35], v[6:7] op_sel_hi:[0,1]
	v_fma_mixlo_f16 v5, v34, v5, 0
	s_mov_b32 s5, 0
	v_lshl_add_u64 v[38:39], s[6:7], 0, v[36:37]
	s_lshl_b32 s4, s3, 7
	v_pack_b32_f16 v2, v1, v3
	v_cvt_pk_f16_f32 v1, v6, v7
	v_alignbit_b32 v3, v5, v3, 16
	v_fma_mixlo_f16 v5, v34, v9, 0
	v_lshl_add_u64 v[38:39], v[38:39], 0, s[4:5]
	v_pack_b32_f16 v4, v35, v1
	v_alignbit_b32 v5, v5, v1, 16
	v_lshlrev_b32_e32 v36, 4, v82
	v_permlane32_swap_b32_e32 v2, v4
	v_permlane32_swap_b32_e32 v3, v5
	v_lshl_add_u64 v[6:7], v[38:39], 0, v[36:37]
	global_store_dwordx4 v[6:7], v[2:5], off sc1
	v_fma_mixlo_f16 v1, v34, v10, 0
	v_fma_mixlo_f16 v8, v34, v14, 0
	v_mov_b32_e32 v2, v11
	v_mov_b32_e32 v3, v12
	v_pk_mul_f32 v[2:3], v[34:35], v[2:3] op_sel_hi:[0,1]
	v_mov_b32_e32 v4, v15
	v_mov_b32_e32 v5, v16
	v_cvt_pk_f16_f32 v3, v2, v3
	v_pk_mul_f32 v[4:5], v[34:35], v[4:5] op_sel_hi:[0,1]
	v_pack_b32_f16 v2, v1, v3
	v_cvt_pk_f16_f32 v1, v4, v5
	v_fma_mixlo_f16 v5, v34, v13, 0
	v_alignbit_b32 v3, v5, v3, 16
	v_fma_mixlo_f16 v5, v34, v17, 0
	v_pack_b32_f16 v4, v8, v1
	v_alignbit_b32 v5, v5, v1, 16
	s_nop 0
	v_permlane32_swap_b32_e32 v2, v4
	v_permlane32_swap_b32_e32 v3, v5
	global_store_dwordx4 v[6:7], v[2:5], off offset:32 sc1
	v_fma_mixlo_f16 v1, v34, v18, 0
	v_fma_mixlo_f16 v8, v34, v22, 0
	v_mov_b32_e32 v2, v19
	v_mov_b32_e32 v3, v20
	v_pk_mul_f32 v[2:3], v[34:35], v[2:3] op_sel_hi:[0,1]
	v_mov_b32_e32 v4, v23
	v_mov_b32_e32 v5, v24
	v_cvt_pk_f16_f32 v3, v2, v3
	v_pk_mul_f32 v[4:5], v[34:35], v[4:5] op_sel_hi:[0,1]
	v_pack_b32_f16 v2, v1, v3
	v_cvt_pk_f16_f32 v1, v4, v5
	v_fma_mixlo_f16 v5, v34, v21, 0
	v_alignbit_b32 v3, v5, v3, 16
	v_fma_mixlo_f16 v5, v34, v25, 0
	v_pack_b32_f16 v4, v8, v1
	v_alignbit_b32 v5, v5, v1, 16
	s_nop 0
	v_permlane32_swap_b32_e32 v2, v4
	v_permlane32_swap_b32_e32 v3, v5
	global_store_dwordx4 v[6:7], v[2:5], off offset:64 sc1
	v_fma_mixlo_f16 v1, v34, v26, 0
	v_fma_mixlo_f16 v8, v34, v30, 0
	v_mov_b32_e32 v2, v27
	v_mov_b32_e32 v3, v28
	v_pk_mul_f32 v[2:3], v[34:35], v[2:3] op_sel_hi:[0,1]
	v_mov_b32_e32 v4, v31
	v_mov_b32_e32 v5, v32
	v_cvt_pk_f16_f32 v3, v2, v3
	v_pk_mul_f32 v[4:5], v[34:35], v[4:5] op_sel_hi:[0,1]
	v_pack_b32_f16 v2, v1, v3
	v_cvt_pk_f16_f32 v1, v4, v5
	v_fma_mixlo_f16 v5, v34, v29, 0
	v_alignbit_b32 v3, v5, v3, 16
	v_fma_mixlo_f16 v5, v34, v33, 0
	v_pack_b32_f16 v4, v8, v1
	v_alignbit_b32 v5, v5, v1, 16
	s_nop 0
	v_permlane32_swap_b32_e32 v2, v4
	v_permlane32_swap_b32_e32 v3, v5
	s_mov_b64 s[4:5], 0
	global_store_dwordx4 v[6:7], v[2:5], off offset:96 sc1

.LBB5_16:
	s_or_b64 exec, exec, s[0:1]
	s_mov_b32 s0, 0x717951a9
	v_cmp_eq_f32_e32 vcc, s0, v4
	s_and_b64 exec, exec, vcc
	s_cbranch_execz .LBB5_18
	v_mov_b32_e32 v0, 0
	v_mov_b32_e32 v1, 0x717951a9
	s_waitcnt lgkmcnt(0)
	global_store_dword v0, v1, s[2:3] sc1

_Z7gemm2_kILi0ELi3ELi1EEv5GArgs:
	v_lshlrev_b32_e32 v192, 4, v0
	s_getpc_b64 s[92:93]
	s_add_u32 s92, s92, 0xffff89f8
	s_addc_u32 s93, s93, 0xffffffff
	global_load_dwordx4 v[188:191], v192, s[92:93]
	s_load_dwordx8 s[8:15], s[0:1], 0x68
	s_cmpk_lt_u32 s2, 0xc0
	s_mov_b64 s[4:5], -1
	s_cbranch_scc0 .LBB11_26
	v_lshrrev_b32_e32 v149, 6, v0
	s_lshl_b32 s3, s2, 8
	v_bfe_u32 v1, v0, 3, 3
	s_load_dwordx4 s[4:7], s[0:1], 0x0
	s_load_dwordx4 s[16:19], s[0:1], 0x18
	s_and_b32 s20, s3, 0xf00
	v_lshl_or_b32 v6, v149, 5, v1
	v_or_b32_e32 v8, s20, v6
	v_mul_u32_u24_e32 v2, 0x340, v8
	v_bfe_u32 v4, v0, 4, 2
	v_lshlrev_b32_e32 v146, 1, v2
	v_mov_b32_e32 v147, 0
	v_bitop3_b32 v4, v4, v0, 7 bitop3:0x78
	s_waitcnt lgkmcnt(0)
	v_lshl_add_u64 v[2:3], s[4:5], 0, v[146:147]
	v_lshlrev_b32_e32 v146, 4, v4
	v_or_b32_e32 v4, 8, v6
	v_lshl_add_u64 v[98:99], v[2:3], 0, v[146:147]
	v_or_b32_e32 v2, s20, v4
	v_lshrrev_b32_e32 v4, 1, v4
	v_xor_b32_e32 v4, v4, v0
	v_mul_u32_u24_e32 v2, 0x340, v2
	v_mov_b32_e32 v3, v147
	v_lshlrev_b32_e32 v4, 4, v4
	v_lshl_add_u64 v[2:3], v[2:3], 1, s[4:5]
	v_and_b32_e32 v4, 0x70, v4
	v_mov_b32_e32 v5, v147
	v_lshl_add_u64 v[100:101], v[2:3], 0, v[4:5]
	v_or_b32_e32 v2, 16, v8
	v_mul_u32_u24_e32 v2, 0x340, v2
	v_mov_b32_e32 v3, v147
	v_lshl_add_u64 v[2:3], v[2:3], 1, s[4:5]
	v_xor_b32_e32 v146, 16, v146
	v_or_b32_e32 v4, 24, v6
	v_lshl_add_u64 v[102:103], v[2:3], 0, v[146:147]
	v_or_b32_e32 v2, s20, v4
	v_lshrrev_b32_e32 v4, 1, v4
	v_xor_b32_e32 v4, v4, v0
	v_lshlrev_b32_e32 v4, 3, v4
	v_mul_u32_u24_e32 v146, 0x340, v2
	v_bitop3_b32 v4, v4, 8, 56 bitop3:0x6c
	s_lshr_b32 s36, s2, 6
	s_bfe_u32 s21, s2, 0x20004
	v_lshl_add_u64 v[2:3], v[146:147], 1, s[4:5]
	v_lshlrev_b32_e32 v146, 1, v4
	v_lshl_add_u64 v[104:105], v[2:3], 0, v[146:147]
	s_mul_i32 s20, s21, 0xc0
	s_mul_i32 s4, s36, 0x300
	v_mul_u32_u24_e32 v2, 24, v149
	v_mul_u32_u24_e32 v4, 3, v149
	s_add_i32 s21, s20, s4
	v_or_b32_e32 v5, v2, v1
	v_add_u32_e32 v2, s21, v5
	v_bfe_u32 v5, v5, 1, 3
	v_lshrrev_b32_e32 v4, 1, v4
	v_and_b32_e32 v7, 7, v0
	s_movk_i32 s22, 0x680
	v_bitop3_b32 v4, v4, v5, 1 bitop3:0x6c
	v_mad_u32_u24 v6, v149, 3, 1
	v_mul_lo_u32 v146, v2, s22
	v_xor_b32_e32 v4, v4, v7
	v_lshl_or_b32 v8, v6, 3, v1
	v_lshl_add_u64 v[2:3], s[6:7], 0, v[146:147]
	v_lshlrev_b32_e32 v146, 4, v4
	v_add_u32_e32 v4, s21, v8
	v_bfe_u32 v8, v8, 1, 3
	v_lshrrev_b32_e32 v9, 1, v6
	v_bitop3_b32 v8, v9, v8, 1 bitop3:0x6c
	v_lshl_add_u64 v[106:107], v[2:3], 0, v[146:147]
	v_mov_b64_e32 v[2:3], s[6:7]
	v_xor_b32_e32 v8, v8, v7
	v_mad_u64_u32 v[4:5], s[4:5], v4, s22, v[2:3]
	v_lshlrev_b32_e32 v146, 4, v8
	v_lshl_add_u64 v[108:109], v[4:5], 0, v[146:147]
	v_mad_u32_u24 v4, v149, 3, 2
	v_lshl_or_b32 v1, v4, 3, v1
	v_add_u32_e32 v5, s21, v1
	v_mad_u64_u32 v[2:3], s[4:5], v5, s22, v[2:3]
	v_bfe_u32 v1, v1, 1, 3
	v_lshrrev_b32_e32 v5, 1, v4
	v_lshlrev_b32_e32 v141, 12, v149
	v_bitop3_b32 v1, v5, v1, 1 bitop3:0x6c
	v_readfirstlane_b32 s33, v141
	v_or_b32_e32 v142, 0x400, v141
	v_xor_b32_e32 v1, v1, v7
	s_mov_b32 m0, s33
	v_readfirstlane_b32 s28, v142
	v_or_b32_e32 v143, 0x800, v141
	v_lshlrev_b32_e32 v146, 4, v1
	global_load_lds_dwordx4 v[98:99], off
	s_mov_b32 m0, s28
	v_readfirstlane_b32 s29, v143
	v_or_b32_e32 v144, 0xc00, v141
	v_mul_u32_u24_e32 v1, 0xc00, v149
	global_load_lds_dwordx4 v[100:101], off
	s_mov_b32 m0, s29
	v_readfirstlane_b32 s30, v144
	v_or_b32_e32 v145, 0x10000, v1
	v_lshlrev_b32_e32 v1, 10, v6
	v_lshl_add_u64 v[110:111], v[2:3], 0, v[146:147]
	global_load_lds_dwordx4 v[102:103], off
	s_mov_b32 m0, s30
	v_readfirstlane_b32 s31, v145
	v_or_b32_e32 v146, 0x10000, v1
	v_lshlrev_b32_e32 v4, 10, v4
	global_load_lds_dwordx4 v[104:105], off
	s_mov_b32 m0, s31
	v_readfirstlane_b32 s34, v146
	v_or_b32_e32 v148, 0x10000, v4
	global_load_lds_dwordx4 v[106:107], off
	s_mov_b32 m0, s34
	v_readfirstlane_b32 s35, v148
	v_or_b32_e32 v134, 0x8000, v141
	global_load_lds_dwordx4 v[108:109], off
	s_mov_b32 m0, s35
	s_mov_b64 s[4:5], 0x80
	v_readfirstlane_b32 s24, v134
	v_or_b32_e32 v135, 0x8400, v141
	global_load_lds_dwordx4 v[110:111], off
	v_lshl_add_u64 v[2:3], v[98:99], 0, s[4:5]
	s_mov_b32 m0, s24
	v_readfirstlane_b32 s21, v135
	v_or_b32_e32 v136, 0x8800, v141
	s_movk_i32 s6, 0xc00
	s_waitcnt vmcnt(0)
	s_waitcnt vmcnt(0) lgkmcnt(0)
	s_barrier
	global_load_lds_dwordx4 v[2:3], off
	v_lshl_add_u64 v[2:3], v[100:101], 0, s[4:5]
	s_mov_b32 m0, s21
	v_readfirstlane_b32 s22, v136
	v_or_b32_e32 v137, 0x8c00, v141
	v_mov_b32_e32 v5, 0x16000
	global_load_lds_dwordx4 v[2:3], off
	v_lshl_add_u64 v[2:3], v[102:103], 0, s[4:5]
	s_mov_b32 m0, s22
	v_readfirstlane_b32 s23, v137
	v_mad_u32_u24 v138, v149, s6, v5
	global_load_lds_dwordx4 v[2:3], off
	v_lshl_add_u64 v[2:3], v[104:105], 0, s[4:5]
	s_mov_b32 m0, s23
	v_readfirstlane_b32 s25, v138
	v_add_u32_e32 v139, 0x16000, v1
	global_load_lds_dwordx4 v[2:3], off
	v_lshl_add_u64 v[2:3], v[106:107], 0, s[4:5]
	s_mov_b32 m0, s25
	v_readfirstlane_b32 s26, v139
	v_add_u32_e32 v140, 0x16000, v4
	global_load_lds_dwordx4 v[2:3], off
	v_lshl_add_u64 v[2:3], v[108:109], 0, s[4:5]
	s_mov_b32 m0, s26
	v_readfirstlane_b32 s27, v140
	global_load_lds_dwordx4 v[2:3], off
	v_lshl_add_u64 v[2:3], v[110:111], 0, s[4:5]
	s_mov_b32 m0, s27
	v_and_b32_e32 v156, 31, v0
	global_load_lds_dwordx4 v[2:3], off
	v_and_b32_e32 v2, 64, v0
	v_mov_b32_e32 v3, 0x60
	v_cmp_ne_u32_e32 vcc, 0, v2
	v_bfe_u32 v153, v0, 5, 1
	v_lshrrev_b32_e32 v157, 1, v0
	v_cndmask_b32_e32 v151, 0, v3, vcc
	v_lshlrev_b32_e32 v3, 6, v0
	v_or_b32_e32 v2, v151, v156
	v_and_b32_e32 v115, 0x6000, v3
	v_bfe_u32 v3, v0, 4, 1
	v_lshlrev_b32_e32 v152, 7, v2
	v_or_b32_e32 v2, 6, v153
	v_bitop3_b32 v3, v157, v3, 7 bitop3:0x6c
	s_load_dwordx2 s[6:7], s[0:1], 0x28
	v_xor_b32_e32 v2, v2, v3
	v_lshlrev_b32_e32 v154, 4, v2
	v_or_b32_e32 v2, 4, v153
	v_xor_b32_e32 v2, v2, v3
	v_lshlrev_b32_e32 v155, 4, v2
	v_or_b32_e32 v2, 2, v153
	s_cmp_lt_u32 s2, 64
	v_xor_b32_e32 v2, v2, v3
	s_cselect_b64 s[4:5], -1, 0
	s_cmp_eq_u32 s36, 1
	v_lshlrev_b32_e32 v18, 4, v2
	v_xor_b32_e32 v2, v3, v153
	s_waitcnt lgkmcnt(0)
	s_cselect_b32 s18, s18, s6
	s_cselect_b32 s19, s19, s7
	s_and_b64 s[6:7], s[4:5], exec
	v_and_b32_e32 v1, 63, v0
	v_lshlrev_b32_e32 v150, 7, v156
	v_lshlrev_b32_e32 v2, 4, v2
	s_cselect_b32 s7, s17, s19
	s_cselect_b32 s6, s16, s18
	v_or_b32_e32 v182, v2, v152
	v_or_b32_e32 v2, v2, v115
	v_add_u32_e32 v112, v2, v150
	ds_read_b128 v[2:5], v112
	v_or_b32_e32 v116, 0x10000, v182
	v_add_u32_e32 v117, 0x11000, v182
	v_add_u32_e32 v118, 0x12000, v182
	ds_read_b128 v[6:9], v116
	ds_read_b128 v[10:13], v117
	ds_read_b128 v[14:17], v112 offset:4096
	ds_read_b128 v[122:125], v118
	v_or_b32_e32 v19, v18, v115
	v_add_u32_e32 v113, v19, v150
	s_waitcnt lgkmcnt(0)
	v_mfma_f32_32x32x16_f16 v[82:97], v[2:5], v[6:9], 0
	ds_read_b128 v[126:129], v113
	v_or_b32_e32 v183, v18, v152
	v_add_u32_e32 v120, 0x11000, v183
	v_or_b32_e32 v119, 0x10000, v183
	ds_read_b128 v[130:133], v113 offset:4096
	ds_read_b128 v[158:161], v119
	v_add_u32_e32 v121, 0x12000, v183
	ds_read_b128 v[162:165], v120
	ds_read_b128 v[166:169], v121
	v_mfma_f32_32x32x16_f16 v[66:81], v[2:5], v[10:13], 0
	v_mfma_f32_32x32x16_f16 v[50:65], v[2:5], v[122:125], 0
	v_mfma_f32_32x32x16_f16 v[34:49], v[14:17], v[6:9], 0
	v_mfma_f32_32x32x16_f16 v[18:33], v[14:17], v[10:13], 0
	v_mfma_f32_32x32x16_f16 v[2:17], v[14:17], v[122:125], 0
	s_waitcnt lgkmcnt(0)
	v_mfma_f32_32x32x16_f16 v[82:97], v[126:129], v[158:161], v[82:97]
	v_or_b32_e32 v114, v155, v115
	v_or_b32_e32 v155, v155, v152
	v_add_u32_e32 v114, v114, v150
	v_or_b32_e32 v122, 0x10000, v155
	v_add_u32_e32 v123, 0x11000, v155
	v_add_u32_e32 v124, 0x12000, v155
	v_mfma_f32_32x32x16_f16 v[66:81], v[126:129], v[162:165], v[66:81]
	v_mfma_f32_32x32x16_f16 v[50:65], v[126:129], v[166:169], v[50:65]
	v_mfma_f32_32x32x16_f16 v[34:49], v[130:133], v[158:161], v[34:49]
	ds_read_b128 v[126:129], v114
	ds_read_b128 v[158:161], v114 offset:4096
	v_mfma_f32_32x32x16_f16 v[18:33], v[130:133], v[162:165], v[18:33]
	ds_read_b128 v[162:165], v122
	ds_read_b128 v[170:173], v123
	ds_read_b128 v[174:177], v124
	v_mfma_f32_32x32x16_f16 v[2:17], v[130:133], v[166:169], v[2:17]
	s_waitcnt lgkmcnt(0)
	v_mfma_f32_32x32x16_f16 v[82:97], v[126:129], v[162:165], v[82:97]
	v_or_b32_e32 v115, v154, v115
	v_or_b32_e32 v133, v154, v152
	v_add_u32_e32 v115, v115, v150
	v_or_b32_e32 v125, 0x10000, v133
	v_mfma_f32_32x32x16_f16 v[66:81], v[126:129], v[170:173], v[66:81]
	v_mfma_f32_32x32x16_f16 v[50:65], v[126:129], v[174:177], v[50:65]
	v_add_u32_e32 v126, 0x11000, v133
	v_add_u32_e32 v127, 0x12000, v133
	v_mfma_f32_32x32x16_f16 v[34:49], v[158:161], v[162:165], v[34:49]
	ds_read_b128 v[128:131], v115
	ds_read_b128 v[162:165], v115 offset:4096
	v_mfma_f32_32x32x16_f16 v[18:33], v[158:161], v[170:173], v[18:33]
	ds_read_b128 v[166:169], v125
	ds_read_b128 v[170:173], v126
	ds_read_b128 v[178:181], v127
	v_mfma_f32_32x32x16_f16 v[2:17], v[158:161], v[174:177], v[2:17]
	s_waitcnt lgkmcnt(0)
	v_mfma_f32_32x32x16_f16 v[82:97], v[128:131], v[166:169], v[82:97]
	v_mfma_f32_32x32x16_f16 v[66:81], v[128:131], v[170:173], v[66:81]
	v_mfma_f32_32x32x16_f16 v[50:65], v[128:131], v[178:181], v[50:65]
	v_mfma_f32_32x32x16_f16 v[34:49], v[162:165], v[166:169], v[34:49]
	v_mfma_f32_32x32x16_f16 v[18:33], v[162:165], v[170:173], v[18:33]
	v_mfma_f32_32x32x16_f16 v[2:17], v[162:165], v[178:181], v[2:17]
	s_mov_b64 s[16:17], 0x100
	s_mov_b32 m0, s33
	v_lshl_add_u64 v[128:129], v[98:99], 0, s[16:17]
	s_waitcnt vmcnt(0)
	s_waitcnt vmcnt(0)
	s_barrier
	global_load_lds_dwordx4 v[128:129], off
	v_lshl_add_u64 v[128:129], v[100:101], 0, s[16:17]
	s_mov_b32 m0, s28
	s_nop 0
	global_load_lds_dwordx4 v[128:129], off
	v_lshl_add_u64 v[128:129], v[102:103], 0, s[16:17]
	s_mov_b32 m0, s29
	s_nop 0
	global_load_lds_dwordx4 v[128:129], off
	v_lshl_add_u64 v[128:129], v[104:105], 0, s[16:17]
	s_mov_b32 m0, s30
	s_nop 0
	global_load_lds_dwordx4 v[128:129], off
	v_lshl_add_u64 v[128:129], v[106:107], 0, s[16:17]
	s_mov_b32 m0, s31
	s_nop 0
	global_load_lds_dwordx4 v[128:129], off
	v_lshl_add_u64 v[128:129], v[108:109], 0, s[16:17]
	s_mov_b32 m0, s34
	s_nop 0
	global_load_lds_dwordx4 v[128:129], off
	v_lshl_add_u64 v[128:129], v[110:111], 0, s[16:17]
	s_mov_b32 m0, s35
	s_nop 0
	global_load_lds_dwordx4 v[128:129], off
	ds_read_b128 v[158:161], v112 offset:32768
	v_add_u32_e32 v129, 0x16000, v182
	v_add_u32_e32 v130, 0x17000, v182
	v_or_b32_e32 v131, 0x18000, v182
	ds_read_b128 v[162:165], v129
	ds_read_b128 v[166:169], v112 offset:36864
	ds_read_b128 v[170:173], v130
	ds_read_b128 v[174:177], v131
	v_add_u32_e32 v128, 0x16000, v183
	ds_read_b128 v[178:181], v128
	s_waitcnt lgkmcnt(0)
	v_mfma_f32_32x32x16_f16 v[82:97], v[158:161], v[162:165], v[82:97]
	v_mfma_f32_32x32x16_f16 v[66:81], v[158:161], v[170:173], v[66:81]
	v_mfma_f32_32x32x16_f16 v[50:65], v[158:161], v[174:177], v[50:65]
	v_mfma_f32_32x32x16_f16 v[34:49], v[166:169], v[162:165], v[34:49]
	v_mfma_f32_32x32x16_f16 v[18:33], v[166:169], v[170:173], v[18:33]
	ds_read_b128 v[158:161], v113 offset:32768
	ds_read_b128 v[162:165], v113 offset:36864
	ds_read_b128 v[170:173], v128 offset:4096
	ds_read_b128 v[182:185], v128 offset:8192
	v_mfma_f32_32x32x16_f16 v[2:17], v[166:169], v[174:177], v[2:17]
	s_waitcnt lgkmcnt(0)
	v_mfma_f32_32x32x16_f16 v[82:97], v[158:161], v[178:181], v[82:97]
	v_add_u32_e32 v132, 0x16000, v155
	v_mfma_f32_32x32x16_f16 v[66:81], v[158:161], v[170:173], v[66:81]
	v_mfma_f32_32x32x16_f16 v[50:65], v[158:161], v[182:185], v[50:65]
	ds_read_b128 v[158:161], v114 offset:32768
	ds_read_b128 v[166:169], v114 offset:36864
	v_mfma_f32_32x32x16_f16 v[34:49], v[162:165], v[178:181], v[34:49]
	v_mfma_f32_32x32x16_f16 v[18:33], v[162:165], v[170:173], v[18:33]
	ds_read_b128 v[170:173], v132
	ds_read_b128 v[174:177], v132 offset:4096
	ds_read_b128 v[178:181], v132 offset:8192
	v_mfma_f32_32x32x16_f16 v[2:17], v[162:165], v[182:185], v[2:17]
	s_waitcnt lgkmcnt(0)
	v_mfma_f32_32x32x16_f16 v[82:97], v[158:161], v[170:173], v[82:97]
	v_add_u32_e32 v133, 0x16000, v133
	v_mfma_f32_32x32x16_f16 v[66:81], v[158:161], v[174:177], v[66:81]
	v_mfma_f32_32x32x16_f16 v[50:65], v[158:161], v[178:181], v[50:65]
	ds_read_b128 v[158:161], v115 offset:32768
	ds_read_b128 v[162:165], v115 offset:36864
	v_mfma_f32_32x32x16_f16 v[34:49], v[166:169], v[170:173], v[34:49]
	v_mfma_f32_32x32x16_f16 v[18:33], v[166:169], v[174:177], v[18:33]
	ds_read_b128 v[170:173], v133
	ds_read_b128 v[174:177], v133 offset:4096
	ds_read_b128 v[182:185], v133 offset:8192
	v_mfma_f32_32x32x16_f16 v[2:17], v[166:169], v[178:181], v[2:17]
	s_waitcnt lgkmcnt(0)
	v_mfma_f32_32x32x16_f16 v[82:97], v[158:161], v[170:173], v[82:97]
	v_mfma_f32_32x32x16_f16 v[66:81], v[158:161], v[174:177], v[66:81]
	v_mfma_f32_32x32x16_f16 v[50:65], v[158:161], v[182:185], v[50:65]
	v_mfma_f32_32x32x16_f16 v[34:49], v[162:165], v[170:173], v[34:49]
	v_mfma_f32_32x32x16_f16 v[18:33], v[162:165], v[174:177], v[18:33]
	v_mfma_f32_32x32x16_f16 v[2:17], v[162:165], v[182:185], v[2:17]
	s_mov_b64 s[16:17], 0x180
	s_mov_b32 m0, s24
	v_lshl_add_u64 v[154:155], v[98:99], 0, s[16:17]
	s_waitcnt vmcnt(0)
	s_waitcnt vmcnt(0)
	s_barrier
	global_load_lds_dwordx4 v[154:155], off
	v_lshl_add_u64 v[154:155], v[100:101], 0, s[16:17]
	s_mov_b32 m0, s21
	s_nop 0
	global_load_lds_dwordx4 v[154:155], off
	v_lshl_add_u64 v[154:155], v[102:103], 0, s[16:17]
	s_mov_b32 m0, s22
	s_nop 0
	global_load_lds_dwordx4 v[154:155], off
	v_lshl_add_u64 v[154:155], v[104:105], 0, s[16:17]
	s_mov_b32 m0, s23
	s_nop 0
	global_load_lds_dwordx4 v[154:155], off
	v_lshl_add_u64 v[154:155], v[106:107], 0, s[16:17]
	s_mov_b32 m0, s25
	s_nop 0
	global_load_lds_dwordx4 v[154:155], off
	v_lshl_add_u64 v[154:155], v[108:109], 0, s[16:17]
	s_mov_b32 m0, s26
	s_nop 0
	global_load_lds_dwordx4 v[154:155], off
	v_lshl_add_u64 v[154:155], v[110:111], 0, s[16:17]
	s_mov_b32 m0, s27
	s_nop 0
	global_load_lds_dwordx4 v[154:155], off
	ds_read_b128 v[158:161], v112
	ds_read_b128 v[162:165], v116
	ds_read_b128 v[166:169], v112 offset:4096
	ds_read_b128 v[170:173], v117
	ds_read_b128 v[174:177], v118
	ds_read_b128 v[178:181], v113
	s_waitcnt lgkmcnt(0)
	v_mfma_f32_32x32x16_f16 v[82:97], v[158:161], v[162:165], v[82:97]
	v_mfma_f32_32x32x16_f16 v[66:81], v[158:161], v[170:173], v[66:81]
	v_mfma_f32_32x32x16_f16 v[50:65], v[158:161], v[174:177], v[50:65]
	v_mfma_f32_32x32x16_f16 v[34:49], v[166:169], v[162:165], v[34:49]
	v_mfma_f32_32x32x16_f16 v[18:33], v[166:169], v[170:173], v[18:33]
	ds_read_b128 v[158:161], v113 offset:4096
	ds_read_b128 v[162:165], v119
	ds_read_b128 v[170:173], v120
	ds_read_b128 v[182:185], v121
	v_mfma_f32_32x32x16_f16 v[2:17], v[166:169], v[174:177], v[2:17]
	s_waitcnt lgkmcnt(0)
	v_mfma_f32_32x32x16_f16 v[82:97], v[178:181], v[162:165], v[82:97]
	v_mfma_f32_32x32x16_f16 v[66:81], v[178:181], v[170:173], v[66:81]
	v_mfma_f32_32x32x16_f16 v[50:65], v[178:181], v[182:185], v[50:65]
	v_mfma_f32_32x32x16_f16 v[34:49], v[158:161], v[162:165], v[34:49]
	v_mfma_f32_32x32x16_f16 v[18:33], v[158:161], v[170:173], v[18:33]
	ds_read_b128 v[162:165], v114
	ds_read_b128 v[166:169], v114 offset:4096
	ds_read_b128 v[170:173], v122
	ds_read_b128 v[174:177], v123
	ds_read_b128 v[178:181], v124
	v_mfma_f32_32x32x16_f16 v[2:17], v[158:161], v[182:185], v[2:17]
	s_waitcnt lgkmcnt(0)
	v_mfma_f32_32x32x16_f16 v[82:97], v[162:165], v[170:173], v[82:97]
	v_mfma_f32_32x32x16_f16 v[66:81], v[162:165], v[174:177], v[66:81]
	v_mfma_f32_32x32x16_f16 v[50:65], v[162:165], v[178:181], v[50:65]
	v_mfma_f32_32x32x16_f16 v[34:49], v[166:169], v[170:173], v[34:49]
	v_mfma_f32_32x32x16_f16 v[18:33], v[166:169], v[174:177], v[18:33]
	ds_read_b128 v[158:161], v115
	ds_read_b128 v[162:165], v115 offset:4096
	ds_read_b128 v[170:173], v125
	ds_read_b128 v[174:177], v126
	ds_read_b128 v[182:185], v127
	v_mfma_f32_32x32x16_f16 v[2:17], v[166:169], v[178:181], v[2:17]
	s_waitcnt lgkmcnt(0)
	v_mfma_f32_32x32x16_f16 v[82:97], v[158:161], v[170:173], v[82:97]
	v_mfma_f32_32x32x16_f16 v[66:81], v[158:161], v[174:177], v[66:81]
	v_mfma_f32_32x32x16_f16 v[50:65], v[158:161], v[182:185], v[50:65]
	v_mfma_f32_32x32x16_f16 v[34:49], v[162:165], v[170:173], v[34:49]
	v_mfma_f32_32x32x16_f16 v[18:33], v[162:165], v[174:177], v[18:33]
	v_mfma_f32_32x32x16_f16 v[2:17], v[162:165], v[182:185], v[2:17]
	s_mov_b64 s[16:17], 0x200
	s_mov_b32 m0, s33
	v_lshl_add_u64 v[154:155], v[98:99], 0, s[16:17]
	s_waitcnt vmcnt(0)
	s_waitcnt vmcnt(0)
	s_barrier
	global_load_lds_dwordx4 v[154:155], off
	v_lshl_add_u64 v[154:155], v[100:101], 0, s[16:17]
	s_mov_b32 m0, s28
	s_nop 0
	global_load_lds_dwordx4 v[154:155], off
	v_lshl_add_u64 v[154:155], v[102:103], 0, s[16:17]
	s_mov_b32 m0, s29
	s_nop 0
	global_load_lds_dwordx4 v[154:155], off
	v_lshl_add_u64 v[154:155], v[104:105], 0, s[16:17]
	s_mov_b32 m0, s30
	s_nop 0
	global_load_lds_dwordx4 v[154:155], off
	v_lshl_add_u64 v[154:155], v[106:107], 0, s[16:17]
	s_mov_b32 m0, s31
	s_nop 0
	global_load_lds_dwordx4 v[154:155], off
	v_lshl_add_u64 v[154:155], v[108:109], 0, s[16:17]
	s_mov_b32 m0, s34
	s_nop 0
	global_load_lds_dwordx4 v[154:155], off
	v_lshl_add_u64 v[154:155], v[110:111], 0, s[16:17]
	s_mov_b32 m0, s35
	s_nop 0
	global_load_lds_dwordx4 v[154:155], off
	ds_read_b128 v[158:161], v112 offset:32768
	ds_read_b128 v[162:165], v129
	ds_read_b128 v[166:169], v112 offset:36864
	ds_read_b128 v[170:173], v130
	ds_read_b128 v[174:177], v131
	ds_read_b128 v[178:181], v128
	s_waitcnt lgkmcnt(0)
	v_mfma_f32_32x32x16_f16 v[82:97], v[158:161], v[162:165], v[82:97]
	v_mfma_f32_32x32x16_f16 v[66:81], v[158:161], v[170:173], v[66:81]
	v_mfma_f32_32x32x16_f16 v[50:65], v[158:161], v[174:177], v[50:65]
	v_mfma_f32_32x32x16_f16 v[34:49], v[166:169], v[162:165], v[34:49]
	v_mfma_f32_32x32x16_f16 v[18:33], v[166:169], v[170:173], v[18:33]
	ds_read_b128 v[158:161], v113 offset:32768
	ds_read_b128 v[162:165], v113 offset:36864
	ds_read_b128 v[170:173], v128 offset:4096
	ds_read_b128 v[182:185], v128 offset:8192
	v_mfma_f32_32x32x16_f16 v[2:17], v[166:169], v[174:177], v[2:17]
	s_waitcnt lgkmcnt(0)
	v_mfma_f32_32x32x16_f16 v[82:97], v[158:161], v[178:181], v[82:97]
	v_mfma_f32_32x32x16_f16 v[66:81], v[158:161], v[170:173], v[66:81]
	v_mfma_f32_32x32x16_f16 v[50:65], v[158:161], v[182:185], v[50:65]
	v_mfma_f32_32x32x16_f16 v[34:49], v[162:165], v[178:181], v[34:49]
	v_mfma_f32_32x32x16_f16 v[18:33], v[162:165], v[170:173], v[18:33]
	ds_read_b128 v[158:161], v114 offset:32768
	ds_read_b128 v[166:169], v114 offset:36864
	ds_read_b128 v[170:173], v132
	ds_read_b128 v[174:177], v132 offset:4096
	ds_read_b128 v[178:181], v132 offset:8192
	v_mfma_f32_32x32x16_f16 v[2:17], v[162:165], v[182:185], v[2:17]
	s_waitcnt lgkmcnt(0)
	v_mfma_f32_32x32x16_f16 v[82:97], v[158:161], v[170:173], v[82:97]
	v_mfma_f32_32x32x16_f16 v[66:81], v[158:161], v[174:177], v[66:81]
	v_mfma_f32_32x32x16_f16 v[50:65], v[158:161], v[178:181], v[50:65]
	v_mfma_f32_32x32x16_f16 v[34:49], v[166:169], v[170:173], v[34:49]
	v_mfma_f32_32x32x16_f16 v[18:33], v[166:169], v[174:177], v[18:33]
	ds_read_b128 v[158:161], v115 offset:32768
	ds_read_b128 v[162:165], v115 offset:36864
	ds_read_b128 v[170:173], v133
	ds_read_b128 v[174:177], v133 offset:4096
	ds_read_b128 v[182:185], v133 offset:8192
	v_mfma_f32_32x32x16_f16 v[2:17], v[166:169], v[178:181], v[2:17]
	s_waitcnt lgkmcnt(0)
	v_mfma_f32_32x32x16_f16 v[82:97], v[158:161], v[170:173], v[82:97]
	v_mfma_f32_32x32x16_f16 v[66:81], v[158:161], v[174:177], v[66:81]
	v_mfma_f32_32x32x16_f16 v[50:65], v[158:161], v[182:185], v[50:65]
	v_mfma_f32_32x32x16_f16 v[34:49], v[162:165], v[170:173], v[34:49]
	v_mfma_f32_32x32x16_f16 v[18:33], v[162:165], v[174:177], v[18:33]
	v_mfma_f32_32x32x16_f16 v[2:17], v[162:165], v[182:185], v[2:17]
	s_mov_b64 s[16:17], 0x280
	s_mov_b32 m0, s24
	v_lshl_add_u64 v[154:155], v[98:99], 0, s[16:17]
	s_waitcnt vmcnt(0)
	s_waitcnt vmcnt(0)
	s_barrier
	global_load_lds_dwordx4 v[154:155], off
	v_lshl_add_u64 v[154:155], v[100:101], 0, s[16:17]
	s_mov_b32 m0, s21
	s_nop 0
	global_load_lds_dwordx4 v[154:155], off
	v_lshl_add_u64 v[154:155], v[102:103], 0, s[16:17]
	s_mov_b32 m0, s22
	s_nop 0
	global_load_lds_dwordx4 v[154:155], off
	v_lshl_add_u64 v[154:155], v[104:105], 0, s[16:17]
	s_mov_b32 m0, s23
	s_nop 0
	global_load_lds_dwordx4 v[154:155], off
	v_lshl_add_u64 v[154:155], v[106:107], 0, s[16:17]
	s_mov_b32 m0, s25
	s_nop 0
	global_load_lds_dwordx4 v[154:155], off
	v_lshl_add_u64 v[154:155], v[108:109], 0, s[16:17]
	s_mov_b32 m0, s26
	s_nop 0
	global_load_lds_dwordx4 v[154:155], off
	v_lshl_add_u64 v[154:155], v[110:111], 0, s[16:17]
	s_mov_b32 m0, s27
	s_nop 0
	global_load_lds_dwordx4 v[154:155], off
	ds_read_b128 v[158:161], v112
	ds_read_b128 v[162:165], v116
	ds_read_b128 v[166:169], v112 offset:4096
	ds_read_b128 v[170:173], v117
	ds_read_b128 v[174:177], v118
	ds_read_b128 v[178:181], v113
	s_waitcnt lgkmcnt(0)
	v_mfma_f32_32x32x16_f16 v[82:97], v[158:161], v[162:165], v[82:97]
	v_mfma_f32_32x32x16_f16 v[66:81], v[158:161], v[170:173], v[66:81]
	v_mfma_f32_32x32x16_f16 v[50:65], v[158:161], v[174:177], v[50:65]
	v_mfma_f32_32x32x16_f16 v[34:49], v[166:169], v[162:165], v[34:49]
	v_mfma_f32_32x32x16_f16 v[18:33], v[166:169], v[170:173], v[18:33]
	ds_read_b128 v[158:161], v113 offset:4096
	ds_read_b128 v[162:165], v119
	ds_read_b128 v[170:173], v120
	ds_read_b128 v[182:185], v121
	v_mfma_f32_32x32x16_f16 v[2:17], v[166:169], v[174:177], v[2:17]
	s_waitcnt lgkmcnt(0)
	v_mfma_f32_32x32x16_f16 v[82:97], v[178:181], v[162:165], v[82:97]
	v_mfma_f32_32x32x16_f16 v[66:81], v[178:181], v[170:173], v[66:81]
	v_mfma_f32_32x32x16_f16 v[50:65], v[178:181], v[182:185], v[50:65]
	v_mfma_f32_32x32x16_f16 v[34:49], v[158:161], v[162:165], v[34:49]
	v_mfma_f32_32x32x16_f16 v[18:33], v[158:161], v[170:173], v[18:33]
	ds_read_b128 v[162:165], v114
	ds_read_b128 v[166:169], v114 offset:4096
	ds_read_b128 v[170:173], v122
	ds_read_b128 v[174:177], v123
	ds_read_b128 v[178:181], v124
	v_mfma_f32_32x32x16_f16 v[2:17], v[158:161], v[182:185], v[2:17]
	s_waitcnt lgkmcnt(0)
	v_mfma_f32_32x32x16_f16 v[82:97], v[162:165], v[170:173], v[82:97]
	v_mfma_f32_32x32x16_f16 v[66:81], v[162:165], v[174:177], v[66:81]
	v_mfma_f32_32x32x16_f16 v[50:65], v[162:165], v[178:181], v[50:65]
	v_mfma_f32_32x32x16_f16 v[34:49], v[166:169], v[170:173], v[34:49]
	v_mfma_f32_32x32x16_f16 v[18:33], v[166:169], v[174:177], v[18:33]
	ds_read_b128 v[158:161], v115
	ds_read_b128 v[162:165], v115 offset:4096
	ds_read_b128 v[170:173], v125
	ds_read_b128 v[174:177], v126
	ds_read_b128 v[182:185], v127
	v_mfma_f32_32x32x16_f16 v[2:17], v[166:169], v[178:181], v[2:17]
	s_waitcnt lgkmcnt(0)
	v_mfma_f32_32x32x16_f16 v[82:97], v[158:161], v[170:173], v[82:97]
	v_mfma_f32_32x32x16_f16 v[66:81], v[158:161], v[174:177], v[66:81]
	v_mfma_f32_32x32x16_f16 v[50:65], v[158:161], v[182:185], v[50:65]
	v_mfma_f32_32x32x16_f16 v[34:49], v[162:165], v[170:173], v[34:49]
	v_mfma_f32_32x32x16_f16 v[18:33], v[162:165], v[174:177], v[18:33]
	v_mfma_f32_32x32x16_f16 v[2:17], v[162:165], v[182:185], v[2:17]
	s_mov_b64 s[22:23], 0x300
	v_readfirstlane_b32 s24, v141
	v_lshl_add_u64 v[154:155], v[98:99], 0, s[22:23]
	s_mov_b32 m0, s24
	v_readfirstlane_b32 s16, v142
	s_waitcnt vmcnt(0)
	s_waitcnt vmcnt(0)
	s_barrier
	global_load_lds_dwordx4 v[154:155], off
	v_lshl_add_u64 v[154:155], v[100:101], 0, s[22:23]
	s_mov_b32 m0, s16
	v_readfirstlane_b32 s17, v143
	global_load_lds_dwordx4 v[154:155], off
	v_lshl_add_u64 v[154:155], v[102:103], 0, s[22:23]
	s_mov_b32 m0, s17
	v_readfirstlane_b32 s18, v144
	global_load_lds_dwordx4 v[154:155], off
	v_lshl_add_u64 v[142:143], v[104:105], 0, s[22:23]
	s_mov_b32 m0, s18
	v_readfirstlane_b32 s19, v145
	global_load_lds_dwordx4 v[142:143], off
	v_lshl_add_u64 v[142:143], v[106:107], 0, s[22:23]
	s_mov_b32 m0, s19
	v_readfirstlane_b32 s21, v146
	global_load_lds_dwordx4 v[142:143], off
	v_lshl_add_u64 v[142:143], v[108:109], 0, s[22:23]
	s_mov_b32 m0, s21
	s_nop 0
	global_load_lds_dwordx4 v[142:143], off
	v_lshl_add_u64 v[142:143], v[110:111], 0, s[22:23]
	v_readfirstlane_b32 s22, v148
	s_mov_b32 m0, s22
	s_nop 0
	global_load_lds_dwordx4 v[142:143], off
	ds_read_b128 v[142:145], v112 offset:32768
	ds_read_b128 v[158:161], v129
	ds_read_b128 v[162:165], v112 offset:36864
	ds_read_b128 v[166:169], v130
	ds_read_b128 v[170:173], v131
	ds_read_b128 v[174:177], v128
	s_waitcnt lgkmcnt(0)
	v_mfma_f32_32x32x16_f16 v[82:97], v[142:145], v[158:161], v[82:97]
	v_mfma_f32_32x32x16_f16 v[66:81], v[142:145], v[166:169], v[66:81]
	v_mfma_f32_32x32x16_f16 v[50:65], v[142:145], v[170:173], v[50:65]
	v_mfma_f32_32x32x16_f16 v[34:49], v[162:165], v[158:161], v[34:49]
	v_mfma_f32_32x32x16_f16 v[18:33], v[162:165], v[166:169], v[18:33]
	ds_read_b128 v[142:145], v113 offset:32768
	ds_read_b128 v[158:161], v113 offset:36864
	ds_read_b128 v[166:169], v128 offset:4096
	ds_read_b128 v[178:181], v128 offset:8192
	v_mfma_f32_32x32x16_f16 v[2:17], v[162:165], v[170:173], v[2:17]
	s_waitcnt lgkmcnt(0)
	v_mfma_f32_32x32x16_f16 v[82:97], v[142:145], v[174:177], v[82:97]
	v_mfma_f32_32x32x16_f16 v[66:81], v[142:145], v[166:169], v[66:81]
	v_mfma_f32_32x32x16_f16 v[50:65], v[142:145], v[178:181], v[50:65]
	v_mfma_f32_32x32x16_f16 v[34:49], v[158:161], v[174:177], v[34:49]
	v_mfma_f32_32x32x16_f16 v[18:33], v[158:161], v[166:169], v[18:33]
	ds_read_b128 v[142:145], v114 offset:32768
	ds_read_b128 v[162:165], v114 offset:36864
	ds_read_b128 v[166:169], v132
	ds_read_b128 v[170:173], v132 offset:4096
	ds_read_b128 v[174:177], v132 offset:8192
	v_mfma_f32_32x32x16_f16 v[2:17], v[158:161], v[178:181], v[2:17]
	s_waitcnt lgkmcnt(0)
	v_mfma_f32_32x32x16_f16 v[82:97], v[142:145], v[166:169], v[82:97]
	v_mfma_f32_32x32x16_f16 v[66:81], v[142:145], v[170:173], v[66:81]
	v_mfma_f32_32x32x16_f16 v[50:65], v[142:145], v[174:177], v[50:65]
	v_mfma_f32_32x32x16_f16 v[34:49], v[162:165], v[166:169], v[34:49]
	v_mfma_f32_32x32x16_f16 v[18:33], v[162:165], v[170:173], v[18:33]
	ds_read_b128 v[142:145], v115 offset:32768
	ds_read_b128 v[158:161], v115 offset:36864
	ds_read_b128 v[166:169], v133
	ds_read_b128 v[170:173], v133 offset:4096
	ds_read_b128 v[178:181], v133 offset:8192
	v_mfma_f32_32x32x16_f16 v[2:17], v[162:165], v[174:177], v[2:17]
	s_waitcnt lgkmcnt(0)
	v_mfma_f32_32x32x16_f16 v[82:97], v[142:145], v[166:169], v[82:97]
	v_mfma_f32_32x32x16_f16 v[66:81], v[142:145], v[170:173], v[66:81]
	v_mfma_f32_32x32x16_f16 v[50:65], v[142:145], v[178:181], v[50:65]
	v_mfma_f32_32x32x16_f16 v[34:49], v[158:161], v[166:169], v[34:49]
	v_mfma_f32_32x32x16_f16 v[18:33], v[158:161], v[170:173], v[18:33]
	v_mfma_f32_32x32x16_f16 v[2:17], v[158:161], v[178:181], v[2:17]
	s_mov_b64 s[34:35], 0x380
	v_readfirstlane_b32 s30, v134
	v_lshl_add_u64 v[142:143], v[98:99], 0, s[34:35]
	s_mov_b32 m0, s30
	v_readfirstlane_b32 s23, v135
	s_waitcnt vmcnt(0)
	s_waitcnt vmcnt(0)
	s_barrier
	global_load_lds_dwordx4 v[142:143], off
	v_lshl_add_u64 v[142:143], v[100:101], 0, s[34:35]
	s_mov_b32 m0, s23
	v_readfirstlane_b32 s25, v136
	global_load_lds_dwordx4 v[142:143], off
	v_lshl_add_u64 v[134:135], v[102:103], 0, s[34:35]
	s_mov_b32 m0, s25
	v_readfirstlane_b32 s26, v137
	global_load_lds_dwordx4 v[134:135], off
	v_lshl_add_u64 v[134:135], v[104:105], 0, s[34:35]
	s_mov_b32 m0, s26
	v_readfirstlane_b32 s27, v138
	global_load_lds_dwordx4 v[134:135], off
	v_lshl_add_u64 v[134:135], v[106:107], 0, s[34:35]
	s_mov_b32 m0, s27
	v_readfirstlane_b32 s28, v139
	global_load_lds_dwordx4 v[134:135], off
	v_lshl_add_u64 v[134:135], v[108:109], 0, s[34:35]
	s_mov_b32 m0, s28
	v_readfirstlane_b32 s29, v140
	global_load_lds_dwordx4 v[134:135], off
	v_lshl_add_u64 v[134:135], v[110:111], 0, s[34:35]
	s_mov_b32 m0, s29
	s_nop 0
	global_load_lds_dwordx4 v[134:135], off
	ds_read_b128 v[134:137], v112
	ds_read_b128 v[138:141], v116
	ds_read_b128 v[142:145], v112 offset:4096
	ds_read_b128 v[158:161], v117
	ds_read_b128 v[162:165], v118
	ds_read_b128 v[166:169], v113
	s_waitcnt lgkmcnt(0)
	v_mfma_f32_32x32x16_f16 v[82:97], v[134:137], v[138:141], v[82:97]
	v_mfma_f32_32x32x16_f16 v[66:81], v[134:137], v[158:161], v[66:81]
	v_mfma_f32_32x32x16_f16 v[50:65], v[134:137], v[162:165], v[50:65]
	v_mfma_f32_32x32x16_f16 v[34:49], v[142:145], v[138:141], v[34:49]
	v_mfma_f32_32x32x16_f16 v[18:33], v[142:145], v[158:161], v[18:33]
	ds_read_b128 v[134:137], v113 offset:4096
	ds_read_b128 v[138:141], v119
	ds_read_b128 v[158:161], v120
	ds_read_b128 v[170:173], v121
	v_mfma_f32_32x32x16_f16 v[2:17], v[142:145], v[162:165], v[2:17]
	s_waitcnt lgkmcnt(0)
	v_mfma_f32_32x32x16_f16 v[82:97], v[166:169], v[138:141], v[82:97]
	v_mfma_f32_32x32x16_f16 v[66:81], v[166:169], v[158:161], v[66:81]
	v_mfma_f32_32x32x16_f16 v[50:65], v[166:169], v[170:173], v[50:65]
	v_mfma_f32_32x32x16_f16 v[34:49], v[134:137], v[138:141], v[34:49]
	v_mfma_f32_32x32x16_f16 v[18:33], v[134:137], v[158:161], v[18:33]
	ds_read_b128 v[138:141], v114
	ds_read_b128 v[142:145], v114 offset:4096
	ds_read_b128 v[158:161], v122
	ds_read_b128 v[162:165], v123
	ds_read_b128 v[166:169], v124
	v_mfma_f32_32x32x16_f16 v[2:17], v[134:137], v[170:173], v[2:17]
	s_waitcnt lgkmcnt(0)
	v_mfma_f32_32x32x16_f16 v[82:97], v[138:141], v[158:161], v[82:97]
	v_mfma_f32_32x32x16_f16 v[66:81], v[138:141], v[162:165], v[66:81]
	v_mfma_f32_32x32x16_f16 v[50:65], v[138:141], v[166:169], v[50:65]
	v_mfma_f32_32x32x16_f16 v[34:49], v[142:145], v[158:161], v[34:49]
	v_mfma_f32_32x32x16_f16 v[18:33], v[142:145], v[162:165], v[18:33]
	ds_read_b128 v[134:137], v115
	ds_read_b128 v[138:141], v115 offset:4096
	ds_read_b128 v[158:161], v125
	ds_read_b128 v[162:165], v126
	ds_read_b128 v[170:173], v127
	v_mfma_f32_32x32x16_f16 v[2:17], v[142:145], v[166:169], v[2:17]
	s_waitcnt lgkmcnt(0)
	v_mfma_f32_32x32x16_f16 v[82:97], v[134:137], v[158:161], v[82:97]
	v_mfma_f32_32x32x16_f16 v[66:81], v[134:137], v[162:165], v[66:81]
	v_mfma_f32_32x32x16_f16 v[50:65], v[134:137], v[170:173], v[50:65]
	v_mfma_f32_32x32x16_f16 v[34:49], v[138:141], v[158:161], v[34:49]
	v_mfma_f32_32x32x16_f16 v[18:33], v[138:141], v[162:165], v[18:33]
	v_mfma_f32_32x32x16_f16 v[2:17], v[138:141], v[170:173], v[2:17]
	s_mov_b64 s[34:35], 0x400
	s_mov_b32 m0, s24
	v_lshl_add_u64 v[134:135], v[98:99], 0, s[34:35]
	s_waitcnt vmcnt(0)
	s_waitcnt vmcnt(0)
	s_barrier
	global_load_lds_dwordx4 v[134:135], off
	v_lshl_add_u64 v[134:135], v[100:101], 0, s[34:35]
	s_mov_b32 m0, s16
	s_nop 0
	global_load_lds_dwordx4 v[134:135], off
	v_lshl_add_u64 v[134:135], v[102:103], 0, s[34:35]
	s_mov_b32 m0, s17
	s_nop 0
	global_load_lds_dwordx4 v[134:135], off
	v_lshl_add_u64 v[134:135], v[104:105], 0, s[34:35]
	s_mov_b32 m0, s18
	s_nop 0
	global_load_lds_dwordx4 v[134:135], off
	v_lshl_add_u64 v[134:135], v[106:107], 0, s[34:35]
	s_mov_b32 m0, s19
	s_nop 0
	global_load_lds_dwordx4 v[134:135], off
	v_lshl_add_u64 v[134:135], v[108:109], 0, s[34:35]
	s_mov_b32 m0, s21
	s_nop 0
	global_load_lds_dwordx4 v[134:135], off
	v_lshl_add_u64 v[134:135], v[110:111], 0, s[34:35]
	s_mov_b32 m0, s22
	s_nop 0
	global_load_lds_dwordx4 v[134:135], off
	ds_read_b128 v[134:137], v112 offset:32768
	ds_read_b128 v[138:141], v129
	ds_read_b128 v[142:145], v112 offset:36864
	ds_read_b128 v[158:161], v130
	ds_read_b128 v[162:165], v131
	ds_read_b128 v[166:169], v128
	s_waitcnt lgkmcnt(0)
	v_mfma_f32_32x32x16_f16 v[82:97], v[134:137], v[138:141], v[82:97]
	v_mfma_f32_32x32x16_f16 v[66:81], v[134:137], v[158:161], v[66:81]
	v_mfma_f32_32x32x16_f16 v[50:65], v[134:137], v[162:165], v[50:65]
	v_mfma_f32_32x32x16_f16 v[34:49], v[142:145], v[138:141], v[34:49]
	v_mfma_f32_32x32x16_f16 v[18:33], v[142:145], v[158:161], v[18:33]
	ds_read_b128 v[134:137], v113 offset:32768
	ds_read_b128 v[138:141], v113 offset:36864
	ds_read_b128 v[158:161], v128 offset:4096
	ds_read_b128 v[170:173], v128 offset:8192
	v_mfma_f32_32x32x16_f16 v[2:17], v[142:145], v[162:165], v[2:17]
	s_waitcnt lgkmcnt(0)
	v_mfma_f32_32x32x16_f16 v[82:97], v[134:137], v[166:169], v[82:97]
	v_mfma_f32_32x32x16_f16 v[66:81], v[134:137], v[158:161], v[66:81]
	v_mfma_f32_32x32x16_f16 v[50:65], v[134:137], v[170:173], v[50:65]
	v_mfma_f32_32x32x16_f16 v[34:49], v[138:141], v[166:169], v[34:49]
	v_mfma_f32_32x32x16_f16 v[18:33], v[138:141], v[158:161], v[18:33]
	ds_read_b128 v[134:137], v114 offset:32768
	ds_read_b128 v[142:145], v114 offset:36864
	ds_read_b128 v[158:161], v132
	ds_read_b128 v[162:165], v132 offset:4096
	ds_read_b128 v[166:169], v132 offset:8192
	v_mfma_f32_32x32x16_f16 v[2:17], v[138:141], v[170:173], v[2:17]
	s_waitcnt lgkmcnt(0)
	v_mfma_f32_32x32x16_f16 v[82:97], v[134:137], v[158:161], v[82:97]
	v_mfma_f32_32x32x16_f16 v[66:81], v[134:137], v[162:165], v[66:81]
	v_mfma_f32_32x32x16_f16 v[50:65], v[134:137], v[166:169], v[50:65]
	v_mfma_f32_32x32x16_f16 v[34:49], v[142:145], v[158:161], v[34:49]
	v_mfma_f32_32x32x16_f16 v[18:33], v[142:145], v[162:165], v[18:33]
	ds_read_b128 v[134:137], v115 offset:32768
	ds_read_b128 v[138:141], v115 offset:36864
	ds_read_b128 v[158:161], v133
	ds_read_b128 v[162:165], v133 offset:4096
	ds_read_b128 v[170:173], v133 offset:8192
	v_mfma_f32_32x32x16_f16 v[2:17], v[142:145], v[166:169], v[2:17]
	s_waitcnt lgkmcnt(0)
	v_mfma_f32_32x32x16_f16 v[82:97], v[134:137], v[158:161], v[82:97]
	v_mfma_f32_32x32x16_f16 v[66:81], v[134:137], v[162:165], v[66:81]
	v_mfma_f32_32x32x16_f16 v[50:65], v[134:137], v[170:173], v[50:65]
	v_mfma_f32_32x32x16_f16 v[34:49], v[138:141], v[158:161], v[34:49]
	v_mfma_f32_32x32x16_f16 v[18:33], v[138:141], v[162:165], v[18:33]
	v_mfma_f32_32x32x16_f16 v[2:17], v[138:141], v[170:173], v[2:17]
	s_mov_b64 s[34:35], 0x480
	s_mov_b32 m0, s30
	v_lshl_add_u64 v[134:135], v[98:99], 0, s[34:35]
	s_waitcnt vmcnt(0)
	s_waitcnt vmcnt(0)
	s_barrier
	global_load_lds_dwordx4 v[134:135], off
	v_lshl_add_u64 v[134:135], v[100:101], 0, s[34:35]
	s_mov_b32 m0, s23
	s_nop 0
	global_load_lds_dwordx4 v[134:135], off
	v_lshl_add_u64 v[134:135], v[102:103], 0, s[34:35]
	s_mov_b32 m0, s25
	s_nop 0
	global_load_lds_dwordx4 v[134:135], off
	v_lshl_add_u64 v[134:135], v[104:105], 0, s[34:35]
	s_mov_b32 m0, s26
	s_nop 0
	global_load_lds_dwordx4 v[134:135], off
	v_lshl_add_u64 v[134:135], v[106:107], 0, s[34:35]
	s_mov_b32 m0, s27
	s_nop 0
	global_load_lds_dwordx4 v[134:135], off
	v_lshl_add_u64 v[134:135], v[108:109], 0, s[34:35]
	s_mov_b32 m0, s28
	s_nop 0
	global_load_lds_dwordx4 v[134:135], off
	v_lshl_add_u64 v[134:135], v[110:111], 0, s[34:35]
	s_mov_b32 m0, s29
	s_nop 0
	global_load_lds_dwordx4 v[134:135], off
	ds_read_b128 v[134:137], v112
	ds_read_b128 v[138:141], v116
	ds_read_b128 v[142:145], v112 offset:4096
	ds_read_b128 v[158:161], v117
	ds_read_b128 v[162:165], v118
	ds_read_b128 v[166:169], v113
	s_waitcnt lgkmcnt(0)
	v_mfma_f32_32x32x16_f16 v[82:97], v[134:137], v[138:141], v[82:97]
	v_mfma_f32_32x32x16_f16 v[66:81], v[134:137], v[158:161], v[66:81]
	v_mfma_f32_32x32x16_f16 v[50:65], v[134:137], v[162:165], v[50:65]
	v_mfma_f32_32x32x16_f16 v[34:49], v[142:145], v[138:141], v[34:49]
	v_mfma_f32_32x32x16_f16 v[18:33], v[142:145], v[158:161], v[18:33]
	ds_read_b128 v[134:137], v113 offset:4096
	ds_read_b128 v[138:141], v119
	ds_read_b128 v[158:161], v120
	ds_read_b128 v[170:173], v121
	v_mfma_f32_32x32x16_f16 v[2:17], v[142:145], v[162:165], v[2:17]
	s_waitcnt lgkmcnt(0)
	v_mfma_f32_32x32x16_f16 v[82:97], v[166:169], v[138:141], v[82:97]
	v_mfma_f32_32x32x16_f16 v[66:81], v[166:169], v[158:161], v[66:81]
	v_mfma_f32_32x32x16_f16 v[50:65], v[166:169], v[170:173], v[50:65]
	v_mfma_f32_32x32x16_f16 v[34:49], v[134:137], v[138:141], v[34:49]
	v_mfma_f32_32x32x16_f16 v[18:33], v[134:137], v[158:161], v[18:33]
	ds_read_b128 v[138:141], v114
	ds_read_b128 v[142:145], v114 offset:4096
	ds_read_b128 v[158:161], v122
	ds_read_b128 v[162:165], v123
	ds_read_b128 v[166:169], v124
	v_mfma_f32_32x32x16_f16 v[2:17], v[134:137], v[170:173], v[2:17]
	s_waitcnt lgkmcnt(0)
	v_mfma_f32_32x32x16_f16 v[82:97], v[138:141], v[158:161], v[82:97]
	v_mfma_f32_32x32x16_f16 v[66:81], v[138:141], v[162:165], v[66:81]
	v_mfma_f32_32x32x16_f16 v[50:65], v[138:141], v[166:169], v[50:65]
	v_mfma_f32_32x32x16_f16 v[34:49], v[142:145], v[158:161], v[34:49]
	v_mfma_f32_32x32x16_f16 v[18:33], v[142:145], v[162:165], v[18:33]
	ds_read_b128 v[134:137], v115
	ds_read_b128 v[138:141], v115 offset:4096
	ds_read_b128 v[158:161], v125
	ds_read_b128 v[162:165], v126
	ds_read_b128 v[170:173], v127
	v_mfma_f32_32x32x16_f16 v[2:17], v[142:145], v[166:169], v[2:17]
	s_waitcnt lgkmcnt(0)
	v_mfma_f32_32x32x16_f16 v[82:97], v[134:137], v[158:161], v[82:97]
	v_mfma_f32_32x32x16_f16 v[66:81], v[134:137], v[162:165], v[66:81]
	v_mfma_f32_32x32x16_f16 v[50:65], v[134:137], v[170:173], v[50:65]
	v_mfma_f32_32x32x16_f16 v[34:49], v[138:141], v[158:161], v[34:49]
	v_mfma_f32_32x32x16_f16 v[18:33], v[138:141], v[162:165], v[18:33]
	v_mfma_f32_32x32x16_f16 v[2:17], v[138:141], v[170:173], v[2:17]
	s_mov_b64 s[34:35], 0x500
	s_mov_b32 m0, s24
	v_lshl_add_u64 v[134:135], v[98:99], 0, s[34:35]
	s_waitcnt vmcnt(0)
	s_waitcnt vmcnt(0)
	s_barrier
	global_load_lds_dwordx4 v[134:135], off
	v_lshl_add_u64 v[134:135], v[100:101], 0, s[34:35]
	s_mov_b32 m0, s16
	s_nop 0
	global_load_lds_dwordx4 v[134:135], off
	v_lshl_add_u64 v[134:135], v[102:103], 0, s[34:35]
	s_mov_b32 m0, s17
	s_nop 0
	global_load_lds_dwordx4 v[134:135], off
	v_lshl_add_u64 v[134:135], v[104:105], 0, s[34:35]
	s_mov_b32 m0, s18
	s_nop 0
	global_load_lds_dwordx4 v[134:135], off
	v_lshl_add_u64 v[134:135], v[106:107], 0, s[34:35]
	s_mov_b32 m0, s19
	s_nop 0
	global_load_lds_dwordx4 v[134:135], off
	v_lshl_add_u64 v[134:135], v[108:109], 0, s[34:35]
	s_mov_b32 m0, s21
	s_nop 0
	global_load_lds_dwordx4 v[134:135], off
	v_lshl_add_u64 v[134:135], v[110:111], 0, s[34:35]
	s_mov_b32 m0, s22
	s_nop 0
	global_load_lds_dwordx4 v[134:135], off
	ds_read_b128 v[134:137], v112 offset:32768
	ds_read_b128 v[138:141], v129
	ds_read_b128 v[142:145], v112 offset:36864
	ds_read_b128 v[158:161], v130
	ds_read_b128 v[162:165], v131
	ds_read_b128 v[166:169], v128
	s_waitcnt lgkmcnt(0)
	v_mfma_f32_32x32x16_f16 v[82:97], v[134:137], v[138:141], v[82:97]
	v_mfma_f32_32x32x16_f16 v[66:81], v[134:137], v[158:161], v[66:81]
	v_mfma_f32_32x32x16_f16 v[50:65], v[134:137], v[162:165], v[50:65]
	v_mfma_f32_32x32x16_f16 v[34:49], v[142:145], v[138:141], v[34:49]
	v_mfma_f32_32x32x16_f16 v[18:33], v[142:145], v[158:161], v[18:33]
	ds_read_b128 v[134:137], v113 offset:32768
	ds_read_b128 v[138:141], v113 offset:36864
	ds_read_b128 v[158:161], v128 offset:4096
	ds_read_b128 v[170:173], v128 offset:8192
	v_mfma_f32_32x32x16_f16 v[2:17], v[142:145], v[162:165], v[2:17]
	s_waitcnt lgkmcnt(0)
	v_mfma_f32_32x32x16_f16 v[82:97], v[134:137], v[166:169], v[82:97]
	v_mfma_f32_32x32x16_f16 v[66:81], v[134:137], v[158:161], v[66:81]
	v_mfma_f32_32x32x16_f16 v[50:65], v[134:137], v[170:173], v[50:65]
	v_mfma_f32_32x32x16_f16 v[34:49], v[138:141], v[166:169], v[34:49]
	v_mfma_f32_32x32x16_f16 v[18:33], v[138:141], v[158:161], v[18:33]
	ds_read_b128 v[134:137], v114 offset:32768
	ds_read_b128 v[142:145], v114 offset:36864
	ds_read_b128 v[158:161], v132
	ds_read_b128 v[162:165], v132 offset:4096
	ds_read_b128 v[166:169], v132 offset:8192
	v_mfma_f32_32x32x16_f16 v[2:17], v[138:141], v[170:173], v[2:17]
	s_waitcnt lgkmcnt(0)
	v_mfma_f32_32x32x16_f16 v[82:97], v[134:137], v[158:161], v[82:97]
	v_mfma_f32_32x32x16_f16 v[66:81], v[134:137], v[162:165], v[66:81]
	v_mfma_f32_32x32x16_f16 v[50:65], v[134:137], v[166:169], v[50:65]
	v_mfma_f32_32x32x16_f16 v[34:49], v[142:145], v[158:161], v[34:49]
	v_mfma_f32_32x32x16_f16 v[18:33], v[142:145], v[162:165], v[18:33]
	ds_read_b128 v[134:137], v115 offset:32768
	ds_read_b128 v[138:141], v115 offset:36864
	ds_read_b128 v[158:161], v133
	ds_read_b128 v[162:165], v133 offset:4096
	ds_read_b128 v[170:173], v133 offset:8192
	v_mfma_f32_32x32x16_f16 v[2:17], v[142:145], v[166:169], v[2:17]
	s_waitcnt lgkmcnt(0)
	v_mfma_f32_32x32x16_f16 v[82:97], v[134:137], v[158:161], v[82:97]
	v_mfma_f32_32x32x16_f16 v[66:81], v[134:137], v[162:165], v[66:81]
	v_mfma_f32_32x32x16_f16 v[50:65], v[134:137], v[170:173], v[50:65]
	v_mfma_f32_32x32x16_f16 v[34:49], v[138:141], v[158:161], v[34:49]
	v_mfma_f32_32x32x16_f16 v[18:33], v[138:141], v[162:165], v[18:33]
	v_mfma_f32_32x32x16_f16 v[2:17], v[138:141], v[170:173], v[2:17]
	s_mov_b64 s[16:17], 0x580
	s_mov_b32 m0, s30
	v_lshl_add_u64 v[98:99], v[98:99], 0, s[16:17]
	s_waitcnt vmcnt(0)
	s_waitcnt vmcnt(0)
	s_barrier
	global_load_lds_dwordx4 v[98:99], off
	v_lshl_add_u64 v[98:99], v[100:101], 0, s[16:17]
	s_mov_b32 m0, s23
	s_nop 0
	global_load_lds_dwordx4 v[98:99], off
	v_lshl_add_u64 v[98:99], v[102:103], 0, s[16:17]
	s_mov_b32 m0, s25
	s_nop 0
	global_load_lds_dwordx4 v[98:99], off
	v_lshl_add_u64 v[98:99], v[104:105], 0, s[16:17]
	s_mov_b32 m0, s26
	s_nop 0
	global_load_lds_dwordx4 v[98:99], off
	v_lshl_add_u64 v[98:99], v[106:107], 0, s[16:17]
	s_mov_b32 m0, s27
	s_nop 0
	global_load_lds_dwordx4 v[98:99], off
	v_lshl_add_u64 v[98:99], v[108:109], 0, s[16:17]
	s_mov_b32 m0, s28
	s_nop 0
	global_load_lds_dwordx4 v[98:99], off
	v_lshl_add_u64 v[98:99], v[110:111], 0, s[16:17]
	s_mov_b32 m0, s29
	s_nop 0
	global_load_lds_dwordx4 v[98:99], off
	ds_read_b128 v[98:101], v112
	ds_read_b128 v[102:105], v116
	ds_read_b128 v[106:109], v112 offset:4096
	ds_read_b128 v[134:137], v117
	ds_read_b128 v[138:141], v118
	ds_read_b128 v[142:145], v113
	s_waitcnt lgkmcnt(0)
	v_mfma_f32_32x32x16_f16 v[82:97], v[98:101], v[102:105], v[82:97]
	v_mfma_f32_32x32x16_f16 v[66:81], v[98:101], v[134:137], v[66:81]
	v_mfma_f32_32x32x16_f16 v[50:65], v[98:101], v[138:141], v[50:65]
	v_mfma_f32_32x32x16_f16 v[34:49], v[106:109], v[102:105], v[34:49]
	v_mfma_f32_32x32x16_f16 v[18:33], v[106:109], v[134:137], v[18:33]
	ds_read_b128 v[98:101], v113 offset:4096
	ds_read_b128 v[102:105], v119
	ds_read_b128 v[116:119], v120
	ds_read_b128 v[134:137], v121
	v_mfma_f32_32x32x16_f16 v[2:17], v[106:109], v[138:141], v[2:17]
	s_waitcnt lgkmcnt(0)
	v_mfma_f32_32x32x16_f16 v[82:97], v[142:145], v[102:105], v[82:97]
	v_mfma_f32_32x32x16_f16 v[66:81], v[142:145], v[116:119], v[66:81]
	v_mfma_f32_32x32x16_f16 v[50:65], v[142:145], v[134:137], v[50:65]
	v_mfma_f32_32x32x16_f16 v[34:49], v[98:101], v[102:105], v[34:49]
	v_mfma_f32_32x32x16_f16 v[18:33], v[98:101], v[116:119], v[18:33]
	ds_read_b128 v[102:105], v114
	ds_read_b128 v[106:109], v114 offset:4096
	ds_read_b128 v[116:119], v122
	ds_read_b128 v[120:123], v123
	ds_read_b128 v[138:141], v124
	v_mfma_f32_32x32x16_f16 v[2:17], v[98:101], v[134:137], v[2:17]
	s_waitcnt lgkmcnt(0)
	v_mfma_f32_32x32x16_f16 v[82:97], v[102:105], v[116:119], v[82:97]
	v_mfma_f32_32x32x16_f16 v[66:81], v[102:105], v[120:123], v[66:81]
	v_mfma_f32_32x32x16_f16 v[50:65], v[102:105], v[138:141], v[50:65]
	v_mfma_f32_32x32x16_f16 v[34:49], v[106:109], v[116:119], v[34:49]
	v_mfma_f32_32x32x16_f16 v[18:33], v[106:109], v[120:123], v[18:33]
	ds_read_b128 v[98:101], v115
	ds_read_b128 v[102:105], v115 offset:4096
	ds_read_b128 v[116:119], v125
	ds_read_b128 v[120:123], v126
	ds_read_b128 v[124:127], v127
	v_mfma_f32_32x32x16_f16 v[2:17], v[106:109], v[138:141], v[2:17]
	s_waitcnt lgkmcnt(0)
	v_mfma_f32_32x32x16_f16 v[82:97], v[98:101], v[116:119], v[82:97]
	v_mfma_f32_32x32x16_f16 v[66:81], v[98:101], v[120:123], v[66:81]
	v_mfma_f32_32x32x16_f16 v[50:65], v[98:101], v[124:127], v[50:65]
	v_mfma_f32_32x32x16_f16 v[34:49], v[102:105], v[116:119], v[34:49]
	v_mfma_f32_32x32x16_f16 v[18:33], v[102:105], v[120:123], v[18:33]
	v_mfma_f32_32x32x16_f16 v[2:17], v[102:105], v[124:127], v[2:17]
	s_waitcnt vmcnt(0)
	s_waitcnt vmcnt(0)
	s_barrier
	ds_read_b128 v[98:101], v112 offset:32768
	ds_read_b128 v[102:105], v129
	ds_read_b128 v[106:109], v112 offset:36864
	ds_read_b128 v[116:119], v130
	ds_read_b128 v[120:123], v131
	ds_read_b128 v[124:127], v128
	s_waitcnt lgkmcnt(4)
	v_mfma_f32_32x32x16_f16 v[82:97], v[98:101], v[102:105], v[82:97]
	s_waitcnt lgkmcnt(2)
	v_mfma_f32_32x32x16_f16 v[66:81], v[98:101], v[116:119], v[66:81]
	s_waitcnt lgkmcnt(1)
	v_mfma_f32_32x32x16_f16 v[50:65], v[98:101], v[120:123], v[50:65]
	v_mfma_f32_32x32x16_f16 v[34:49], v[106:109], v[102:105], v[34:49]
	v_mfma_f32_32x32x16_f16 v[18:33], v[106:109], v[116:119], v[18:33]
	ds_read_b128 v[98:101], v113 offset:32768
	ds_read_b128 v[102:105], v113 offset:36864
	ds_read_b128 v[110:113], v128 offset:4096
	ds_read_b128 v[116:119], v128 offset:8192
	v_mfma_f32_32x32x16_f16 v[2:17], v[106:109], v[120:123], v[2:17]
	s_waitcnt lgkmcnt(3)
	v_mfma_f32_32x32x16_f16 v[82:97], v[98:101], v[124:127], v[82:97]
	s_waitcnt lgkmcnt(1)
	v_mfma_f32_32x32x16_f16 v[66:81], v[98:101], v[110:113], v[66:81]
	s_waitcnt lgkmcnt(0)
	v_mfma_f32_32x32x16_f16 v[50:65], v[98:101], v[116:119], v[50:65]
	v_mfma_f32_32x32x16_f16 v[34:49], v[102:105], v[124:127], v[34:49]
	v_mfma_f32_32x32x16_f16 v[18:33], v[102:105], v[110:113], v[18:33]
	ds_read_b128 v[98:101], v114 offset:32768
	ds_read_b128 v[106:109], v114 offset:36864
	ds_read_b128 v[110:113], v132
	ds_read_b128 v[120:123], v132 offset:4096
	ds_read_b128 v[124:127], v132 offset:8192
	v_mfma_f32_32x32x16_f16 v[2:17], v[102:105], v[116:119], v[2:17]
	s_waitcnt lgkmcnt(2)
	v_mfma_f32_32x32x16_f16 v[82:97], v[98:101], v[110:113], v[82:97]
	s_waitcnt lgkmcnt(1)
	v_mfma_f32_32x32x16_f16 v[66:81], v[98:101], v[120:123], v[66:81]
	s_waitcnt lgkmcnt(0)
	v_mfma_f32_32x32x16_f16 v[50:65], v[98:101], v[124:127], v[50:65]
	v_mfma_f32_32x32x16_f16 v[34:49], v[106:109], v[110:113], v[34:49]
	v_mfma_f32_32x32x16_f16 v[18:33], v[106:109], v[120:123], v[18:33]
	ds_read_b128 v[98:101], v115 offset:32768
	ds_read_b128 v[102:105], v115 offset:36864
	ds_read_b128 v[110:113], v133
	ds_read_b128 v[114:117], v133 offset:4096
	ds_read_b128 v[118:121], v133 offset:8192
	v_mfma_f32_32x32x16_f16 v[2:17], v[106:109], v[124:127], v[2:17]
	s_waitcnt lgkmcnt(2)
	v_mfma_f32_32x32x16_f16 v[82:97], v[98:101], v[110:113], v[82:97]
	s_waitcnt lgkmcnt(1)
	v_mfma_f32_32x32x16_f16 v[66:81], v[98:101], v[114:117], v[66:81]
	s_waitcnt lgkmcnt(0)
	v_mfma_f32_32x32x16_f16 v[50:65], v[98:101], v[118:121], v[50:65]
	v_mfma_f32_32x32x16_f16 v[34:49], v[102:105], v[110:113], v[34:49]
	v_mfma_f32_32x32x16_f16 v[18:33], v[102:105], v[114:117], v[18:33]
	v_mfma_f32_32x32x16_f16 v[2:17], v[102:105], v[118:121], v[2:17]
	v_add_u32_e32 v158, s20, v151
	v_and_b32_e32 v154, 32, v0
	v_mov_b32_e32 v155, v147
	v_lshl_add_u64 v[98:99], s[6:7], 0, v[154:155]
	v_or_b32_e32 v100, v158, v156
	v_lshlrev_b32_e32 v146, 2, v158
	v_lshlrev_b32_e32 v100, 2, v100
	v_lshl_add_u64 v[102:103], v[98:99], 0, v[146:147]
	s_waitcnt vmcnt(0)
	s_barrier
	global_load_dwordx4 v[138:141], v[102:103], off offset:16
	global_load_dwordx4 v[134:137], v[102:103], off offset:64
	global_load_dwordx4 v[130:133], v[102:103], off offset:80
	global_load_dwordx4 v[126:129], v[102:103], off offset:128
	global_load_dwordx4 v[122:125], v[102:103], off offset:144
	global_load_dwordx4 v[118:121], v[102:103], off offset:192
	global_load_dword v152, v100, s[6:7]
	global_load_dwordx4 v[142:145], v[102:103], off
	global_load_dword v150, v100, s[6:7] offset:128
	global_load_dword v148, v100, s[6:7] offset:256
	global_load_dwordx4 v[114:117], v[102:103], off offset:208
	global_load_dwordx4 v[110:113], v[102:103], off offset:256
	s_nop 0
	global_load_dwordx4 v[98:101], v[102:103], off offset:336
	global_load_dwordx4 v[106:109], v[102:103], off offset:272
	s_nop 0
	global_load_dwordx4 v[102:105], v[102:103], off offset:320
	v_mul_u32_u24_e32 v146, 0x1200, v149
	v_mov_b32_e32 v155, 0x1c0
	s_movk_i32 s18, 0x1200
	v_lshl_or_b32 v146, v156, 2, v146
	s_bfe_u32 s6, s3, 0x30009
	v_bitop3_b32 v155, s3, v155, v157 bitop3:0xc8
	v_mul_u32_u24_e32 v156, 0x90, v156
	s_movk_i32 s3, 0x240
	v_mad_u32_u24 v156, v149, s18, v156
	v_mad_u32_u24 v149, v153, s3, v146
	v_mul_u32_u24_e64 v157, s6, 12
	s_cmpk_gt_u32 s2, 0x7f
	ds_write2_b32 v149, v82, v83 offset1:36
	ds_write2_b32 v149, v84, v85 offset0:72 offset1:108
	v_add_u32_e32 v153, 0x400, v149
	v_lshrrev_b32_e32 v83, 6, v158
	s_cselect_b64 s[16:17], -1, 0
	s_and_b64 s[6:7], s[4:5], exec
	ds_write2_b32 v153, v86, v87 offset0:32 offset1:68
	ds_write2_b32 v153, v88, v89 offset0:104 offset1:140
	v_add_u32_e32 v86, 0x800, v149
	v_and_b32_e32 v89, 32, v151
	v_add_lshl_u32 v146, v83, v157, 15
	s_cselect_b32 s7, s11, s13
	s_cselect_b32 s6, s10, s12
	v_mov_b32_e32 v159, 0x3e000000
	ds_write2_b32 v86, v90, v91 offset0:64 offset1:100
	ds_write2_b32 v86, v92, v93 offset0:136 offset1:172
	v_add_u32_e32 v82, 0xc00, v149
	s_mov_b64 s[10:11], -1
	s_and_b64 vcc, exec, s[16:17]
	v_lshl_add_u64 v[84:85], v[146:147], 1, s[14:15]
	v_lshlrev_b32_e32 v83, 1, v89
	v_lshlrev_b32_e32 v91, 3, v155
	ds_write2_b32 v82, v94, v95 offset0:96 offset1:132
	ds_write2_b32 v82, v96, v97 offset0:168 offset1:204
	s_cbranch_vccz .LBB11_3
	ds_read2_b32 v[92:93], v149 offset1:36
	ds_read2_b32 v[94:95], v149 offset0:72 offset1:108
	ds_read2_b32 v[96:97], v153 offset0:32 offset1:68
	ds_read2_b32 v[160:161], v153 offset0:104 offset1:140
	s_mov_b64 s[10:11], 0
	s_waitcnt vmcnt(8) lgkmcnt(3)
	v_add_f32_e32 v87, v152, v92
	v_cvt_f16_f32_e32 v87, v87
	v_mov_b32_e32 v92, v93
	s_waitcnt lgkmcnt(2)
	v_mov_b32_e32 v93, v94
	v_mov_b32_e32 v94, v95
	v_pk_add_f32 v[92:93], v[152:153], v[92:93] op_sel_hi:[0,1]
	s_waitcnt lgkmcnt(1)
	v_mov_b32_e32 v95, v96
	v_cvt_pk_f16_f32 v88, v92, v93
	v_pk_add_f32 v[94:95], v[152:153], v[94:95] op_sel_hi:[0,1]
	v_pack_b32_f16 v92, v87, v88
	v_cvt_pk_f16_f32 v87, v94, v95
	v_mov_b32_e32 v94, v97
	s_waitcnt lgkmcnt(0)
	v_mov_b32_e32 v95, v160
	v_alignbit_b32 v93, v87, v88, 16
	v_add_f32_e32 v88, v152, v161
	v_pk_add_f32 v[94:95], v[152:153], v[94:95] op_sel_hi:[0,1]
	v_cvt_f16_f32_e32 v88, v88
	v_cvt_pk_f16_f32 v90, v94, v95
	ds_read2_b32 v[160:161], v86 offset0:64 offset1:100
	v_alignbit_b32 v94, v90, v87, 16
	v_or3_b32 v87, v83, v91, v1
	v_lshlrev_b32_e32 v96, 4, v87
	ds_read2_b32 v[86:87], v86 offset0:136 offset1:172
	v_mov_b32_e32 v97, v147
	v_alignbit_b32 v95, v88, v90, 16
	v_lshl_add_u64 v[162:163], v[84:85], 0, v[96:97]
	global_store_dwordx4 v[162:163], v[92:95], off sc1
	s_waitcnt lgkmcnt(1)
	v_add_f32_e32 v88, v152, v160
	ds_read2_b32 v[94:95], v82 offset0:96 offset1:132
	v_mov_b32_e32 v92, v161
	ds_read2_b32 v[160:161], v82 offset0:168 offset1:204
	v_cvt_f16_f32_e32 v88, v88
	s_waitcnt lgkmcnt(2)
	v_mov_b32_e32 v93, v86
	v_pk_add_f32 v[92:93], v[152:153], v[92:93] op_sel_hi:[0,1]
	v_cvt_pk_f16_f32 v90, v92, v93
	v_pack_b32_f16 v92, v88, v90
	v_mov_b32_e32 v86, v87
	s_waitcnt lgkmcnt(1)
	v_mov_b32_e32 v87, v94
	s_waitcnt lgkmcnt(0)
	v_add_f32_e32 v88, v152, v161
	v_pk_add_f32 v[86:87], v[152:153], v[86:87] op_sel_hi:[0,1]
	v_cvt_f16_f32_e32 v88, v88
	v_cvt_pk_f16_f32 v82, v86, v87
	v_mov_b32_e32 v86, v95
	v_mov_b32_e32 v87, v160
	v_pk_add_f32 v[86:87], v[152:153], v[86:87] op_sel_hi:[0,1]
	v_cvt_pk_f16_f32 v86, v86, v87
	v_alignbit_b32 v94, v86, v82, 16
	v_alignbit_b32 v95, v88, v86, 16
	v_or_b32_e32 v86, 0x800, v96
	v_mov_b32_e32 v87, v147
	v_alignbit_b32 v93, v82, v90, 16
	v_lshl_add_u64 v[86:87], v[84:85], 0, v[86:87]
	global_store_dwordx4 v[86:87], v[92:95], off sc1
.LBB11_3:
	v_cndmask_b32_e64 v82, 1.0, v159, s[4:5]
	s_nop 0
	v_lshrrev_b32_e32 v92, 3, v155
	s_andn2_b64 vcc, exec, s[10:11]
	v_add_u32_e32 v88, v156, v154
	v_lshl_add_u64 v[86:87], v[146:147], 1, s[6:7]
	v_lshrrev_b32_e32 v90, 4, v89
	v_lshlrev_b32_e32 v89, 4, v1
	s_cbranch_vccnz .LBB11_5
	ds_read_b128 v[94:97], v88
	ds_read_b128 v[160:163], v88 offset:16
	v_or_b32_e32 v93, v92, v90
	s_waitcnt vmcnt(7) lgkmcnt(1)
	v_pk_add_f32 v[94:95], v[94:95], v[142:143]
	v_pk_add_f32 v[96:97], v[96:97], v[144:145]
	v_pk_mul_f32 v[94:95], v[82:83], v[94:95] op_sel_hi:[0,1]
	v_pk_mul_f32 v[96:97], v[82:83], v[96:97] op_sel_hi:[0,1]
	v_cvt_pk_f16_f32 v94, v94, v95
	v_cvt_pk_f16_f32 v95, v96, v97
	s_waitcnt lgkmcnt(0)
	v_pk_add_f32 v[96:97], v[160:161], v[138:139]
	v_pk_add_f32 v[146:147], v[162:163], v[140:141]
	v_pk_mul_f32 v[96:97], v[82:83], v[96:97] op_sel_hi:[0,1]
	v_pk_mul_f32 v[146:147], v[82:83], v[146:147] op_sel_hi:[0,1]
	v_cvt_pk_f16_f32 v96, v96, v97
	v_cvt_pk_f16_f32 v97, v146, v147
	v_lshl_or_b32 v146, v93, 10, v89
	v_mov_b32_e32 v147, 0
	v_lshl_add_u64 v[146:147], v[86:87], 0, v[146:147]
	ds_read_b128 v[160:163], v88 offset:64
	global_store_dwordx4 v[146:147], v[94:97], off sc1
	ds_read_b128 v[94:97], v88 offset:80
	s_waitcnt lgkmcnt(1)
	v_pk_add_f32 v[160:161], v[160:161], v[134:135]
	v_pk_add_f32 v[162:163], v[162:163], v[136:137]
	s_waitcnt lgkmcnt(0)
	v_pk_add_f32 v[94:95], v[94:95], v[130:131]
	v_pk_mul_f32 v[160:161], v[82:83], v[160:161] op_sel_hi:[0,1]
	v_pk_mul_f32 v[162:163], v[82:83], v[162:163] op_sel_hi:[0,1]
	v_pk_mul_f32 v[94:95], v[82:83], v[94:95] op_sel_hi:[0,1]
	v_cvt_pk_f16_f32 v160, v160, v161
	v_cvt_pk_f16_f32 v161, v162, v163
	v_cvt_pk_f16_f32 v162, v94, v95
	v_pk_add_f32 v[94:95], v[96:97], v[132:133]
	s_nop 0
	v_pk_mul_f32 v[94:95], v[82:83], v[94:95] op_sel_hi:[0,1]
	v_cvt_pk_f16_f32 v163, v94, v95
	global_store_dwordx4 v[146:147], v[160:163], off offset:1024 sc1
.LBB11_5:
	v_add_u32_e32 v94, 32, v158
	ds_write2_b32 v149, v66, v67 offset1:36
	ds_write2_b32 v149, v68, v69 offset0:72 offset1:108
	v_lshrrev_b32_e32 v66, 6, v94
	v_add_u32_e32 v93, 0x400, v149
	v_and_b32_e32 v69, 32, v94
	v_add_lshl_u32 v66, v66, v157, 15
	v_cndmask_b32_e64 v68, 0, 1, s[16:17]
	ds_write2_b32 v93, v70, v71 offset0:32 offset1:68
	ds_write2_b32 v93, v72, v73 offset0:104 offset1:140
	v_add_u32_e32 v71, 0x800, v149
	v_add_u32_e32 v70, 0xc00, v149
	v_mov_b32_e32 v67, 0
	s_mov_b64 s[10:11], -1
	v_cmp_ne_u32_e64 s[4:5], 1, v68
	s_andn2_b64 vcc, exec, s[16:17]
	v_lshlrev_b32_e32 v66, 1, v66
	v_lshlrev_b32_e32 v68, 1, v69
	ds_write2_b32 v71, v74, v75 offset0:64 offset1:100
	ds_write2_b32 v71, v76, v77 offset0:136 offset1:172
	ds_write2_b32 v70, v78, v79 offset0:96 offset1:132
	ds_write2_b32 v70, v80, v81 offset0:168 offset1:204
	s_cbranch_vccnz .LBB11_7
	ds_read2_b32 v[72:73], v149 offset1:36
	ds_read2_b32 v[74:75], v149 offset0:72 offset1:108
	ds_read2_b32 v[78:79], v93 offset0:32 offset1:68
	ds_read2_b32 v[96:97], v71 offset0:136 offset1:172
	v_lshl_add_u64 v[76:77], s[14:15], 0, v[66:67]
	s_mov_b64 s[10:11], 0
	s_waitcnt vmcnt(6) lgkmcnt(3)
	v_add_f32_e32 v80, v150, v72
	v_cvt_f16_f32_e32 v80, v80
	v_mov_b32_e32 v72, v73
	s_waitcnt lgkmcnt(2)
	v_mov_b32_e32 v73, v74
	v_pk_add_f32 v[72:73], v[150:151], v[72:73] op_sel_hi:[0,1]
	v_cvt_pk_f16_f32 v73, v72, v73
	v_pack_b32_f16 v72, v80, v73
	ds_read2_b32 v[80:81], v93 offset0:104 offset1:140
	v_mov_b32_e32 v74, v75
	s_waitcnt lgkmcnt(2)
	v_mov_b32_e32 v75, v78
	v_pk_add_f32 v[74:75], v[150:151], v[74:75] op_sel_hi:[0,1]
	v_cvt_pk_f16_f32 v78, v74, v75
	v_mov_b32_e32 v74, v79
	s_waitcnt lgkmcnt(0)
	v_mov_b32_e32 v75, v80
	v_add_f32_e32 v79, v150, v81
	ds_read2_b32 v[80:81], v71 offset0:64 offset1:100
	v_cvt_f16_f32_e32 v79, v79
	v_pk_add_f32 v[74:75], v[150:151], v[74:75] op_sel_hi:[0,1]
	v_cvt_pk_f16_f32 v75, v74, v75
	v_alignbit_b32 v73, v78, v73, 16
	v_alignbit_b32 v74, v75, v78, 16
	v_or3_b32 v78, v68, v91, v1
	v_alignbit_b32 v75, v79, v75, 16
	v_lshlrev_b32_e32 v78, 4, v78
	v_mov_b32_e32 v79, v67
	s_waitcnt lgkmcnt(0)
	v_add_f32_e32 v71, v150, v80
	v_lshl_add_u64 v[94:95], v[76:77], 0, v[78:79]
	v_cvt_f16_f32_e32 v71, v71
	global_store_dwordx4 v[94:95], v[72:75], off sc1
	ds_read2_b32 v[74:75], v70 offset0:96 offset1:132
	v_mov_b32_e32 v80, v97
	v_mov_b32_e32 v72, v81
	v_mov_b32_e32 v73, v96
	v_pk_add_f32 v[72:73], v[150:151], v[72:73] op_sel_hi:[0,1]
	v_cvt_pk_f16_f32 v73, v72, v73
	v_pack_b32_f16 v72, v71, v73
	ds_read2_b32 v[70:71], v70 offset0:168 offset1:204
	s_waitcnt lgkmcnt(1)
	v_mov_b32_e32 v81, v74
	v_pk_add_f32 v[80:81], v[150:151], v[80:81] op_sel_hi:[0,1]
	v_mov_b32_e32 v74, v75
	v_cvt_pk_f16_f32 v79, v80, v81
	s_waitcnt lgkmcnt(0)
	v_mov_b32_e32 v75, v70
	v_add_f32_e32 v70, v150, v71
	v_cvt_f16_f32_e32 v80, v70
	v_pk_add_f32 v[70:71], v[150:151], v[74:75] op_sel_hi:[0,1]
	v_cvt_pk_f16_f32 v70, v70, v71
	v_alignbit_b32 v74, v70, v79, 16
	v_alignbit_b32 v75, v80, v70, 16
	v_or_b32_e32 v70, 0x800, v78
	v_mov_b32_e32 v71, v67
	v_alignbit_b32 v73, v79, v73, 16
	v_lshl_add_u64 v[70:71], v[76:77], 0, v[70:71]
	global_store_dwordx4 v[70:71], v[72:75], off sc1
.LBB11_7:
	s_andn2_b64 vcc, exec, s[10:11]
	v_lshrrev_b32_e32 v69, 4, v69
	s_cbranch_vccnz .LBB11_9
	ds_read_b128 v[70:73], v88
	ds_read_b128 v[74:77], v88 offset:16
	v_mov_b32_e32 v67, 0
	v_or_b32_e32 v80, v92, v69
	v_lshl_add_u64 v[78:79], s[6:7], 0, v[66:67]
	s_waitcnt vmcnt(11) lgkmcnt(1)
	v_pk_add_f32 v[70:71], v[70:71], v[126:127]
	v_pk_add_f32 v[72:73], v[72:73], v[128:129]
	v_pk_mul_f32 v[70:71], v[82:83], v[70:71] op_sel_hi:[0,1]
	v_pk_mul_f32 v[72:73], v[82:83], v[72:73] op_sel_hi:[0,1]
	v_cvt_pk_f16_f32 v70, v70, v71
	v_cvt_pk_f16_f32 v71, v72, v73
	s_waitcnt vmcnt(10) lgkmcnt(0)
	v_pk_add_f32 v[72:73], v[74:75], v[122:123]
	v_pk_add_f32 v[74:75], v[76:77], v[124:125]
	v_pk_mul_f32 v[72:73], v[82:83], v[72:73] op_sel_hi:[0,1]
	v_pk_mul_f32 v[74:75], v[82:83], v[74:75] op_sel_hi:[0,1]
	v_lshl_or_b32 v80, v80, 10, v89
	v_mov_b32_e32 v81, v67
	v_cvt_pk_f16_f32 v72, v72, v73
	v_cvt_pk_f16_f32 v73, v74, v75
	v_lshl_add_u64 v[78:79], v[78:79], 0, v[80:81]
	ds_read_b128 v[74:77], v88 offset:64
	global_store_dwordx4 v[78:79], v[70:73], off sc1
	ds_read_b128 v[70:73], v88 offset:80
	s_waitcnt vmcnt(10) lgkmcnt(1)
	v_pk_add_f32 v[74:75], v[74:75], v[118:119]
	v_pk_add_f32 v[76:77], v[76:77], v[120:121]
	s_waitcnt vmcnt(5) lgkmcnt(0)
	v_pk_add_f32 v[70:71], v[70:71], v[114:115]
	v_pk_mul_f32 v[74:75], v[82:83], v[74:75] op_sel_hi:[0,1]
	v_pk_mul_f32 v[76:77], v[82:83], v[76:77] op_sel_hi:[0,1]
	v_pk_mul_f32 v[70:71], v[82:83], v[70:71] op_sel_hi:[0,1]
	v_cvt_pk_f16_f32 v74, v74, v75
	v_cvt_pk_f16_f32 v75, v76, v77
	v_cvt_pk_f16_f32 v76, v70, v71
	v_pk_add_f32 v[70:71], v[72:73], v[116:117]
	s_nop 0
	v_pk_mul_f32 v[70:71], v[82:83], v[70:71] op_sel_hi:[0,1]
	v_cvt_pk_f16_f32 v77, v70, v71
	global_store_dwordx4 v[78:79], v[74:77], off offset:1024 sc1
.LBB11_9:
	v_add_u32_e32 v70, 64, v158
	ds_write2_b32 v149, v50, v51 offset1:36
	ds_write2_b32 v149, v52, v53 offset0:72 offset1:108
	v_lshrrev_b32_e32 v50, 6, v70
	v_add_lshl_u32 v50, v50, v157, 15
	v_add_u32_e32 v67, 0x400, v149
	v_add_u32_e32 v53, 0x800, v149
	v_add_u32_e32 v52, 0xc00, v149
	v_mov_b32_e32 v51, 0
	s_mov_b64 s[10:11], -1
	s_and_b64 vcc, exec, s[4:5]
	v_lshlrev_b32_e32 v50, 1, v50
	ds_write2_b32 v67, v54, v55 offset0:32 offset1:68
	ds_write2_b32 v67, v56, v57 offset0:104 offset1:140
	ds_write2_b32 v53, v58, v59 offset0:64 offset1:100
	ds_write2_b32 v53, v60, v61 offset0:136 offset1:172
	ds_write2_b32 v52, v62, v63 offset0:96 offset1:132
	ds_write2_b32 v52, v64, v65 offset0:168 offset1:204
	s_cbranch_vccnz .LBB11_11
	ds_read2_b32 v[54:55], v149 offset1:36
	ds_read2_b32 v[56:57], v149 offset0:72 offset1:108
	ds_read2_b32 v[60:61], v67 offset0:32 offset1:68
	ds_read2_b32 v[70:71], v53 offset0:136 offset1:172
	v_lshl_add_u64 v[58:59], s[14:15], 0, v[50:51]
	s_mov_b64 s[10:11], 0
	s_waitcnt vmcnt(5) lgkmcnt(3)
	v_add_f32_e32 v62, v148, v54
	v_cvt_f16_f32_e32 v62, v62
	v_mov_b32_e32 v54, v55
	s_waitcnt lgkmcnt(2)
	v_mov_b32_e32 v55, v56
	v_pk_add_f32 v[54:55], v[148:149], v[54:55] op_sel_hi:[0,1]
	v_cvt_pk_f16_f32 v55, v54, v55
	v_pack_b32_f16 v54, v62, v55
	ds_read2_b32 v[62:63], v67 offset0:104 offset1:140
	v_mov_b32_e32 v56, v57
	s_waitcnt lgkmcnt(2)
	v_mov_b32_e32 v57, v60
	v_pk_add_f32 v[56:57], v[148:149], v[56:57] op_sel_hi:[0,1]
	v_cvt_pk_f16_f32 v60, v56, v57
	v_mov_b32_e32 v56, v61
	s_waitcnt lgkmcnt(0)
	v_mov_b32_e32 v57, v62
	v_add_f32_e32 v61, v148, v63
	ds_read2_b32 v[62:63], v53 offset0:64 offset1:100
	v_cvt_f16_f32_e32 v61, v61
	v_pk_add_f32 v[56:57], v[148:149], v[56:57] op_sel_hi:[0,1]
	v_cvt_pk_f16_f32 v57, v56, v57
	v_alignbit_b32 v55, v60, v55, 16
	v_alignbit_b32 v56, v57, v60, 16
	v_or3_b32 v60, v83, v91, v1
	v_alignbit_b32 v57, v61, v57, 16
	v_lshlrev_b32_e32 v60, 4, v60
	v_mov_b32_e32 v61, v51
	s_waitcnt lgkmcnt(0)
	v_add_f32_e32 v53, v148, v62
	v_lshl_add_u64 v[64:65], v[58:59], 0, v[60:61]
	v_cvt_f16_f32_e32 v53, v53
	global_store_dwordx4 v[64:65], v[54:57], off sc1
	ds_read2_b32 v[56:57], v52 offset0:96 offset1:132
	v_mov_b32_e32 v62, v71
	v_mov_b32_e32 v54, v63
	v_mov_b32_e32 v55, v70
	v_pk_add_f32 v[54:55], v[148:149], v[54:55] op_sel_hi:[0,1]
	v_cvt_pk_f16_f32 v55, v54, v55
	v_pack_b32_f16 v54, v53, v55
	ds_read2_b32 v[52:53], v52 offset0:168 offset1:204
	s_waitcnt lgkmcnt(1)
	v_mov_b32_e32 v63, v56
	v_pk_add_f32 v[62:63], v[148:149], v[62:63] op_sel_hi:[0,1]
	v_mov_b32_e32 v56, v57
	v_cvt_pk_f16_f32 v61, v62, v63
	s_waitcnt lgkmcnt(0)
	v_mov_b32_e32 v57, v52
	v_add_f32_e32 v52, v148, v53
	v_cvt_f16_f32_e32 v62, v52
	v_pk_add_f32 v[52:53], v[148:149], v[56:57] op_sel_hi:[0,1]
	v_cvt_pk_f16_f32 v52, v52, v53
	v_alignbit_b32 v56, v52, v61, 16
	v_alignbit_b32 v57, v62, v52, 16
	v_or_b32_e32 v52, 0x800, v60
	v_mov_b32_e32 v53, v51
	v_alignbit_b32 v55, v61, v55, 16
	v_lshl_add_u64 v[52:53], v[58:59], 0, v[52:53]
	global_store_dwordx4 v[52:53], v[54:57], off sc1
.LBB11_11:
	s_andn2_b64 vcc, exec, s[10:11]
	s_cbranch_vccnz .LBB11_13
	ds_read_b128 v[52:55], v88
	ds_read_b128 v[56:59], v88 offset:16
	v_mov_b32_e32 v51, 0
	v_or_b32_e32 v62, v92, v90
	v_lshl_add_u64 v[60:61], s[6:7], 0, v[50:51]
	s_waitcnt vmcnt(3) lgkmcnt(1)
	v_pk_add_f32 v[52:53], v[52:53], v[110:111]
	v_pk_add_f32 v[54:55], v[54:55], v[112:113]
	v_pk_mul_f32 v[52:53], v[82:83], v[52:53] op_sel_hi:[0,1]
	v_pk_mul_f32 v[54:55], v[82:83], v[54:55] op_sel_hi:[0,1]
	v_cvt_pk_f16_f32 v52, v52, v53
	v_cvt_pk_f16_f32 v53, v54, v55
	s_waitcnt vmcnt(1) lgkmcnt(0)
	v_pk_add_f32 v[54:55], v[56:57], v[106:107]
	v_pk_add_f32 v[56:57], v[58:59], v[108:109]
	v_pk_mul_f32 v[54:55], v[82:83], v[54:55] op_sel_hi:[0,1]
	v_pk_mul_f32 v[56:57], v[82:83], v[56:57] op_sel_hi:[0,1]
	v_lshl_or_b32 v62, v62, 10, v89
	v_mov_b32_e32 v63, v51
	v_cvt_pk_f16_f32 v54, v54, v55
	v_cvt_pk_f16_f32 v55, v56, v57
	v_lshl_add_u64 v[60:61], v[60:61], 0, v[62:63]
	ds_read_b128 v[56:59], v88 offset:64
	global_store_dwordx4 v[60:61], v[52:55], off sc1
	ds_read_b128 v[52:55], v88 offset:80
	s_waitcnt vmcnt(1) lgkmcnt(1)
	v_pk_add_f32 v[56:57], v[56:57], v[102:103]
	v_pk_add_f32 v[58:59], v[58:59], v[104:105]
	s_waitcnt lgkmcnt(0)
	v_pk_add_f32 v[52:53], v[52:53], v[98:99]
	v_pk_mul_f32 v[56:57], v[82:83], v[56:57] op_sel_hi:[0,1]
	v_pk_mul_f32 v[58:59], v[82:83], v[58:59] op_sel_hi:[0,1]
	v_pk_mul_f32 v[52:53], v[82:83], v[52:53] op_sel_hi:[0,1]
	v_cvt_pk_f16_f32 v56, v56, v57
	v_cvt_pk_f16_f32 v57, v58, v59
	v_cvt_pk_f16_f32 v58, v52, v53
	v_pk_add_f32 v[52:53], v[54:55], v[100:101]
	s_nop 0
	v_pk_mul_f32 v[52:53], v[82:83], v[52:53] op_sel_hi:[0,1]
	v_cvt_pk_f16_f32 v59, v52, v53
	global_store_dwordx4 v[60:61], v[56:59], off offset:1024 sc1
.LBB11_13:
	v_or_b32_e32 v51, 32, v155
	ds_write2_b32 v149, v34, v35 offset1:36
	ds_write2_b32 v149, v36, v37 offset0:72 offset1:108
	v_add_u32_e32 v37, 0x400, v149
	v_add_u32_e32 v36, 0x800, v149
	v_add_u32_e32 v35, 0xc00, v149
	s_mov_b64 s[10:11], -1
	s_and_b64 vcc, exec, s[4:5]
	v_lshlrev_b32_e32 v34, 3, v51
	ds_write2_b32 v37, v38, v39 offset0:32 offset1:68
	ds_write2_b32 v37, v40, v41 offset0:104 offset1:140
	ds_write2_b32 v36, v42, v43 offset0:64 offset1:100
	ds_write2_b32 v36, v44, v45 offset0:136 offset1:172
	ds_write2_b32 v35, v46, v47 offset0:96 offset1:132
	ds_write2_b32 v35, v48, v49 offset0:168 offset1:204
	s_cbranch_vccnz .LBB11_15
	ds_read2_b32 v[38:39], v149 offset1:36
	ds_read2_b32 v[40:41], v149 offset0:72 offset1:108
	ds_read2_b32 v[42:43], v37 offset0:32 offset1:68
	s_mov_b64 s[10:11], 0
	s_waitcnt vmcnt(8) lgkmcnt(2)
	v_add_f32_e32 v44, v152, v38
	v_cvt_f16_f32_e32 v44, v44
	v_mov_b32_e32 v38, v39
	s_waitcnt lgkmcnt(1)
	v_mov_b32_e32 v39, v40
	v_pk_add_f32 v[38:39], v[152:153], v[38:39] op_sel_hi:[0,1]
	v_cvt_pk_f16_f32 v39, v38, v39
	v_pack_b32_f16 v38, v44, v39
	ds_read2_b32 v[44:45], v37 offset0:104 offset1:140
	v_mov_b32_e32 v40, v41
	s_waitcnt lgkmcnt(1)
	v_mov_b32_e32 v41, v42
	v_pk_add_f32 v[40:41], v[152:153], v[40:41] op_sel_hi:[0,1]
	v_cvt_pk_f16_f32 v37, v40, v41
	s_waitcnt lgkmcnt(0)
	v_add_f32_e32 v42, v152, v45
	v_mov_b32_e32 v40, v43
	v_mov_b32_e32 v41, v44
	v_cvt_f16_f32_e32 v42, v42
	v_pk_add_f32 v[40:41], v[152:153], v[40:41] op_sel_hi:[0,1]
	v_cvt_pk_f16_f32 v41, v40, v41
	ds_read2_b32 v[44:45], v36 offset0:64 offset1:100
	v_alignbit_b32 v39, v37, v39, 16
	v_alignbit_b32 v40, v41, v37, 16
	v_or3_b32 v37, v83, v34, v1
	v_alignbit_b32 v41, v42, v41, 16
	v_lshlrev_b32_e32 v42, 4, v37
	ds_read2_b32 v[36:37], v36 offset0:136 offset1:172
	v_mov_b32_e32 v43, 0
	v_lshl_add_u64 v[46:47], v[84:85], 0, v[42:43]
	global_store_dwordx4 v[46:47], v[38:41], off sc1
	ds_read2_b32 v[40:41], v35 offset0:96 offset1:132
	v_or_b32_e32 v42, 0x800, v42
	s_waitcnt lgkmcnt(2)
	v_add_f32_e32 v38, v152, v44
	v_cvt_f16_f32_e32 v44, v38
	v_mov_b32_e32 v38, v45
	s_waitcnt lgkmcnt(1)
	v_mov_b32_e32 v39, v36
	v_pk_add_f32 v[38:39], v[152:153], v[38:39] op_sel_hi:[0,1]
	v_cvt_pk_f16_f32 v46, v38, v39
	v_pack_b32_f16 v36, v44, v46
	ds_read2_b32 v[44:45], v35 offset0:168 offset1:204
	v_mov_b32_e32 v38, v37
	s_waitcnt lgkmcnt(1)
	v_mov_b32_e32 v39, v40
	v_pk_add_f32 v[38:39], v[152:153], v[38:39] op_sel_hi:[0,1]
	v_cvt_pk_f16_f32 v35, v38, v39
	s_waitcnt lgkmcnt(0)
	v_add_f32_e32 v40, v152, v45
	v_cvt_f16_f32_e32 v40, v40
	v_mov_b32_e32 v38, v41
	v_mov_b32_e32 v39, v44
	v_pk_add_f32 v[38:39], v[152:153], v[38:39] op_sel_hi:[0,1]
	v_cvt_pk_f16_f32 v39, v38, v39
	v_alignbit_b32 v37, v35, v46, 16
	v_alignbit_b32 v38, v39, v35, 16
	v_alignbit_b32 v39, v40, v39, 16
	v_lshl_add_u64 v[40:41], v[84:85], 0, v[42:43]
	global_store_dwordx4 v[40:41], v[36:39], off sc1
.LBB11_15:
	s_andn2_b64 vcc, exec, s[10:11]
	v_lshrrev_b32_e32 v35, 3, v51
	s_cbranch_vccnz .LBB11_17
	ds_read_b128 v[36:39], v88
	ds_read_b128 v[40:43], v88 offset:16
	v_or_b32_e32 v44, v35, v90
	v_lshl_or_b32 v44, v44, 10, v89
	v_mov_b32_e32 v45, 0
	s_waitcnt vmcnt(7) lgkmcnt(1)
	v_pk_add_f32 v[36:37], v[36:37], v[142:143]
	v_pk_add_f32 v[38:39], v[38:39], v[144:145]
	v_pk_mul_f32 v[36:37], v[82:83], v[36:37] op_sel_hi:[0,1]
	v_pk_mul_f32 v[38:39], v[82:83], v[38:39] op_sel_hi:[0,1]
	v_cvt_pk_f16_f32 v36, v36, v37
	v_cvt_pk_f16_f32 v37, v38, v39
	s_waitcnt lgkmcnt(0)
	v_pk_add_f32 v[38:39], v[40:41], v[138:139]
	v_pk_add_f32 v[40:41], v[42:43], v[140:141]
	v_pk_mul_f32 v[38:39], v[82:83], v[38:39] op_sel_hi:[0,1]
	v_pk_mul_f32 v[40:41], v[82:83], v[40:41] op_sel_hi:[0,1]
	v_cvt_pk_f16_f32 v38, v38, v39
	v_cvt_pk_f16_f32 v39, v40, v41
	v_lshl_add_u64 v[46:47], v[86:87], 0, v[44:45]
	ds_read_b128 v[40:43], v88 offset:64
	global_store_dwordx4 v[46:47], v[36:39], off sc1
	ds_read_b128 v[36:39], v88 offset:80
	v_or_b32_e32 v44, 0x400, v44
	s_waitcnt lgkmcnt(1)
	v_pk_add_f32 v[40:41], v[40:41], v[134:135]
	v_pk_add_f32 v[42:43], v[42:43], v[136:137]
	s_waitcnt lgkmcnt(0)
	v_pk_add_f32 v[36:37], v[36:37], v[130:131]
	v_pk_mul_f32 v[40:41], v[82:83], v[40:41] op_sel_hi:[0,1]
	v_pk_mul_f32 v[42:43], v[82:83], v[42:43] op_sel_hi:[0,1]
	v_pk_mul_f32 v[36:37], v[82:83], v[36:37] op_sel_hi:[0,1]
	v_cvt_pk_f16_f32 v40, v40, v41
	v_cvt_pk_f16_f32 v41, v42, v43
	v_cvt_pk_f16_f32 v42, v36, v37
	v_pk_add_f32 v[36:37], v[38:39], v[132:133]
	s_nop 0
	v_pk_mul_f32 v[36:37], v[82:83], v[36:37] op_sel_hi:[0,1]
	v_cvt_pk_f16_f32 v43, v36, v37
	v_lshl_add_u64 v[36:37], v[86:87], 0, v[44:45]
	global_store_dwordx4 v[36:37], v[40:43], off sc1
.LBB11_17:
	ds_write2_b32 v149, v18, v19 offset1:36
	ds_write2_b32 v149, v20, v21 offset0:72 offset1:108
	v_add_u32_e32 v20, 0x400, v149
	v_add_u32_e32 v19, 0x800, v149
	v_add_u32_e32 v18, 0xc00, v149
	s_and_b64 vcc, exec, s[4:5]
	s_mov_b64 s[10:11], -1
	ds_write2_b32 v20, v22, v23 offset0:32 offset1:68
	ds_write2_b32 v20, v24, v25 offset0:104 offset1:140
	ds_write2_b32 v19, v26, v27 offset0:64 offset1:100
	ds_write2_b32 v19, v28, v29 offset0:136 offset1:172
	ds_write2_b32 v18, v30, v31 offset0:96 offset1:132
	ds_write2_b32 v18, v32, v33 offset0:168 offset1:204
	s_cbranch_vccnz .LBB11_19
	ds_read2_b32 v[22:23], v149 offset1:36
	ds_read2_b32 v[24:25], v149 offset0:72 offset1:108
	ds_read2_b32 v[28:29], v20 offset0:32 offset1:68
	ds_read2_b32 v[32:33], v19 offset0:136 offset1:172
	v_mov_b32_e32 v67, 0
	s_waitcnt vmcnt(6) lgkmcnt(3)
	v_add_f32_e32 v21, v150, v22
	v_cvt_f16_f32_e32 v21, v21
	v_mov_b32_e32 v22, v23
	s_waitcnt lgkmcnt(2)
	v_mov_b32_e32 v23, v24
	v_pk_add_f32 v[22:23], v[150:151], v[22:23] op_sel_hi:[0,1]
	v_cvt_pk_f16_f32 v23, v22, v23
	v_pack_b32_f16 v22, v21, v23
	ds_read2_b32 v[20:21], v20 offset0:104 offset1:140
	v_mov_b32_e32 v24, v25
	s_waitcnt lgkmcnt(2)
	v_mov_b32_e32 v25, v28
	v_pk_add_f32 v[24:25], v[150:151], v[24:25] op_sel_hi:[0,1]
	v_cvt_pk_f16_f32 v28, v24, v25
	s_waitcnt lgkmcnt(0)
	v_mov_b32_e32 v25, v20
	v_add_f32_e32 v20, v150, v21
	v_mov_b32_e32 v24, v29
	v_cvt_f16_f32_e32 v29, v20
	v_pk_add_f32 v[20:21], v[150:151], v[24:25] op_sel_hi:[0,1]
	v_cvt_pk_f16_f32 v20, v20, v21
	v_alignbit_b32 v24, v20, v28, 16
	v_alignbit_b32 v25, v29, v20, 16
	v_or3_b32 v20, v68, v34, v1
	v_alignbit_b32 v23, v28, v23, 16
	v_lshlrev_b32_e32 v28, 4, v20
	ds_read2_b32 v[20:21], v19 offset0:64 offset1:100
	v_lshl_add_u64 v[26:27], s[14:15], 0, v[66:67]
	v_mov_b32_e32 v29, v67
	v_lshl_add_u64 v[30:31], v[26:27], 0, v[28:29]
	global_store_dwordx4 v[30:31], v[22:25], off sc1
	s_waitcnt lgkmcnt(0)
	v_add_f32_e32 v19, v150, v20
	v_cvt_f16_f32_e32 v19, v19
	v_mov_b32_e32 v20, v21
	v_mov_b32_e32 v21, v32
	v_pk_add_f32 v[20:21], v[150:151], v[20:21] op_sel_hi:[0,1]
	ds_read2_b32 v[22:23], v18 offset0:96 offset1:132
	v_cvt_pk_f16_f32 v21, v20, v21
	v_pack_b32_f16 v20, v19, v21
	ds_read2_b32 v[18:19], v18 offset0:168 offset1:204
	v_mov_b32_e32 v24, v33
	s_waitcnt lgkmcnt(1)
	v_mov_b32_e32 v25, v22
	v_pk_add_f32 v[24:25], v[150:151], v[24:25] op_sel_hi:[0,1]
	v_mov_b32_e32 v22, v23
	s_waitcnt lgkmcnt(0)
	v_mov_b32_e32 v23, v18
	v_add_f32_e32 v18, v150, v19
	v_cvt_pk_f16_f32 v24, v24, v25
	v_cvt_f16_f32_e32 v25, v18
	v_pk_add_f32 v[18:19], v[150:151], v[22:23] op_sel_hi:[0,1]
	v_cvt_pk_f16_f32 v18, v18, v19
	v_alignbit_b32 v22, v18, v24, 16
	v_alignbit_b32 v23, v25, v18, 16
	v_or_b32_e32 v18, 0x800, v28
	v_mov_b32_e32 v19, v67
	v_alignbit_b32 v21, v24, v21, 16
	v_lshl_add_u64 v[18:19], v[26:27], 0, v[18:19]
	s_mov_b64 s[10:11], 0
	global_store_dwordx4 v[18:19], v[20:23], off sc1
.LBB11_19:
	s_andn2_b64 vcc, exec, s[10:11]
	s_cbranch_vccnz .LBB11_21
	ds_read_b128 v[18:21], v88
	ds_read_b128 v[22:25], v88 offset:16
	v_mov_b32_e32 v67, 0
	v_or_b32_e32 v28, v35, v69
	v_lshl_add_u64 v[26:27], s[6:7], 0, v[66:67]
	s_waitcnt vmcnt(11) lgkmcnt(1)
	v_pk_add_f32 v[18:19], v[18:19], v[126:127]
	v_pk_add_f32 v[20:21], v[20:21], v[128:129]
	v_pk_mul_f32 v[18:19], v[82:83], v[18:19] op_sel_hi:[0,1]
	v_pk_mul_f32 v[20:21], v[82:83], v[20:21] op_sel_hi:[0,1]
	v_cvt_pk_f16_f32 v18, v18, v19
	v_cvt_pk_f16_f32 v19, v20, v21
	s_waitcnt vmcnt(10) lgkmcnt(0)
	v_pk_add_f32 v[20:21], v[22:23], v[122:123]
	v_pk_add_f32 v[22:23], v[24:25], v[124:125]
	v_pk_mul_f32 v[20:21], v[82:83], v[20:21] op_sel_hi:[0,1]
	v_pk_mul_f32 v[22:23], v[82:83], v[22:23] op_sel_hi:[0,1]
	v_lshl_or_b32 v66, v28, 10, v89
	v_cvt_pk_f16_f32 v20, v20, v21
	v_cvt_pk_f16_f32 v21, v22, v23
	v_lshl_add_u64 v[28:29], v[26:27], 0, v[66:67]
	ds_read_b128 v[22:25], v88 offset:64
	global_store_dwordx4 v[28:29], v[18:21], off sc1
	ds_read_b128 v[18:21], v88 offset:80
	v_or_b32_e32 v66, 0x400, v66
	s_waitcnt vmcnt(10) lgkmcnt(1)
	v_pk_add_f32 v[22:23], v[22:23], v[118:119]
	v_pk_add_f32 v[24:25], v[24:25], v[120:121]
	s_waitcnt vmcnt(5) lgkmcnt(0)
	v_pk_add_f32 v[18:19], v[18:19], v[114:115]
	v_pk_mul_f32 v[22:23], v[82:83], v[22:23] op_sel_hi:[0,1]
	v_pk_mul_f32 v[24:25], v[82:83], v[24:25] op_sel_hi:[0,1]
	v_pk_mul_f32 v[18:19], v[82:83], v[18:19] op_sel_hi:[0,1]
	v_cvt_pk_f16_f32 v22, v22, v23
	v_cvt_pk_f16_f32 v23, v24, v25
	v_cvt_pk_f16_f32 v24, v18, v19
	v_pk_add_f32 v[18:19], v[20:21], v[116:117]
	s_nop 0
	v_pk_mul_f32 v[18:19], v[82:83], v[18:19] op_sel_hi:[0,1]
	v_cvt_pk_f16_f32 v25, v18, v19
	v_lshl_add_u64 v[18:19], v[26:27], 0, v[66:67]
	global_store_dwordx4 v[18:19], v[22:25], off sc1
.LBB11_21:
	ds_write2_b32 v149, v2, v3 offset1:36
	ds_write2_b32 v149, v4, v5 offset0:72 offset1:108
	v_add_u32_e32 v4, 0x400, v149
	v_add_u32_e32 v3, 0x800, v149
	v_add_u32_e32 v2, 0xc00, v149
	s_and_b64 vcc, exec, s[4:5]
	s_mov_b64 s[4:5], -1
	ds_write2_b32 v4, v6, v7 offset0:32 offset1:68
	ds_write2_b32 v4, v8, v9 offset0:104 offset1:140
	ds_write2_b32 v3, v10, v11 offset0:64 offset1:100
	ds_write2_b32 v3, v12, v13 offset0:136 offset1:172
	ds_write2_b32 v2, v14, v15 offset0:96 offset1:132
	ds_write2_b32 v2, v16, v17 offset0:168 offset1:204
	s_cbranch_vccnz .LBB11_23
	ds_read2_b32 v[6:7], v149 offset1:36
	ds_read2_b32 v[8:9], v149 offset0:72 offset1:108
	ds_read2_b32 v[12:13], v4 offset0:32 offset1:68
	v_mov_b32_e32 v51, 0
	v_or3_b32 v1, v83, v34, v1
	s_waitcnt vmcnt(5) lgkmcnt(2)
	v_add_f32_e32 v5, v148, v6
	v_cvt_f16_f32_e32 v5, v5
	v_mov_b32_e32 v6, v7
	s_waitcnt lgkmcnt(1)
	v_mov_b32_e32 v7, v8
	v_pk_add_f32 v[6:7], v[148:149], v[6:7] op_sel_hi:[0,1]
	v_cvt_pk_f16_f32 v7, v6, v7
	v_pack_b32_f16 v6, v5, v7
	ds_read2_b32 v[4:5], v4 offset0:104 offset1:140
	v_mov_b32_e32 v8, v9
	s_waitcnt lgkmcnt(1)
	v_mov_b32_e32 v9, v12
	v_pk_add_f32 v[8:9], v[148:149], v[8:9] op_sel_hi:[0,1]
	v_cvt_pk_f16_f32 v12, v8, v9
	s_waitcnt lgkmcnt(0)
	v_mov_b32_e32 v9, v4
	v_add_f32_e32 v4, v148, v5
	v_mov_b32_e32 v8, v13
	v_cvt_f16_f32_e32 v13, v4
	v_pk_add_f32 v[4:5], v[148:149], v[8:9] op_sel_hi:[0,1]
	v_cvt_pk_f16_f32 v4, v4, v5
	v_alignbit_b32 v8, v4, v12, 16
	v_alignbit_b32 v9, v13, v4, 16
	ds_read2_b32 v[4:5], v3 offset0:64 offset1:100
	v_lshl_add_u64 v[10:11], s[14:15], 0, v[50:51]
	v_alignbit_b32 v7, v12, v7, 16
	v_lshlrev_b32_e32 v12, 4, v1
	v_mov_b32_e32 v13, v51
	v_lshl_add_u64 v[14:15], v[10:11], 0, v[12:13]
	ds_read2_b32 v[16:17], v3 offset0:136 offset1:172
	global_store_dwordx4 v[14:15], v[6:9], off sc1
	ds_read2_b32 v[6:7], v2 offset0:96 offset1:132
	ds_read2_b32 v[2:3], v2 offset0:168 offset1:204
	s_waitcnt lgkmcnt(3)
	v_add_f32_e32 v1, v148, v4
	v_cvt_f16_f32_e32 v1, v1
	v_mov_b32_e32 v4, v5
	s_waitcnt lgkmcnt(2)
	v_mov_b32_e32 v5, v16
	v_pk_add_f32 v[4:5], v[148:149], v[4:5] op_sel_hi:[0,1]
	v_mov_b32_e32 v8, v17
	s_waitcnt lgkmcnt(1)
	v_mov_b32_e32 v9, v6
	v_cvt_pk_f16_f32 v5, v4, v5
	v_pk_add_f32 v[8:9], v[148:149], v[8:9] op_sel_hi:[0,1]
	v_mov_b32_e32 v6, v7
	s_waitcnt lgkmcnt(0)
	v_mov_b32_e32 v7, v2
	v_add_f32_e32 v2, v148, v3
	v_pack_b32_f16 v4, v1, v5
	v_cvt_pk_f16_f32 v1, v8, v9
	v_cvt_f16_f32_e32 v8, v2
	v_pk_add_f32 v[2:3], v[148:149], v[6:7] op_sel_hi:[0,1]
	v_cvt_pk_f16_f32 v2, v2, v3
	v_alignbit_b32 v6, v2, v1, 16
	v_alignbit_b32 v7, v8, v2, 16
	v_or_b32_e32 v2, 0x800, v12
	v_mov_b32_e32 v3, v51
	v_alignbit_b32 v5, v1, v5, 16
	v_lshl_add_u64 v[2:3], v[10:11], 0, v[2:3]
	s_mov_b64 s[4:5], 0
	global_store_dwordx4 v[2:3], v[4:7], off sc1
.LBB11_23:
	s_andn2_b64 vcc, exec, s[4:5]
	s_cbranch_vccnz .LBB11_25
	ds_read_b128 v[2:5], v88
	ds_read_b128 v[6:9], v88 offset:16
	v_mov_b32_e32 v51, 0
	v_or_b32_e32 v1, v35, v90
	v_lshl_add_u64 v[10:11], s[6:7], 0, v[50:51]
	s_waitcnt vmcnt(3) lgkmcnt(1)
	v_pk_add_f32 v[2:3], v[2:3], v[110:111]
	v_pk_add_f32 v[4:5], v[4:5], v[112:113]
	v_pk_mul_f32 v[2:3], v[82:83], v[2:3] op_sel_hi:[0,1]
	v_pk_mul_f32 v[4:5], v[82:83], v[4:5] op_sel_hi:[0,1]
	v_cvt_pk_f16_f32 v2, v2, v3
	v_cvt_pk_f16_f32 v3, v4, v5
	s_waitcnt vmcnt(1) lgkmcnt(0)
	v_pk_add_f32 v[4:5], v[6:7], v[106:107]
	v_pk_add_f32 v[6:7], v[8:9], v[108:109]
	v_pk_mul_f32 v[4:5], v[82:83], v[4:5] op_sel_hi:[0,1]
	v_pk_mul_f32 v[6:7], v[82:83], v[6:7] op_sel_hi:[0,1]
	v_lshl_or_b32 v50, v1, 10, v89
	v_cvt_pk_f16_f32 v4, v4, v5
	v_cvt_pk_f16_f32 v5, v6, v7
	v_lshl_add_u64 v[12:13], v[10:11], 0, v[50:51]
	ds_read_b128 v[6:9], v88 offset:64
	global_store_dwordx4 v[12:13], v[2:5], off sc1
	ds_read_b128 v[2:5], v88 offset:80
	v_or_b32_e32 v50, 0x400, v50
	s_waitcnt vmcnt(1) lgkmcnt(1)
	v_pk_add_f32 v[6:7], v[6:7], v[102:103]
	v_pk_add_f32 v[8:9], v[8:9], v[104:105]
	s_waitcnt lgkmcnt(0)
	v_pk_add_f32 v[2:3], v[2:3], v[98:99]
	v_pk_mul_f32 v[6:7], v[82:83], v[6:7] op_sel_hi:[0,1]
	v_pk_mul_f32 v[8:9], v[82:83], v[8:9] op_sel_hi:[0,1]
	v_pk_mul_f32 v[2:3], v[82:83], v[2:3] op_sel_hi:[0,1]
	v_cvt_pk_f16_f32 v6, v6, v7
	v_cvt_pk_f16_f32 v7, v8, v9
	v_cvt_pk_f16_f32 v8, v2, v3
	v_pk_add_f32 v[2:3], v[4:5], v[100:101]
	s_nop 0
	v_pk_mul_f32 v[2:3], v[82:83], v[2:3] op_sel_hi:[0,1]
	v_cvt_pk_f16_f32 v9, v2, v3
	v_lshl_add_u64 v[2:3], v[10:11], 0, v[50:51]
	global_store_dwordx4 v[2:3], v[6:9], off sc1

.LBB11_36:
	s_or_b64 exec, exec, s[0:1]
	s_mov_b32 s0, 0x717951a9
	v_cmp_eq_f32_e32 vcc, s0, v4
	s_and_b64 exec, exec, vcc
	s_cbranch_execz .LBB11_38
	v_mov_b32_e32 v0, 0
	v_mov_b32_e32 v1, 0x717951a9
	global_store_dword v0, v1, s[8:9] sc1

_Z6gemm_kILi1ELi128ELi4ELi8EEv5GArgs:
	v_lshlrev_b32_e32 v176, 4, v0
	s_getpc_b64 s[92:93]
	s_add_u32 s92, s92, 0xffff2af8
	s_addc_u32 s93, s93, 0xffffffff
	global_load_dwordx4 v[172:175], v176, s[92:93]
	s_cmpk_lt_u32 s2, 0xc0
	s_mov_b64 s[4:5], -1
	s_cbranch_scc0 .LBB12_2
	s_load_dwordx4 s[4:7], s[0:1], 0x0
	v_lshrrev_b32_e32 v44, 6, v0
	s_lshl_b32 s3, s2, 7
	v_bfe_u32 v1, v0, 3, 3
	s_and_b32 s3, s3, 0xf80
	v_lshl_or_b32 v6, v44, 4, v1
	v_and_b32_e32 v2, 7, v0
	v_bitop3_b32 v4, v44, v2, 1 bitop3:0x6c
	v_or_b32_e32 v2, s3, v6
	v_mul_u32_u24_e32 v2, 0x340, v2
	v_bfe_u32 v5, v0, 4, 2
	v_lshlrev_b32_e32 v34, 1, v2
	v_mov_b32_e32 v35, 0
	v_xor_b32_e32 v5, v4, v5
	s_waitcnt lgkmcnt(0)
	v_lshl_add_u64 v[2:3], s[4:5], 0, v[34:35]
	v_lshlrev_b32_e32 v34, 4, v5
	v_or_b32_e32 v7, 8, v6
	v_lshl_add_u64 v[36:37], v[2:3], 0, v[34:35]
	v_or_b32_e32 v2, s3, v7
	v_bfe_u32 v5, v7, 1, 3
	s_lshl_b32 s8, s2, 2
	v_mul_u32_u24_e32 v2, 0x340, v2
	v_mov_b32_e32 v3, v35
	v_xor_b32_e32 v4, v4, v5
	v_lshl_add_u64 v[2:3], v[2:3], 1, s[4:5]
	v_lshlrev_b32_e32 v4, 4, v4
	v_mov_b32_e32 v5, v35
	s_and_b32 s10, s8, 0x380
	v_lshl_add_u64 v[38:39], v[2:3], 0, v[4:5]
	v_or_b32_e32 v2, s10, v6
	v_mul_u32_u24_e32 v2, 0x680, v2
	v_mov_b32_e32 v3, v35
	v_lshl_add_u64 v[2:3], s[6:7], 0, v[2:3]
	v_lshl_add_u64 v[40:41], v[2:3], 0, v[34:35]
	v_or_b32_e32 v2, s10, v7
	v_mul_u32_u24_e32 v34, 0x680, v2
	v_lshl_add_u64 v[2:3], s[6:7], 0, v[34:35]
	v_lshl_add_u64 v[42:43], v[2:3], 0, v[4:5]
	v_lshlrev_b32_e32 v4, 11, v44
	v_or_b32_e32 v2, 0x400, v4
	v_readfirstlane_b32 s19, v4
	s_mov_b32 m0, s19
	v_readfirstlane_b32 s20, v2
	v_or_b32_e32 v2, 0x10000, v4
	global_load_lds_dwordx4 v[36:37], off
	s_mov_b32 m0, s20
	v_readfirstlane_b32 s21, v2
	v_or_b32_e32 v2, 0x10400, v4
	global_load_lds_dwordx4 v[38:39], off
	s_mov_b32 m0, s21
	v_readfirstlane_b32 s22, v2
	v_or_b32_e32 v5, 0x4000, v4
	global_load_lds_dwordx4 v[40:41], off
	s_mov_b32 m0, s22
	s_mov_b64 s[4:5], 0x80
	v_readfirstlane_b32 s15, v5
	v_or_b32_e32 v5, 0x4400, v4
	global_load_lds_dwordx4 v[42:43], off
	v_lshl_add_u64 v[2:3], v[36:37], 0, s[4:5]
	s_mov_b32 m0, s15
	v_readfirstlane_b32 s16, v5
	v_or_b32_e32 v5, 0x14000, v4
	global_load_lds_dwordx4 v[2:3], off
	v_lshl_add_u64 v[2:3], v[38:39], 0, s[4:5]
	s_mov_b32 m0, s16
	v_readfirstlane_b32 s17, v5
	v_or_b32_e32 v5, 0x14400, v4
	global_load_lds_dwordx4 v[2:3], off
	v_lshl_add_u64 v[2:3], v[40:41], 0, s[4:5]
	s_mov_b32 m0, s17
	v_readfirstlane_b32 s18, v5
	v_or_b32_e32 v5, 0x8000, v4
	global_load_lds_dwordx4 v[2:3], off
	v_lshl_add_u64 v[2:3], v[42:43], 0, s[4:5]
	s_mov_b32 m0, s18
	s_mov_b64 s[4:5], 0x100
	v_readfirstlane_b32 s11, v5
	v_or_b32_e32 v5, 0x8400, v4
	global_load_lds_dwordx4 v[2:3], off
	v_lshl_add_u64 v[2:3], v[36:37], 0, s[4:5]
	s_mov_b32 m0, s11
	v_readfirstlane_b32 s12, v5
	v_or_b32_e32 v5, 0x18000, v4
	global_load_lds_dwordx4 v[2:3], off
	v_lshl_add_u64 v[2:3], v[38:39], 0, s[4:5]
	s_mov_b32 m0, s12
	v_readfirstlane_b32 s13, v5
	v_or_b32_e32 v5, 0x18400, v4
	global_load_lds_dwordx4 v[2:3], off
	v_lshl_add_u64 v[2:3], v[40:41], 0, s[4:5]
	s_mov_b32 m0, s13
	v_readfirstlane_b32 s14, v5
	v_or_b32_e32 v5, 0xc000, v4
	global_load_lds_dwordx4 v[2:3], off
	v_lshl_add_u64 v[2:3], v[42:43], 0, s[4:5]
	s_mov_b32 m0, s14
	s_mov_b64 s[4:5], 0x180
	v_readfirstlane_b32 s25, v5
	v_or_b32_e32 v5, 0xc400, v4
	global_load_lds_dwordx4 v[2:3], off
	v_lshl_add_u64 v[2:3], v[36:37], 0, s[4:5]
	s_mov_b32 m0, s25
	v_readfirstlane_b32 s23, v5
	v_or_b32_e32 v5, 0x1c000, v4
	s_waitcnt vmcnt(8)
	s_waitcnt vmcnt(0) lgkmcnt(0)
	s_barrier
	global_load_lds_dwordx4 v[2:3], off
	v_lshl_add_u64 v[2:3], v[38:39], 0, s[4:5]
	s_mov_b32 m0, s23
	v_readfirstlane_b32 s24, v5
	v_or_b32_e32 v4, 0x1c400, v4
	global_load_lds_dwordx4 v[2:3], off
	v_lshl_add_u64 v[2:3], v[40:41], 0, s[4:5]
	s_mov_b32 m0, s24
	v_readfirstlane_b32 s26, v4
	global_load_lds_dwordx4 v[2:3], off
	v_lshl_add_u64 v[2:3], v[42:43], 0, s[4:5]
	s_mov_b32 m0, s26
	v_bfe_u32 v46, v0, 5, 1
	global_load_lds_dwordx4 v[2:3], off
	v_lshrrev_b32_e32 v2, 1, v0
	v_bfe_u32 v3, v0, 4, 1
	v_bitop3_b32 v2, v2, v3, 7 bitop3:0x6c
	v_or_b32_e32 v3, 6, v46
	s_load_dwordx2 s[8:9], s[0:1], 0x18
	s_load_dwordx2 s[6:7], s[0:1], 0x30
	s_load_dwordx2 s[4:5], s[0:1], 0x48
	v_xor_b32_e32 v3, v2, v3
	v_lshlrev_b32_e32 v72, 4, v3
	v_or_b32_e32 v3, 4, v46
	v_xor_b32_e32 v3, v2, v3
	v_lshlrev_b32_e32 v62, 4, v3
	v_or_b32_e32 v3, 2, v46
	v_and_b32_e32 v47, 31, v0
	v_xor_b32_e32 v3, v2, v3
	v_xor_b32_e32 v2, v2, v46
	v_bfe_u32 v45, v0, 6, 2
	v_lshrrev_b32_e32 v34, 8, v0
	s_mov_b32 s27, 0x10000
	v_lshlrev_b32_e32 v50, 7, v47
	v_lshlrev_b32_e32 v6, 4, v2
	v_lshlrev_b32_e32 v2, 12, v45
	v_lshlrev_b32_e32 v68, 13, v34
	v_lshlrev_b32_e32 v52, 4, v3
	v_or3_b32 v73, v2, v50, s27
	v_or3_b32 v49, v6, v68, v50
	ds_read_b128 v[2:5], v49
	v_or_b32_e32 v51, v73, v6
	ds_read_b128 v[6:9], v51
	v_or_b32_e32 v14, v52, v68
	v_add_u32_e32 v48, v14, v50
	ds_read_b128 v[54:57], v48
	v_or_b32_e32 v53, v73, v52
	ds_read_b128 v[10:13], v49 offset:4096
	ds_read_b128 v[58:61], v53
	s_waitcnt lgkmcnt(0)
	v_mfma_f32_32x32x16_f16 v[18:33], v[2:5], v[6:9], 0
	v_or_b32_e32 v52, v62, v68
	v_add_u32_e32 v52, v52, v50
	v_mfma_f32_32x32x16_f16 v[18:33], v[54:57], v[58:61], v[18:33]
	ds_read_b128 v[54:57], v48 offset:4096
	v_mfma_f32_32x32x16_f16 v[2:17], v[10:13], v[6:9], 0
	s_waitcnt lgkmcnt(0)
	v_mfma_f32_32x32x16_f16 v[2:17], v[54:57], v[58:61], v[2:17]
	ds_read_b128 v[56:59], v52
	v_or_b32_e32 v54, v73, v62
	ds_read_b128 v[60:63], v54
	ds_read_b128 v[64:67], v52 offset:4096
	v_or_b32_e32 v55, v72, v68
	v_add_u32_e32 v50, v55, v50
	ds_read_b128 v[68:71], v50
	v_or_b32_e32 v55, v73, v72
	s_waitcnt lgkmcnt(0)
	v_mfma_f32_32x32x16_f16 v[18:33], v[56:59], v[60:63], v[18:33]
	ds_read_b128 v[56:59], v55
	v_mfma_f32_32x32x16_f16 v[2:17], v[64:67], v[60:63], v[2:17]
	ds_read_b128 v[60:63], v50 offset:4096
	s_waitcnt lgkmcnt(0)
	v_mfma_f32_32x32x16_f16 v[18:33], v[68:71], v[56:59], v[18:33]
	v_mfma_f32_32x32x16_f16 v[2:17], v[60:63], v[56:59], v[2:17]
	s_mov_b64 s[28:29], 0x200
	s_mov_b32 m0, s19
	v_lshl_add_u64 v[56:57], v[36:37], 0, s[28:29]
	s_waitcnt vmcnt(8)
	s_barrier
	global_load_lds_dwordx4 v[56:57], off
	v_lshl_add_u64 v[56:57], v[38:39], 0, s[28:29]
	s_mov_b32 m0, s20
	s_nop 0
	global_load_lds_dwordx4 v[56:57], off
	v_lshl_add_u64 v[56:57], v[40:41], 0, s[28:29]
	s_mov_b32 m0, s21
	s_nop 0
	global_load_lds_dwordx4 v[56:57], off
	v_lshl_add_u64 v[56:57], v[42:43], 0, s[28:29]
	s_mov_b32 m0, s22
	s_nop 0
	global_load_lds_dwordx4 v[56:57], off
	ds_read_b128 v[56:59], v49 offset:16384
	ds_read_b128 v[60:63], v51 offset:16384
	ds_read_b128 v[64:67], v49 offset:20480
	ds_read_b128 v[68:71], v48 offset:16384
	s_waitcnt lgkmcnt(0)
	v_mfma_f32_32x32x16_f16 v[18:33], v[56:59], v[60:63], v[18:33]
	ds_read_b128 v[56:59], v53 offset:16384
	v_mfma_f32_32x32x16_f16 v[2:17], v[64:67], v[60:63], v[2:17]
	ds_read_b128 v[60:63], v48 offset:20480
	s_waitcnt lgkmcnt(0)
	v_mfma_f32_32x32x16_f16 v[18:33], v[68:71], v[56:59], v[18:33]
	v_mfma_f32_32x32x16_f16 v[2:17], v[60:63], v[56:59], v[2:17]
	ds_read_b128 v[56:59], v52 offset:16384
	ds_read_b128 v[60:63], v54 offset:16384
	ds_read_b128 v[64:67], v52 offset:20480
	ds_read_b128 v[68:71], v50 offset:16384
	s_waitcnt lgkmcnt(0)
	v_mfma_f32_32x32x16_f16 v[18:33], v[56:59], v[60:63], v[18:33]
	ds_read_b128 v[56:59], v55 offset:16384
	v_mfma_f32_32x32x16_f16 v[2:17], v[64:67], v[60:63], v[2:17]
	ds_read_b128 v[60:63], v50 offset:20480
	s_waitcnt lgkmcnt(0)
	v_mfma_f32_32x32x16_f16 v[18:33], v[68:71], v[56:59], v[18:33]
	v_mfma_f32_32x32x16_f16 v[2:17], v[60:63], v[56:59], v[2:17]
	s_mov_b64 s[28:29], 0x280
	s_mov_b32 m0, s15
	v_lshl_add_u64 v[56:57], v[36:37], 0, s[28:29]
	s_waitcnt vmcnt(8)
	s_barrier
	global_load_lds_dwordx4 v[56:57], off
	v_lshl_add_u64 v[56:57], v[38:39], 0, s[28:29]
	s_mov_b32 m0, s16
	s_nop 0
	global_load_lds_dwordx4 v[56:57], off
	v_lshl_add_u64 v[56:57], v[40:41], 0, s[28:29]
	s_mov_b32 m0, s17
	s_nop 0
	global_load_lds_dwordx4 v[56:57], off
	v_lshl_add_u64 v[56:57], v[42:43], 0, s[28:29]
	s_mov_b32 m0, s18
	s_nop 0
	global_load_lds_dwordx4 v[56:57], off
	ds_read_b128 v[56:59], v49 offset:32768
	ds_read_b128 v[60:63], v51 offset:32768
	ds_read_b128 v[64:67], v49 offset:36864
	ds_read_b128 v[68:71], v48 offset:32768
	s_waitcnt lgkmcnt(0)
	v_mfma_f32_32x32x16_f16 v[18:33], v[56:59], v[60:63], v[18:33]
	ds_read_b128 v[56:59], v53 offset:32768
	v_mfma_f32_32x32x16_f16 v[2:17], v[64:67], v[60:63], v[2:17]
	ds_read_b128 v[60:63], v48 offset:36864
	s_waitcnt lgkmcnt(0)
	v_mfma_f32_32x32x16_f16 v[18:33], v[68:71], v[56:59], v[18:33]
	v_mfma_f32_32x32x16_f16 v[2:17], v[60:63], v[56:59], v[2:17]
	ds_read_b128 v[56:59], v52 offset:32768
	ds_read_b128 v[60:63], v54 offset:32768
	ds_read_b128 v[64:67], v52 offset:36864
	ds_read_b128 v[68:71], v50 offset:32768
	s_waitcnt lgkmcnt(0)
	v_mfma_f32_32x32x16_f16 v[18:33], v[56:59], v[60:63], v[18:33]
	ds_read_b128 v[56:59], v55 offset:32768
	v_mfma_f32_32x32x16_f16 v[2:17], v[64:67], v[60:63], v[2:17]
	ds_read_b128 v[60:63], v50 offset:36864
	s_waitcnt lgkmcnt(0)
	v_mfma_f32_32x32x16_f16 v[18:33], v[68:71], v[56:59], v[18:33]
	v_mfma_f32_32x32x16_f16 v[2:17], v[60:63], v[56:59], v[2:17]
	s_mov_b64 s[28:29], 0x300
	s_mov_b32 m0, s11
	v_lshl_add_u64 v[56:57], v[36:37], 0, s[28:29]
	s_waitcnt vmcnt(8)
	s_barrier
	global_load_lds_dwordx4 v[56:57], off
	v_lshl_add_u64 v[56:57], v[38:39], 0, s[28:29]
	s_mov_b32 m0, s12
	s_nop 0
	global_load_lds_dwordx4 v[56:57], off
	v_lshl_add_u64 v[56:57], v[40:41], 0, s[28:29]
	s_mov_b32 m0, s13
	s_nop 0
	global_load_lds_dwordx4 v[56:57], off
	v_lshl_add_u64 v[56:57], v[42:43], 0, s[28:29]
	s_mov_b32 m0, s14
	s_nop 0
	global_load_lds_dwordx4 v[56:57], off
	ds_read_b128 v[56:59], v49 offset:49152
	ds_read_b128 v[60:63], v51 offset:49152
	ds_read_b128 v[64:67], v49 offset:53248
	ds_read_b128 v[68:71], v48 offset:49152
	s_waitcnt lgkmcnt(0)
	v_mfma_f32_32x32x16_f16 v[18:33], v[56:59], v[60:63], v[18:33]
	ds_read_b128 v[56:59], v53 offset:49152
	v_mfma_f32_32x32x16_f16 v[2:17], v[64:67], v[60:63], v[2:17]
	ds_read_b128 v[60:63], v48 offset:53248
	s_waitcnt lgkmcnt(0)
	v_mfma_f32_32x32x16_f16 v[18:33], v[68:71], v[56:59], v[18:33]
	v_mfma_f32_32x32x16_f16 v[2:17], v[60:63], v[56:59], v[2:17]
	ds_read_b128 v[56:59], v52 offset:49152
	ds_read_b128 v[60:63], v54 offset:49152
	ds_read_b128 v[64:67], v52 offset:53248
	ds_read_b128 v[68:71], v50 offset:49152
	s_waitcnt lgkmcnt(0)
	v_mfma_f32_32x32x16_f16 v[18:33], v[56:59], v[60:63], v[18:33]
	ds_read_b128 v[56:59], v55 offset:49152
	v_mfma_f32_32x32x16_f16 v[2:17], v[64:67], v[60:63], v[2:17]
	ds_read_b128 v[60:63], v50 offset:53248
	s_waitcnt lgkmcnt(0)
	v_mfma_f32_32x32x16_f16 v[18:33], v[68:71], v[56:59], v[18:33]
	v_mfma_f32_32x32x16_f16 v[2:17], v[60:63], v[56:59], v[2:17]
	s_mov_b64 s[28:29], 0x380
	s_mov_b32 m0, s25
	v_lshl_add_u64 v[56:57], v[36:37], 0, s[28:29]
	s_waitcnt vmcnt(8)
	s_barrier
	global_load_lds_dwordx4 v[56:57], off
	v_lshl_add_u64 v[56:57], v[38:39], 0, s[28:29]
	s_mov_b32 m0, s23
	s_nop 0
	global_load_lds_dwordx4 v[56:57], off
	v_lshl_add_u64 v[56:57], v[40:41], 0, s[28:29]
	s_mov_b32 m0, s24
	s_nop 0
	global_load_lds_dwordx4 v[56:57], off
	v_lshl_add_u64 v[56:57], v[42:43], 0, s[28:29]
	s_mov_b32 m0, s26
	s_nop 0
	global_load_lds_dwordx4 v[56:57], off
	ds_read_b128 v[56:59], v49
	ds_read_b128 v[60:63], v51
	ds_read_b128 v[64:67], v49 offset:4096
	ds_read_b128 v[68:71], v48
	s_waitcnt lgkmcnt(0)
	v_mfma_f32_32x32x16_f16 v[18:33], v[56:59], v[60:63], v[18:33]
	ds_read_b128 v[56:59], v53
	v_mfma_f32_32x32x16_f16 v[2:17], v[64:67], v[60:63], v[2:17]
	ds_read_b128 v[60:63], v48 offset:4096
	s_waitcnt lgkmcnt(0)
	v_mfma_f32_32x32x16_f16 v[18:33], v[68:71], v[56:59], v[18:33]
	v_mfma_f32_32x32x16_f16 v[2:17], v[60:63], v[56:59], v[2:17]
	ds_read_b128 v[56:59], v52
	ds_read_b128 v[60:63], v54
	ds_read_b128 v[64:67], v52 offset:4096
	ds_read_b128 v[68:71], v50
	s_waitcnt lgkmcnt(0)
	v_mfma_f32_32x32x16_f16 v[18:33], v[56:59], v[60:63], v[18:33]
	ds_read_b128 v[56:59], v55
	v_mfma_f32_32x32x16_f16 v[2:17], v[64:67], v[60:63], v[2:17]
	ds_read_b128 v[60:63], v50 offset:4096
	s_waitcnt lgkmcnt(0)
	v_mfma_f32_32x32x16_f16 v[18:33], v[68:71], v[56:59], v[18:33]
	v_mfma_f32_32x32x16_f16 v[2:17], v[60:63], v[56:59], v[2:17]
	s_mov_b64 s[28:29], 0x400
	s_mov_b32 m0, s19
	v_lshl_add_u64 v[56:57], v[36:37], 0, s[28:29]
	s_waitcnt vmcnt(8)
	s_barrier
	global_load_lds_dwordx4 v[56:57], off
	v_lshl_add_u64 v[56:57], v[38:39], 0, s[28:29]
	s_mov_b32 m0, s20
	s_nop 0
	global_load_lds_dwordx4 v[56:57], off
	v_lshl_add_u64 v[56:57], v[40:41], 0, s[28:29]
	s_mov_b32 m0, s21
	s_nop 0
	global_load_lds_dwordx4 v[56:57], off
	v_lshl_add_u64 v[56:57], v[42:43], 0, s[28:29]
	s_mov_b32 m0, s22
	s_nop 0
	global_load_lds_dwordx4 v[56:57], off
	ds_read_b128 v[56:59], v49 offset:16384
	ds_read_b128 v[60:63], v51 offset:16384
	ds_read_b128 v[64:67], v49 offset:20480
	ds_read_b128 v[68:71], v48 offset:16384
	s_waitcnt lgkmcnt(0)
	v_mfma_f32_32x32x16_f16 v[18:33], v[56:59], v[60:63], v[18:33]
	ds_read_b128 v[56:59], v53 offset:16384
	v_mfma_f32_32x32x16_f16 v[2:17], v[64:67], v[60:63], v[2:17]
	ds_read_b128 v[60:63], v48 offset:20480
	s_waitcnt lgkmcnt(0)
	v_mfma_f32_32x32x16_f16 v[18:33], v[68:71], v[56:59], v[18:33]
	v_mfma_f32_32x32x16_f16 v[2:17], v[60:63], v[56:59], v[2:17]
	ds_read_b128 v[56:59], v52 offset:16384
	ds_read_b128 v[60:63], v54 offset:16384
	ds_read_b128 v[64:67], v52 offset:20480
	ds_read_b128 v[68:71], v50 offset:16384
	s_waitcnt lgkmcnt(0)
	v_mfma_f32_32x32x16_f16 v[18:33], v[56:59], v[60:63], v[18:33]
	ds_read_b128 v[56:59], v55 offset:16384
	v_mfma_f32_32x32x16_f16 v[2:17], v[64:67], v[60:63], v[2:17]
	ds_read_b128 v[60:63], v50 offset:20480
	s_waitcnt lgkmcnt(0)
	v_mfma_f32_32x32x16_f16 v[18:33], v[68:71], v[56:59], v[18:33]
	v_mfma_f32_32x32x16_f16 v[2:17], v[60:63], v[56:59], v[2:17]
	s_mov_b64 s[28:29], 0x480
	s_mov_b32 m0, s15
	v_lshl_add_u64 v[56:57], v[36:37], 0, s[28:29]
	s_waitcnt vmcnt(8)
	s_barrier
	global_load_lds_dwordx4 v[56:57], off
	v_lshl_add_u64 v[56:57], v[38:39], 0, s[28:29]
	s_mov_b32 m0, s16
	s_nop 0
	global_load_lds_dwordx4 v[56:57], off
	v_lshl_add_u64 v[56:57], v[40:41], 0, s[28:29]
	s_mov_b32 m0, s17
	s_nop 0
	global_load_lds_dwordx4 v[56:57], off
	v_lshl_add_u64 v[56:57], v[42:43], 0, s[28:29]
	s_mov_b32 m0, s18
	s_nop 0
	global_load_lds_dwordx4 v[56:57], off
	ds_read_b128 v[56:59], v49 offset:32768
	ds_read_b128 v[60:63], v51 offset:32768
	ds_read_b128 v[64:67], v49 offset:36864
	ds_read_b128 v[68:71], v48 offset:32768
	s_waitcnt lgkmcnt(0)
	v_mfma_f32_32x32x16_f16 v[18:33], v[56:59], v[60:63], v[18:33]
	ds_read_b128 v[56:59], v53 offset:32768
	v_mfma_f32_32x32x16_f16 v[2:17], v[64:67], v[60:63], v[2:17]
	ds_read_b128 v[60:63], v48 offset:36864
	s_waitcnt lgkmcnt(0)
	v_mfma_f32_32x32x16_f16 v[18:33], v[68:71], v[56:59], v[18:33]
	v_mfma_f32_32x32x16_f16 v[2:17], v[60:63], v[56:59], v[2:17]
	ds_read_b128 v[56:59], v52 offset:32768
	ds_read_b128 v[60:63], v54 offset:32768
	ds_read_b128 v[64:67], v52 offset:36864
	ds_read_b128 v[68:71], v50 offset:32768
	s_waitcnt lgkmcnt(0)
	v_mfma_f32_32x32x16_f16 v[18:33], v[56:59], v[60:63], v[18:33]
	ds_read_b128 v[56:59], v55 offset:32768
	v_mfma_f32_32x32x16_f16 v[2:17], v[64:67], v[60:63], v[2:17]
	ds_read_b128 v[60:63], v50 offset:36864
	s_waitcnt lgkmcnt(0)
	v_mfma_f32_32x32x16_f16 v[18:33], v[68:71], v[56:59], v[18:33]
	v_mfma_f32_32x32x16_f16 v[2:17], v[60:63], v[56:59], v[2:17]
	s_mov_b64 s[28:29], 0x500
	s_mov_b32 m0, s11
	v_lshl_add_u64 v[56:57], v[36:37], 0, s[28:29]
	s_waitcnt vmcnt(8)
	s_barrier
	global_load_lds_dwordx4 v[56:57], off
	v_lshl_add_u64 v[56:57], v[38:39], 0, s[28:29]
	s_mov_b32 m0, s12
	s_nop 0
	global_load_lds_dwordx4 v[56:57], off
	v_lshl_add_u64 v[56:57], v[40:41], 0, s[28:29]
	s_mov_b32 m0, s13
	s_nop 0
	global_load_lds_dwordx4 v[56:57], off
	v_lshl_add_u64 v[56:57], v[42:43], 0, s[28:29]
	s_mov_b32 m0, s14
	s_nop 0
	global_load_lds_dwordx4 v[56:57], off
	ds_read_b128 v[56:59], v49 offset:49152
	ds_read_b128 v[60:63], v51 offset:49152
	ds_read_b128 v[64:67], v49 offset:53248
	ds_read_b128 v[68:71], v48 offset:49152
	s_waitcnt lgkmcnt(0)
	v_mfma_f32_32x32x16_f16 v[18:33], v[56:59], v[60:63], v[18:33]
	ds_read_b128 v[56:59], v53 offset:49152
	v_mfma_f32_32x32x16_f16 v[2:17], v[64:67], v[60:63], v[2:17]
	ds_read_b128 v[60:63], v48 offset:53248
	s_waitcnt lgkmcnt(0)
	v_mfma_f32_32x32x16_f16 v[18:33], v[68:71], v[56:59], v[18:33]
	v_mfma_f32_32x32x16_f16 v[2:17], v[60:63], v[56:59], v[2:17]
	ds_read_b128 v[56:59], v52 offset:49152
	ds_read_b128 v[60:63], v54 offset:49152
	ds_read_b128 v[64:67], v52 offset:53248
	ds_read_b128 v[68:71], v50 offset:49152
	s_waitcnt lgkmcnt(0)
	v_mfma_f32_32x32x16_f16 v[18:33], v[56:59], v[60:63], v[18:33]
	ds_read_b128 v[56:59], v55 offset:49152
	v_mfma_f32_32x32x16_f16 v[2:17], v[64:67], v[60:63], v[2:17]
	ds_read_b128 v[60:63], v50 offset:53248
	s_waitcnt lgkmcnt(0)
	v_mfma_f32_32x32x16_f16 v[18:33], v[68:71], v[56:59], v[18:33]
	v_mfma_f32_32x32x16_f16 v[2:17], v[60:63], v[56:59], v[2:17]
	s_mov_b64 s[28:29], 0x580
	s_mov_b32 m0, s25
	v_lshl_add_u64 v[64:65], v[36:37], 0, s[28:29]
	s_waitcnt vmcnt(8)
	s_barrier
	global_load_lds_dwordx4 v[64:65], off
	v_lshl_add_u64 v[66:67], v[38:39], 0, s[28:29]
	s_mov_b32 m0, s23
	v_lshl_add_u64 v[68:69], v[40:41], 0, s[28:29]
	global_load_lds_dwordx4 v[66:67], off
	s_mov_b32 m0, s24
	v_lshl_add_u64 v[70:71], v[42:43], 0, s[28:29]
	global_load_lds_dwordx4 v[68:69], off
	s_mov_b32 m0, s26
	s_nop 0
	global_load_lds_dwordx4 v[70:71], off
	ds_read_b128 v[36:39], v49
	ds_read_b128 v[40:43], v51
	ds_read_b128 v[56:59], v49 offset:4096
	ds_read_b128 v[60:63], v48
	s_waitcnt lgkmcnt(0)
	v_mfma_f32_32x32x16_f16 v[18:33], v[36:39], v[40:43], v[18:33]
	ds_read_b128 v[36:39], v53
	v_mfma_f32_32x32x16_f16 v[2:17], v[56:59], v[40:43], v[2:17]
	ds_read_b128 v[40:43], v48 offset:4096
	s_waitcnt lgkmcnt(0)
	v_mfma_f32_32x32x16_f16 v[18:33], v[60:63], v[36:39], v[18:33]
	v_mfma_f32_32x32x16_f16 v[2:17], v[40:43], v[36:39], v[2:17]
	ds_read_b128 v[36:39], v52
	ds_read_b128 v[40:43], v54
	ds_read_b128 v[56:59], v52 offset:4096
	ds_read_b128 v[60:63], v50
	s_waitcnt lgkmcnt(0)
	v_mfma_f32_32x32x16_f16 v[18:33], v[36:39], v[40:43], v[18:33]
	ds_read_b128 v[36:39], v55
	v_mfma_f32_32x32x16_f16 v[2:17], v[56:59], v[40:43], v[2:17]
	ds_read_b128 v[40:43], v50 offset:4096
	s_waitcnt lgkmcnt(0)
	v_mfma_f32_32x32x16_f16 v[18:33], v[60:63], v[36:39], v[18:33]
	v_mfma_f32_32x32x16_f16 v[2:17], v[40:43], v[36:39], v[2:17]
	s_mov_b32 m0, s19
	s_waitcnt vmcnt(8)
	s_barrier
	global_load_lds_dwordx4 v[64:65], off
	s_mov_b32 m0, s20
	s_nop 0
	global_load_lds_dwordx4 v[66:67], off
	s_mov_b32 m0, s21
	s_nop 0
	global_load_lds_dwordx4 v[68:69], off
	s_mov_b32 m0, s22
	s_nop 0
	global_load_lds_dwordx4 v[70:71], off
	ds_read_b128 v[36:39], v49 offset:16384
	ds_read_b128 v[40:43], v51 offset:16384
	ds_read_b128 v[56:59], v49 offset:20480
	ds_read_b128 v[60:63], v48 offset:16384
	s_waitcnt lgkmcnt(0)
	v_mfma_f32_32x32x16_f16 v[18:33], v[36:39], v[40:43], v[18:33]
	ds_read_b128 v[36:39], v53 offset:16384
	v_mfma_f32_32x32x16_f16 v[2:17], v[56:59], v[40:43], v[2:17]
	ds_read_b128 v[40:43], v48 offset:20480
	s_waitcnt lgkmcnt(0)
	v_mfma_f32_32x32x16_f16 v[18:33], v[60:63], v[36:39], v[18:33]
	v_mfma_f32_32x32x16_f16 v[2:17], v[40:43], v[36:39], v[2:17]
	ds_read_b128 v[36:39], v52 offset:16384
	ds_read_b128 v[40:43], v54 offset:16384
	ds_read_b128 v[56:59], v52 offset:20480
	ds_read_b128 v[60:63], v50 offset:16384
	s_waitcnt lgkmcnt(0)
	v_mfma_f32_32x32x16_f16 v[18:33], v[36:39], v[40:43], v[18:33]
	ds_read_b128 v[36:39], v55 offset:16384
	v_mfma_f32_32x32x16_f16 v[2:17], v[56:59], v[40:43], v[2:17]
	ds_read_b128 v[40:43], v50 offset:20480
	s_waitcnt lgkmcnt(0)
	v_mfma_f32_32x32x16_f16 v[18:33], v[60:63], v[36:39], v[18:33]
	v_mfma_f32_32x32x16_f16 v[2:17], v[40:43], v[36:39], v[2:17]
	s_mov_b32 m0, s15
	s_waitcnt vmcnt(8)
	s_barrier
	global_load_lds_dwordx4 v[64:65], off
	s_mov_b32 m0, s16
	s_nop 0
	global_load_lds_dwordx4 v[66:67], off
	s_mov_b32 m0, s17
	s_nop 0
	global_load_lds_dwordx4 v[68:69], off
	s_mov_b32 m0, s18
	s_nop 0
	global_load_lds_dwordx4 v[70:71], off
	ds_read_b128 v[36:39], v49 offset:32768
	ds_read_b128 v[40:43], v51 offset:32768
	ds_read_b128 v[56:59], v49 offset:36864
	ds_read_b128 v[60:63], v48 offset:32768
	s_waitcnt lgkmcnt(0)
	v_mfma_f32_32x32x16_f16 v[18:33], v[36:39], v[40:43], v[18:33]
	ds_read_b128 v[36:39], v53 offset:32768
	v_mfma_f32_32x32x16_f16 v[2:17], v[56:59], v[40:43], v[2:17]
	ds_read_b128 v[40:43], v48 offset:36864
	s_waitcnt lgkmcnt(0)
	v_mfma_f32_32x32x16_f16 v[18:33], v[60:63], v[36:39], v[18:33]
	v_mfma_f32_32x32x16_f16 v[2:17], v[40:43], v[36:39], v[2:17]
	ds_read_b128 v[36:39], v52 offset:32768
	ds_read_b128 v[40:43], v54 offset:32768
	ds_read_b128 v[56:59], v52 offset:36864
	ds_read_b128 v[60:63], v50 offset:32768
	s_waitcnt lgkmcnt(0)
	v_mfma_f32_32x32x16_f16 v[18:33], v[36:39], v[40:43], v[18:33]
	ds_read_b128 v[36:39], v55 offset:32768
	v_mfma_f32_32x32x16_f16 v[2:17], v[56:59], v[40:43], v[2:17]
	ds_read_b128 v[40:43], v50 offset:36864
	s_waitcnt lgkmcnt(0)
	v_mfma_f32_32x32x16_f16 v[18:33], v[60:63], v[36:39], v[18:33]
	v_mfma_f32_32x32x16_f16 v[2:17], v[40:43], v[36:39], v[2:17]
	s_mov_b32 m0, s11
	s_waitcnt vmcnt(8)
	s_barrier
	global_load_lds_dwordx4 v[64:65], off
	s_mov_b32 m0, s12
	s_nop 0
	global_load_lds_dwordx4 v[66:67], off
	s_mov_b32 m0, s13
	s_nop 0
	global_load_lds_dwordx4 v[68:69], off
	s_mov_b32 m0, s14
	s_nop 0
	global_load_lds_dwordx4 v[70:71], off
	ds_read_b128 v[36:39], v49 offset:49152
	ds_read_b128 v[40:43], v51 offset:49152
	ds_read_b128 v[56:59], v49 offset:53248
	ds_read_b128 v[60:63], v48 offset:49152
	s_waitcnt lgkmcnt(0)
	v_mfma_f32_32x32x16_f16 v[18:33], v[36:39], v[40:43], v[18:33]
	ds_read_b128 v[36:39], v53 offset:49152
	v_mfma_f32_32x32x16_f16 v[2:17], v[56:59], v[40:43], v[2:17]
	ds_read_b128 v[40:43], v48 offset:53248
	s_waitcnt lgkmcnt(0)
	v_mfma_f32_32x32x16_f16 v[18:33], v[60:63], v[36:39], v[18:33]
	v_mfma_f32_32x32x16_f16 v[2:17], v[40:43], v[36:39], v[2:17]
	ds_read_b128 v[36:39], v52 offset:49152
	ds_read_b128 v[40:43], v54 offset:49152
	ds_read_b128 v[56:59], v52 offset:53248
	ds_read_b128 v[60:63], v50 offset:49152
	s_waitcnt lgkmcnt(0)
	v_mfma_f32_32x32x16_f16 v[18:33], v[36:39], v[40:43], v[18:33]
	ds_read_b128 v[36:39], v55 offset:49152
	v_mfma_f32_32x32x16_f16 v[2:17], v[56:59], v[40:43], v[2:17]
	ds_read_b128 v[40:43], v50 offset:53248
	s_waitcnt lgkmcnt(0)
	v_mfma_f32_32x32x16_f16 v[18:33], v[60:63], v[36:39], v[18:33]
	v_mfma_f32_32x32x16_f16 v[2:17], v[40:43], v[36:39], v[2:17]
	v_mul_u32_u24_e32 v56, 0x2400, v44
	v_lshl_or_b32 v36, v47, 2, v56
	s_movk_i32 s11, 0x240
	v_mad_u32_u24 v36, v46, s11, v36
	s_waitcnt vmcnt(8)
	s_barrier
	s_waitcnt vmcnt(0)
	s_waitcnt vmcnt(0)
	s_barrier
	s_nop 3
	ds_write2_b32 v36, v18, v19 offset1:36
	ds_write2_b32 v36, v20, v21 offset0:72 offset1:108
	v_add_u32_e32 v18, 0x400, v36
	ds_write2_b32 v18, v22, v23 offset0:32 offset1:68
	ds_write2_b32 v18, v24, v25 offset0:104 offset1:140
	v_add_u32_e32 v18, 0x800, v36
	ds_write2_b32 v18, v26, v27 offset0:64 offset1:100
	ds_write2_b32 v18, v28, v29 offset0:136 offset1:172
	v_add_u32_e32 v18, 0xc00, v36
	ds_write2_b32 v18, v30, v31 offset0:96 offset1:132
	ds_write2_b32 v18, v32, v33 offset0:168 offset1:204
	v_add_u32_e32 v18, 0x1000, v36
	ds_write2_b32 v18, v2, v3 offset0:128 offset1:164
	ds_write2_b32 v18, v4, v5 offset0:200 offset1:236
	v_add_u32_e32 v2, 0x1400, v36
	ds_write2_b32 v2, v6, v7 offset0:160 offset1:196
	v_add_u32_e32 v2, 0x1600, v36
	ds_write2_b32 v2, v8, v9 offset0:104 offset1:140
	v_add_u32_e32 v2, 0x1800, v36
	ds_write2_b32 v2, v10, v11 offset0:192 offset1:228
	v_add_u32_e32 v2, 0x1c00, v36
	ds_write2_b32 v2, v12, v13 offset0:8 offset1:44
	v_add_u32_e32 v2, 0x1e00, v36
	v_lshl_or_b32 v5, v45, 5, s10
	v_lshlrev_b32_e32 v6, 2, v0
	ds_write2_b32 v2, v14, v15 offset0:96 offset1:132
	v_add_u32_e32 v2, 0x2000, v36
	v_lshlrev_b32_e32 v4, 6, v34
	v_lshlrev_b32_e32 v34, 2, v5
	v_and_b32_e32 v6, 28, v6
	ds_write2_b32 v2, v16, v17 offset0:40 offset1:76
	v_lshl_add_u64 v[2:3], s[8:9], 0, v[34:35]
	v_lshlrev_b32_e32 v34, 2, v6
	v_lshl_add_u64 v[10:11], v[2:3], 0, v[34:35]
	v_or3_b32 v2, s3, v4, v1
	v_or_b32_e32 v3, v5, v6
	s_movk_i32 s3, 0x300
	v_mad_u32_u24 v36, v2, s3, v3
	v_add_u32_e32 v2, 0x4800, v36
	v_mov_b32_e32 v3, v35
	v_lshlrev_b64 v[40:41], 2, v[2:3]
	v_lshl_add_u64 v[12:13], s[6:7], 0, v[40:41]
	global_load_dwordx4 v[2:5], v[10:11], off
	global_load_dwordx4 v[6:9], v[12:13], off
	v_add_u32_e32 v10, 0x3000, v36
	v_mov_b32_e32 v11, v35
	v_lshlrev_b64 v[42:43], 2, v[10:11]
	v_lshl_add_u64 v[10:11], s[6:7], 0, v[42:43]
	global_load_dwordx4 v[10:13], v[10:11], off
	v_add_u32_e32 v14, 0x1800, v36
	v_mov_b32_e32 v15, v35
	v_lshlrev_b64 v[44:45], 2, v[14:15]
	v_lshl_add_u64 v[14:15], s[6:7], 0, v[44:45]
	v_mov_b32_e32 v37, v35
	global_load_dwordx4 v[14:17], v[14:15], off
	v_lshlrev_b64 v[46:47], 2, v[36:37]
	v_lshl_add_u64 v[18:19], s[6:7], 0, v[46:47]
	global_load_dwordx4 v[18:21], v[18:19], off
	v_add_u32_e32 v22, 0x6000, v36
	v_mov_b32_e32 v23, v35
	v_lshlrev_b64 v[48:49], 2, v[22:23]
	v_lshl_add_u64 v[22:23], s[6:7], 0, v[48:49]
	v_add_u32_e32 v26, 0x7800, v36
	v_mov_b32_e32 v27, v35
	global_load_dwordx4 v[22:25], v[22:23], off
	v_lshlrev_b64 v[50:51], 2, v[26:27]
	v_lshl_add_u64 v[26:27], s[6:7], 0, v[50:51]
	global_load_dwordx4 v[26:29], v[26:27], off
	v_add_u32_e32 v30, 0x9000, v36
	v_mov_b32_e32 v31, v35
	v_add_u32_e32 v36, 0xa800, v36
	v_lshlrev_b64 v[52:53], 2, v[30:31]
	v_lshlrev_b64 v[54:55], 2, v[36:37]
	v_lshl_add_u64 v[30:31], s[6:7], 0, v[52:53]
	v_lshl_add_u64 v[36:37], s[6:7], 0, v[54:55]
	global_load_dwordx4 v[30:33], v[30:31], off
	v_or_b32_e32 v34, v56, v34
	global_load_dwordx4 v[36:39], v[36:37], off
	s_movk_i32 s3, 0x90
	v_mad_u32_u24 v1, v1, s3, v34
	v_lshl_add_u64 v[58:59], s[4:5], 0, v[42:43]
	v_lshl_add_u64 v[60:61], s[4:5], 0, v[40:41]
	ds_read_b128 v[40:43], v1 offset:3456
	v_lshl_add_u64 v[34:35], s[4:5], 0, v[46:47]
	v_lshl_add_u64 v[56:57], s[4:5], 0, v[44:45]
	ds_read_b128 v[44:47], v1 offset:2304
	v_lshl_add_u64 v[48:49], s[4:5], 0, v[48:49]
	v_lshl_add_u64 v[50:51], s[4:5], 0, v[50:51]
	v_lshl_add_u64 v[52:53], s[4:5], 0, v[52:53]
	v_lshl_add_u64 v[54:55], s[4:5], 0, v[54:55]
	s_mov_b64 s[4:5], 0
	s_waitcnt vmcnt(8) lgkmcnt(1)
	v_pk_add_f32 v[40:41], v[2:3], v[40:41]
	s_waitcnt vmcnt(7)
	v_pk_add_f32 v[6:7], v[40:41], v[6:7]
	v_pk_add_f32 v[40:41], v[4:5], v[42:43]
	s_waitcnt lgkmcnt(0)
	v_pk_add_f32 v[44:45], v[2:3], v[44:45]
	v_pk_add_f32 v[8:9], v[40:41], v[8:9]
	ds_read_b128 v[40:43], v1 offset:1152
	s_waitcnt vmcnt(6)
	v_pk_add_f32 v[10:11], v[44:45], v[10:11]
	v_pk_add_f32 v[44:45], v[4:5], v[46:47]
	s_nop 0
	v_pk_add_f32 v[12:13], v[44:45], v[12:13]
	ds_read_b128 v[44:47], v1
	s_waitcnt lgkmcnt(1)
	v_pk_add_f32 v[40:41], v[2:3], v[40:41]
	s_waitcnt vmcnt(5)
	v_pk_add_f32 v[14:15], v[40:41], v[14:15]
	v_pk_add_f32 v[40:41], v[4:5], v[42:43]
	s_nop 0
	v_pk_add_f32 v[16:17], v[40:41], v[16:17]
	s_waitcnt lgkmcnt(0)
	v_pk_add_f32 v[40:41], v[2:3], v[44:45]
	s_waitcnt vmcnt(4)
	v_pk_add_f32 v[18:19], v[40:41], v[18:19]
	v_pk_add_f32 v[40:41], v[4:5], v[46:47]
	s_nop 0
	v_pk_add_f32 v[20:21], v[40:41], v[20:21]
	global_store_dwordx4 v[34:35], v[18:21], off sc1
	ds_read_b128 v[18:21], v1 offset:4608
	global_store_dwordx4 v[56:57], v[14:17], off sc1
	global_store_dwordx4 v[58:59], v[10:13], off sc1
	global_store_dwordx4 v[60:61], v[6:9], off sc1
	ds_read_b128 v[6:9], v1 offset:5760
	s_waitcnt lgkmcnt(1)
	v_pk_add_f32 v[10:11], v[2:3], v[18:19]
	v_pk_add_f32 v[12:13], v[4:5], v[20:21]
	s_waitcnt vmcnt(7)
	v_pk_add_f32 v[10:11], v[10:11], v[22:23]
	v_pk_add_f32 v[12:13], v[12:13], v[24:25]
	global_store_dwordx4 v[48:49], v[10:13], off sc1
	ds_read_b128 v[10:13], v1 offset:6912
	s_waitcnt lgkmcnt(1)
	v_pk_add_f32 v[6:7], v[2:3], v[6:7]
	v_pk_add_f32 v[8:9], v[4:5], v[8:9]
	s_waitcnt vmcnt(7)
	v_pk_add_f32 v[6:7], v[6:7], v[26:27]
	v_pk_add_f32 v[8:9], v[8:9], v[28:29]
	global_store_dwordx4 v[50:51], v[6:9], off sc1
	ds_read_b128 v[6:9], v1 offset:8064
	s_waitcnt lgkmcnt(1)
	v_pk_add_f32 v[10:11], v[2:3], v[10:11]
	v_pk_add_f32 v[12:13], v[4:5], v[12:13]
	s_waitcnt vmcnt(7)
	v_pk_add_f32 v[10:11], v[10:11], v[30:31]
	v_pk_add_f32 v[12:13], v[12:13], v[32:33]
	s_waitcnt lgkmcnt(0)
	v_pk_add_f32 v[2:3], v[2:3], v[6:7]
	v_pk_add_f32 v[4:5], v[4:5], v[8:9]
	s_waitcnt vmcnt(6)
	v_pk_add_f32 v[2:3], v[2:3], v[36:37]
	v_pk_add_f32 v[4:5], v[4:5], v[38:39]
	global_store_dwordx4 v[52:53], v[10:13], off sc1
	global_store_dwordx4 v[54:55], v[2:5], off sc1

.Lwi2_loop:
	s_add_i32 s22, s20, 2
	s_lshl_b32 s2, s22, 7
	s_add_i32 s23, s40, s43
	v_lshl_add_u64 v[96:97], v[66:67], 0, s[2:3]
	s_mov_b32 m0, s23
	s_add_i32 s23, s23, 0x400
	global_load_lds_dwordx4 v[96:97], off
	v_lshl_add_u64 v[96:97], v[74:75], 0, s[2:3]
	s_mov_b32 m0, s23
	s_add_i32 s23, s23, 0x400
	global_load_lds_dwordx4 v[96:97], off
	v_lshl_add_u64 v[96:97], v[68:69], 0, s[2:3]
	s_mov_b32 m0, s23
	s_add_i32 s23, s23, 0x400
	global_load_lds_dwordx4 v[96:97], off
	v_lshl_add_u64 v[96:97], v[70:71], 0, s[2:3]
	s_mov_b32 m0, s23
	s_nop 0
	global_load_lds_dwordx4 v[96:97], off
	s_mul_i32 s22, s22, 0xc0000
	s_mov_b32 s23, 0
	v_lshl_add_u64 v[176:177], v[72:73], 0, s[22:23]
	v_lshl_add_u64 v[178:179], v[176:177], 0, s[44:45]
	v_lshl_add_u64 v[180:181], v[176:177], 0, s[46:47]
	v_lshl_add_u64 v[182:183], v[176:177], 0, s[48:49]
	v_lshl_add_u64 v[184:185], v[176:177], 0, s[50:51]
	v_lshl_add_u64 v[186:187], v[176:177], 0, s[52:53]
	v_lshl_add_u64 v[188:189], v[176:177], 0, s[54:55]
	v_lshl_add_u64 v[190:191], v[176:177], 0, s[56:57]
	global_load_dwordx4 v[96:99], v[176:177], off
	global_load_dwordx4 v[100:103], v[178:179], off
	global_load_dwordx4 v[104:107], v[180:181], off
	global_load_dwordx4 v[108:111], v[182:183], off
	global_load_dwordx4 v[112:115], v[184:185], off
	global_load_dwordx4 v[116:119], v[186:187], off
	global_load_dwordx4 v[120:123], v[188:189], off
	global_load_dwordx4 v[124:127], v[190:191], off
	v_or_b32_e32 v95, s41, v88
	v_mov_b32_e32 v192, v88
	v_add3_u32 v95, v95, v89, v90
	v_add3_u32 v192, v192, v91, v90
	ds_read_b128 v[128:131], v95
	ds_read_b128 v[132:135], v192 offset:49152
	ds_read_b128 v[136:139], v95 offset:4096
	ds_read_b128 v[140:143], v192 offset:53248
	v_or_b32_e32 v95, s41, v92
	v_mov_b32_e32 v192, v92
	s_waitcnt lgkmcnt(0)
	v_mfma_f32_32x32x16_f16 v[18:33], v[136:139], v[132:135], v[18:33]
	v_mfma_f32_32x32x16_f16 v[2:17], v[136:139], v[140:143], v[2:17]
	v_add3_u32 v95, v95, v89, v90
	v_add3_u32 v192, v192, v91, v90
	v_mfma_f32_32x32x16_f16 v[50:65], v[128:131], v[132:135], v[50:65]
	v_mfma_f32_32x32x16_f16 v[34:49], v[128:131], v[140:143], v[34:49]
	ds_read_b128 v[128:131], v95
	ds_read_b128 v[132:135], v192 offset:49152
	ds_read_b128 v[136:139], v95 offset:4096
	ds_read_b128 v[140:143], v192 offset:53248
	v_or_b32_e32 v95, s41, v93
	v_mov_b32_e32 v192, v93
	s_waitcnt lgkmcnt(0)
	v_mfma_f32_32x32x16_f16 v[18:33], v[136:139], v[132:135], v[18:33]
	v_mfma_f32_32x32x16_f16 v[2:17], v[136:139], v[140:143], v[2:17]
	v_add3_u32 v95, v95, v89, v90
	v_add3_u32 v192, v192, v91, v90
	v_mfma_f32_32x32x16_f16 v[50:65], v[128:131], v[132:135], v[50:65]
	v_mfma_f32_32x32x16_f16 v[34:49], v[128:131], v[140:143], v[34:49]
	ds_read_b128 v[128:131], v95
	ds_read_b128 v[132:135], v192 offset:49152
	ds_read_b128 v[136:139], v95 offset:4096
	ds_read_b128 v[140:143], v192 offset:53248
	v_or_b32_e32 v95, s41, v94
	v_mov_b32_e32 v192, v94
	s_waitcnt lgkmcnt(0)
	v_mfma_f32_32x32x16_f16 v[18:33], v[136:139], v[132:135], v[18:33]
	v_mfma_f32_32x32x16_f16 v[2:17], v[136:139], v[140:143], v[2:17]
	v_add3_u32 v95, v95, v89, v90
	v_add3_u32 v192, v192, v91, v90
	v_mfma_f32_32x32x16_f16 v[50:65], v[128:131], v[132:135], v[50:65]
	v_mfma_f32_32x32x16_f16 v[34:49], v[128:131], v[140:143], v[34:49]
	ds_read_b128 v[128:131], v95
	ds_read_b128 v[132:135], v192 offset:49152
	ds_read_b128 v[136:139], v95 offset:4096
	ds_read_b128 v[140:143], v192 offset:53248
	s_waitcnt lgkmcnt(0)
	v_mfma_f32_32x32x16_f16 v[50:65], v[128:131], v[132:135], v[50:65]
	v_mfma_f32_32x32x16_f16 v[34:49], v[128:131], v[140:143], v[34:49]
	v_mfma_f32_32x32x16_f16 v[18:33], v[136:139], v[132:135], v[18:33]
	v_mfma_f32_32x32x16_f16 v[2:17], v[136:139], v[140:143], v[2:17]
	v_or_b32_e32 v95, 0x4000, v82
	v_or_b32_e32 v192, 0x4000, v84
	v_or_b32_e32 v193, 0x4000, v87
	v_add_u32_e32 v95, v95, v83
	v_add_u32_e32 v192, v192, v85
	v_add_u32_e32 v193, v193, v86
	s_waitcnt vmcnt(12)
	v_cvt_pk_f16_f32 v128, v144, v148
	v_cvt_pk_f16_f32 v129, v152, v156
	v_cvt_pk_f16_f32 v130, v160, v164
	v_cvt_pk_f16_f32 v131, v168, v172
	v_cvt_pk_f16_f32 v132, v145, v149
	v_cvt_pk_f16_f32 v133, v153, v157
	v_cvt_pk_f16_f32 v134, v161, v165
	v_cvt_pk_f16_f32 v135, v169, v173
	v_cvt_pk_f16_f32 v136, v146, v150
	v_cvt_pk_f16_f32 v137, v154, v158
	v_cvt_pk_f16_f32 v138, v162, v166
	v_cvt_pk_f16_f32 v139, v170, v174
	v_cvt_pk_f16_f32 v140, v147, v151
	v_cvt_pk_f16_f32 v141, v155, v159
	v_cvt_pk_f16_f32 v142, v163, v167
	v_cvt_pk_f16_f32 v143, v171, v175
	ds_write_b128 v95, v[128:131] offset:49152
	ds_write_b128 v95, v[132:135] offset:49280
	ds_write_b128 v192, v[136:139] offset:49152
	ds_write_b128 v193, v[140:143] offset:49152
	s_mov_b32 s58, s41
	s_mov_b32 s41, s42
	s_mov_b32 s42, s43
	s_mov_b32 s43, s58
	s_add_i32 s20, s20, 1
	s_waitcnt lgkmcnt(0)
	s_barrier
	s_add_i32 s22, s20, 2
	s_lshl_b32 s2, s22, 7
	s_add_i32 s23, s40, s43
	v_lshl_add_u64 v[144:145], v[66:67], 0, s[2:3]
	s_mov_b32 m0, s23
	s_add_i32 s23, s23, 0x400
	global_load_lds_dwordx4 v[144:145], off
	v_lshl_add_u64 v[144:145], v[74:75], 0, s[2:3]
	s_mov_b32 m0, s23
	s_add_i32 s23, s23, 0x400
	global_load_lds_dwordx4 v[144:145], off
	v_lshl_add_u64 v[144:145], v[68:69], 0, s[2:3]
	s_mov_b32 m0, s23
	s_add_i32 s23, s23, 0x400
	global_load_lds_dwordx4 v[144:145], off
	v_lshl_add_u64 v[144:145], v[70:71], 0, s[2:3]
	s_mov_b32 m0, s23
	s_nop 0
	global_load_lds_dwordx4 v[144:145], off
	s_mul_i32 s22, s22, 0xc0000
	s_mov_b32 s23, 0
	v_lshl_add_u64 v[176:177], v[72:73], 0, s[22:23]
	v_lshl_add_u64 v[178:179], v[176:177], 0, s[44:45]
	v_lshl_add_u64 v[180:181], v[176:177], 0, s[46:47]
	v_lshl_add_u64 v[182:183], v[176:177], 0, s[48:49]
	v_lshl_add_u64 v[184:185], v[176:177], 0, s[50:51]
	v_lshl_add_u64 v[186:187], v[176:177], 0, s[52:53]
	v_lshl_add_u64 v[188:189], v[176:177], 0, s[54:55]
	v_lshl_add_u64 v[190:191], v[176:177], 0, s[56:57]
	global_load_dwordx4 v[144:147], v[176:177], off
	global_load_dwordx4 v[148:151], v[178:179], off
	global_load_dwordx4 v[152:155], v[180:181], off
	global_load_dwordx4 v[156:159], v[182:183], off
	global_load_dwordx4 v[160:163], v[184:185], off
	global_load_dwordx4 v[164:167], v[186:187], off
	global_load_dwordx4 v[168:171], v[188:189], off
	global_load_dwordx4 v[172:175], v[190:191], off
	v_or_b32_e32 v95, s41, v88
	v_or_b32_e32 v192, 0x4000, v88
	v_add3_u32 v95, v95, v89, v90
	v_add3_u32 v192, v192, v91, v90
	ds_read_b128 v[128:131], v95
	ds_read_b128 v[132:135], v192 offset:49152
	ds_read_b128 v[136:139], v95 offset:4096
	ds_read_b128 v[140:143], v192 offset:53248
	v_or_b32_e32 v95, s41, v92
	v_or_b32_e32 v192, 0x4000, v92
	s_waitcnt lgkmcnt(0)
	v_mfma_f32_32x32x16_f16 v[18:33], v[136:139], v[132:135], v[18:33]
	v_mfma_f32_32x32x16_f16 v[2:17], v[136:139], v[140:143], v[2:17]
	v_add3_u32 v95, v95, v89, v90
	v_add3_u32 v192, v192, v91, v90
	v_mfma_f32_32x32x16_f16 v[50:65], v[128:131], v[132:135], v[50:65]
	v_mfma_f32_32x32x16_f16 v[34:49], v[128:131], v[140:143], v[34:49]
	ds_read_b128 v[128:131], v95
	ds_read_b128 v[132:135], v192 offset:49152
	ds_read_b128 v[136:139], v95 offset:4096
	ds_read_b128 v[140:143], v192 offset:53248
	v_or_b32_e32 v95, s41, v93
	v_or_b32_e32 v192, 0x4000, v93
	s_waitcnt lgkmcnt(0)
	v_mfma_f32_32x32x16_f16 v[18:33], v[136:139], v[132:135], v[18:33]
	v_mfma_f32_32x32x16_f16 v[2:17], v[136:139], v[140:143], v[2:17]
	v_add3_u32 v95, v95, v89, v90
	v_add3_u32 v192, v192, v91, v90
	v_mfma_f32_32x32x16_f16 v[50:65], v[128:131], v[132:135], v[50:65]
	v_mfma_f32_32x32x16_f16 v[34:49], v[128:131], v[140:143], v[34:49]
	ds_read_b128 v[128:131], v95
	ds_read_b128 v[132:135], v192 offset:49152
	ds_read_b128 v[136:139], v95 offset:4096
	ds_read_b128 v[140:143], v192 offset:53248
	v_or_b32_e32 v95, s41, v94
	v_or_b32_e32 v192, 0x4000, v94
	s_waitcnt lgkmcnt(0)
	v_mfma_f32_32x32x16_f16 v[18:33], v[136:139], v[132:135], v[18:33]
	v_mfma_f32_32x32x16_f16 v[2:17], v[136:139], v[140:143], v[2:17]
	v_add3_u32 v95, v95, v89, v90
	v_add3_u32 v192, v192, v91, v90
	v_mfma_f32_32x32x16_f16 v[50:65], v[128:131], v[132:135], v[50:65]
	v_mfma_f32_32x32x16_f16 v[34:49], v[128:131], v[140:143], v[34:49]
	ds_read_b128 v[128:131], v95
	ds_read_b128 v[132:135], v192 offset:49152
	ds_read_b128 v[136:139], v95 offset:4096
	ds_read_b128 v[140:143], v192 offset:53248
	s_waitcnt lgkmcnt(0)
	v_mfma_f32_32x32x16_f16 v[50:65], v[128:131], v[132:135], v[50:65]
	v_mfma_f32_32x32x16_f16 v[34:49], v[128:131], v[140:143], v[34:49]
	v_mfma_f32_32x32x16_f16 v[18:33], v[136:139], v[132:135], v[18:33]
	v_mfma_f32_32x32x16_f16 v[2:17], v[136:139], v[140:143], v[2:17]
	v_mov_b32_e32 v95, v82
	v_mov_b32_e32 v192, v84
	v_mov_b32_e32 v193, v87
	v_add_u32_e32 v95, v95, v83
	v_add_u32_e32 v192, v192, v85
	v_add_u32_e32 v193, v193, v86
	s_waitcnt vmcnt(12)
	v_cvt_pk_f16_f32 v128, v96, v100
	v_cvt_pk_f16_f32 v129, v104, v108
	v_cvt_pk_f16_f32 v130, v112, v116
	v_cvt_pk_f16_f32 v131, v120, v124
	v_cvt_pk_f16_f32 v132, v97, v101
	v_cvt_pk_f16_f32 v133, v105, v109
	v_cvt_pk_f16_f32 v134, v113, v117
	v_cvt_pk_f16_f32 v135, v121, v125
	v_cvt_pk_f16_f32 v136, v98, v102
	v_cvt_pk_f16_f32 v137, v106, v110
	v_cvt_pk_f16_f32 v138, v114, v118
	v_cvt_pk_f16_f32 v139, v122, v126
	v_cvt_pk_f16_f32 v140, v99, v103
	v_cvt_pk_f16_f32 v141, v107, v111
	v_cvt_pk_f16_f32 v142, v115, v119
	v_cvt_pk_f16_f32 v143, v123, v127
	ds_write_b128 v95, v[128:131] offset:49152
	ds_write_b128 v95, v[132:135] offset:49280
	ds_write_b128 v192, v[136:139] offset:49152
	ds_write_b128 v193, v[140:143] offset:49152
	s_mov_b32 s58, s41
	s_mov_b32 s41, s42
	s_mov_b32 s42, s43
	s_mov_b32 s43, s58
	s_add_i32 s20, s20, 1
	s_waitcnt lgkmcnt(0)
	s_barrier
	s_cmp_eq_u32 s20, 10
	s_cbranch_scc0 .Lwi2_loop
	v_or_b32_e32 v95, s41, v88
	v_mov_b32_e32 v192, v88
	v_add3_u32 v95, v95, v89, v90
	v_add3_u32 v192, v192, v91, v90
	ds_read_b128 v[128:131], v95
	ds_read_b128 v[132:135], v192 offset:49152
	ds_read_b128 v[136:139], v95 offset:4096
	ds_read_b128 v[140:143], v192 offset:53248
	v_or_b32_e32 v95, s41, v92
	v_mov_b32_e32 v192, v92
	s_waitcnt lgkmcnt(0)
	v_mfma_f32_32x32x16_f16 v[18:33], v[136:139], v[132:135], v[18:33]
	v_mfma_f32_32x32x16_f16 v[2:17], v[136:139], v[140:143], v[2:17]
	v_add3_u32 v95, v95, v89, v90
	v_add3_u32 v192, v192, v91, v90
	v_mfma_f32_32x32x16_f16 v[50:65], v[128:131], v[132:135], v[50:65]
	v_mfma_f32_32x32x16_f16 v[34:49], v[128:131], v[140:143], v[34:49]
	ds_read_b128 v[128:131], v95
	ds_read_b128 v[132:135], v192 offset:49152
	ds_read_b128 v[136:139], v95 offset:4096
	ds_read_b128 v[140:143], v192 offset:53248
	v_or_b32_e32 v95, s41, v93
	v_mov_b32_e32 v192, v93
	s_waitcnt lgkmcnt(0)
	v_mfma_f32_32x32x16_f16 v[18:33], v[136:139], v[132:135], v[18:33]
	v_mfma_f32_32x32x16_f16 v[2:17], v[136:139], v[140:143], v[2:17]
	v_add3_u32 v95, v95, v89, v90
	v_add3_u32 v192, v192, v91, v90
	v_mfma_f32_32x32x16_f16 v[50:65], v[128:131], v[132:135], v[50:65]
	v_mfma_f32_32x32x16_f16 v[34:49], v[128:131], v[140:143], v[34:49]
	ds_read_b128 v[128:131], v95
	ds_read_b128 v[132:135], v192 offset:49152
	ds_read_b128 v[136:139], v95 offset:4096
	ds_read_b128 v[140:143], v192 offset:53248
	v_or_b32_e32 v95, s41, v94
	v_mov_b32_e32 v192, v94
	s_waitcnt lgkmcnt(0)
	v_mfma_f32_32x32x16_f16 v[18:33], v[136:139], v[132:135], v[18:33]
	v_mfma_f32_32x32x16_f16 v[2:17], v[136:139], v[140:143], v[2:17]
	v_add3_u32 v95, v95, v89, v90
	v_add3_u32 v192, v192, v91, v90
	v_mfma_f32_32x32x16_f16 v[50:65], v[128:131], v[132:135], v[50:65]
	v_mfma_f32_32x32x16_f16 v[34:49], v[128:131], v[140:143], v[34:49]
	ds_read_b128 v[128:131], v95
	ds_read_b128 v[132:135], v192 offset:49152
	ds_read_b128 v[136:139], v95 offset:4096
	ds_read_b128 v[140:143], v192 offset:53248
	s_waitcnt lgkmcnt(0)
	v_mfma_f32_32x32x16_f16 v[50:65], v[128:131], v[132:135], v[50:65]
	v_mfma_f32_32x32x16_f16 v[34:49], v[128:131], v[140:143], v[34:49]
	v_mfma_f32_32x32x16_f16 v[18:33], v[136:139], v[132:135], v[18:33]
	v_mfma_f32_32x32x16_f16 v[2:17], v[136:139], v[140:143], v[2:17]
	v_or_b32_e32 v95, 0x4000, v82
	v_or_b32_e32 v192, 0x4000, v84
	v_or_b32_e32 v193, 0x4000, v87
	v_add_u32_e32 v95, v95, v83
	v_add_u32_e32 v192, v192, v85
	v_add_u32_e32 v193, v193, v86
	s_waitcnt vmcnt(0)
	v_cvt_pk_f16_f32 v128, v144, v148
	v_cvt_pk_f16_f32 v129, v152, v156
	v_cvt_pk_f16_f32 v130, v160, v164
	v_cvt_pk_f16_f32 v131, v168, v172
	v_cvt_pk_f16_f32 v132, v145, v149
	v_cvt_pk_f16_f32 v133, v153, v157
	v_cvt_pk_f16_f32 v134, v161, v165
	v_cvt_pk_f16_f32 v135, v169, v173
	v_cvt_pk_f16_f32 v136, v146, v150
	v_cvt_pk_f16_f32 v137, v154, v158
	v_cvt_pk_f16_f32 v138, v162, v166
	v_cvt_pk_f16_f32 v139, v170, v174
	v_cvt_pk_f16_f32 v140, v147, v151
	v_cvt_pk_f16_f32 v141, v155, v159
	v_cvt_pk_f16_f32 v142, v163, v167
	v_cvt_pk_f16_f32 v143, v171, v175
	ds_write_b128 v95, v[128:131] offset:49152
	ds_write_b128 v95, v[132:135] offset:49280
	ds_write_b128 v192, v[136:139] offset:49152
	ds_write_b128 v193, v[140:143] offset:49152
	s_mov_b32 s58, s41
	s_mov_b32 s41, s42
	s_mov_b32 s42, s43
	s_mov_b32 s43, s58
	s_add_i32 s20, s20, 1
	s_waitcnt lgkmcnt(0)
	s_barrier
	v_or_b32_e32 v95, s41, v88
	v_or_b32_e32 v192, 0x4000, v88
	v_add3_u32 v95, v95, v89, v90
	v_add3_u32 v192, v192, v91, v90
	ds_read_b128 v[128:131], v95
	ds_read_b128 v[132:135], v192 offset:49152
	ds_read_b128 v[136:139], v95 offset:4096
	ds_read_b128 v[140:143], v192 offset:53248
	v_or_b32_e32 v95, s41, v92
	v_or_b32_e32 v192, 0x4000, v92
	s_waitcnt lgkmcnt(0)
	v_mfma_f32_32x32x16_f16 v[18:33], v[136:139], v[132:135], v[18:33]
	v_mfma_f32_32x32x16_f16 v[2:17], v[136:139], v[140:143], v[2:17]
	v_add3_u32 v95, v95, v89, v90
	v_add3_u32 v192, v192, v91, v90
	v_mfma_f32_32x32x16_f16 v[50:65], v[128:131], v[132:135], v[50:65]
	v_mfma_f32_32x32x16_f16 v[34:49], v[128:131], v[140:143], v[34:49]
	ds_read_b128 v[128:131], v95
	ds_read_b128 v[132:135], v192 offset:49152
	ds_read_b128 v[136:139], v95 offset:4096
	ds_read_b128 v[140:143], v192 offset:53248
	v_or_b32_e32 v95, s41, v93
	v_or_b32_e32 v192, 0x4000, v93
	s_waitcnt lgkmcnt(0)
	v_mfma_f32_32x32x16_f16 v[18:33], v[136:139], v[132:135], v[18:33]
	v_mfma_f32_32x32x16_f16 v[2:17], v[136:139], v[140:143], v[2:17]
	v_add3_u32 v95, v95, v89, v90
	v_add3_u32 v192, v192, v91, v90
	v_mfma_f32_32x32x16_f16 v[50:65], v[128:131], v[132:135], v[50:65]
	v_mfma_f32_32x32x16_f16 v[34:49], v[128:131], v[140:143], v[34:49]
	ds_read_b128 v[128:131], v95
	ds_read_b128 v[132:135], v192 offset:49152
	ds_read_b128 v[136:139], v95 offset:4096
	ds_read_b128 v[140:143], v192 offset:53248
	v_or_b32_e32 v95, s41, v94
	v_or_b32_e32 v192, 0x4000, v94
	s_waitcnt lgkmcnt(0)
	v_mfma_f32_32x32x16_f16 v[18:33], v[136:139], v[132:135], v[18:33]
	v_mfma_f32_32x32x16_f16 v[2:17], v[136:139], v[140:143], v[2:17]
	v_add3_u32 v95, v95, v89, v90
	v_add3_u32 v192, v192, v91, v90
	v_mfma_f32_32x32x16_f16 v[50:65], v[128:131], v[132:135], v[50:65]
	v_mfma_f32_32x32x16_f16 v[34:49], v[128:131], v[140:143], v[34:49]
	ds_read_b128 v[128:131], v95
	ds_read_b128 v[132:135], v192 offset:49152
	ds_read_b128 v[136:139], v95 offset:4096
	ds_read_b128 v[140:143], v192 offset:53248
	s_waitcnt lgkmcnt(0)
	v_mfma_f32_32x32x16_f16 v[50:65], v[128:131], v[132:135], v[50:65]
	v_mfma_f32_32x32x16_f16 v[34:49], v[128:131], v[140:143], v[34:49]
	v_mfma_f32_32x32x16_f16 v[18:33], v[136:139], v[132:135], v[18:33]
	v_mfma_f32_32x32x16_f16 v[2:17], v[136:139], v[140:143], v[2:17]
	v_mul_u32_u24_e32 v66, 0x4400, v1
	v_lshl_or_b32 v1, v78, 2, v66
	s_movk_i32 s4, 0x440
	v_mad_u32_u24 v1, v77, s4, v1
	s_waitcnt vmcnt(0)
	s_barrier
	ds_write2_b32 v1, v50, v34 offset1:32
	ds_write2_b32 v1, v51, v35 offset0:68 offset1:100
	ds_write2_b32 v1, v52, v36 offset0:136 offset1:168
	ds_write2_b32 v1, v53, v37 offset0:204 offset1:236
	v_add_u32_e32 v34, 0x800, v1
	ds_write2_b32 v34, v54, v38 offset0:32 offset1:64
	ds_write2_b32 v34, v55, v39 offset0:100 offset1:132
	ds_write2_b32 v34, v56, v40 offset0:168 offset1:200
	v_add_u32_e32 v34, 0xa00, v1
	ds_write2_b32 v34, v57, v41 offset0:108 offset1:140
	v_add_u32_e32 v34, 0x1000, v1
	ds_write2_b32 v34, v58, v42 offset0:64 offset1:96
	ds_write2_b32 v34, v59, v43 offset0:132 offset1:164
	ds_write2_b32 v34, v60, v44 offset0:200 offset1:232
	v_add_u32_e32 v34, 0x1400, v1
	ds_write2_b32 v34, v61, v45 offset0:12 offset1:44
	v_add_u32_e32 v34, 0x1800, v1
	ds_write2_b32 v34, v62, v46 offset0:96 offset1:128
	ds_write2_b32 v34, v63, v47 offset0:164 offset1:196
	v_add_u32_e32 v34, 0x1a00, v1
	ds_write2_b32 v34, v64, v48 offset0:104 offset1:136
	v_add_u32_e32 v34, 0x1c00, v1
	ds_write2_b32 v34, v65, v49 offset0:44 offset1:76
	v_add_u32_e32 v34, 0x2000, v1
	ds_write2_b32 v34, v18, v2 offset0:128 offset1:160
	ds_write2_b32 v34, v19, v3 offset0:196 offset1:228
	v_add_u32_e32 v2, 0x2400, v1
	ds_write2_b32 v2, v20, v4 offset0:8 offset1:40
	ds_write2_b32 v2, v21, v5 offset0:76 offset1:108
	v_add_u32_e32 v2, 0x2800, v1
	ds_write2_b32 v2, v22, v6 offset0:160 offset1:192
	v_add_u32_e32 v2, 0x2a00, v1
	ds_write2_b32 v2, v23, v7 offset0:100 offset1:132
	v_add_u32_e32 v2, 0x2c00, v1
	ds_write2_b32 v2, v24, v8 offset0:40 offset1:72
	ds_write2_b32 v2, v25, v9 offset0:108 offset1:140
	v_add_u32_e32 v2, 0x3000, v1
	s_mul_i32 s2, s12, 0x3000
	ds_write2_b32 v2, v26, v10 offset0:192 offset1:224
	v_add_u32_e32 v2, 0x3400, v1
	s_mul_hi_u32 s3, s12, 0x3000
	ds_write2_b32 v2, v27, v11 offset0:4 offset1:36
	ds_write2_b32 v2, v28, v12 offset0:72 offset1:104
	ds_write2_b32 v2, v29, v13 offset0:140 offset1:172
	v_add_u32_e32 v2, 0x3a00, v1
	s_add_u32 s2, s6, s2
	v_lshlrev_b32_e32 v0, 3, v0
	ds_write2_b32 v2, v30, v14 offset0:96 offset1:128
	s_addc_u32 s3, s7, s3
	v_lshl_or_b32 v8, v80, 6, s10
	v_mov_b32_e32 v9, 0
	v_and_b32_e32 v14, 56, v0
	v_lshl_add_u64 v[2:3], v[8:9], 2, s[2:3]
	v_lshlrev_b32_e32 v12, 2, v14
	v_mov_b32_e32 v13, v9
	v_add_u32_e32 v1, 0x3c00, v1
	v_lshl_add_u64 v[10:11], v[2:3], 0, v[12:13]
	ds_write2_b32 v1, v31, v15 offset0:36 offset1:68
	ds_write2_b32 v1, v32, v16 offset0:104 offset1:136
	ds_write2_b32 v1, v33, v17 offset0:172 offset1:204
	global_load_dwordx4 v[4:7], v[10:11], off offset:16
	global_load_dwordx4 v[0:3], v[10:11], off
	v_lshl_add_u32 v10, v79, 6, s8
	v_or_b32_e32 v11, v66, v12
	v_lshl_add_u64 v[12:13], v[8:9], 1, s[0:1]
	v_lshlrev_b32_e32 v8, 1, v14
	v_lshl_add_u64 v[8:9], v[12:13], 0, v[8:9]
	v_add_u32_e32 v12, v10, v76
	v_cmp_gt_i32_e32 vcc, s9, v12
	s_and_saveexec_b64 s[0:1], vcc
	s_cbranch_execz .LBB13_6
	s_movk_i32 s2, 0x110
	v_mad_u32_u24 v13, v76, s2, v11
	ds_read_b128 v[14:17], v13 offset:16
	ds_read_b128 v[18:21], v13
	s_mov_b32 s4, 0x3f3504f3
	s_mov_b32 s8, 0x3ea7ba05
	s_mov_b32 s10, 0xbfba00e3
	s_waitcnt vmcnt(1) lgkmcnt(1)
	v_pk_add_f32 v[16:17], v[6:7], v[16:17]
	s_brev_b32 s3, -2
	v_pk_mul_f32 v[22:23], v[16:17], 0.5 op_sel_hi:[1,0]
	v_pk_mul_f32 v[16:17], v[16:17], s[4:5] op_sel_hi:[1,0]
	s_mov_b32 s2, 0xbfb8aa3b
	v_and_b32_e32 v24, 0x7fffffff, v16
	v_and_b32_e32 v25, 0x7fffffff, v17
	v_pk_mul_f32 v[26:27], v[24:25], v[24:25]
	v_pk_fma_f32 v[24:25], v[24:25], s[8:9], 1.0 op_sel_hi:[1,0,0]
	s_mov_b32 s6, 0x3f87dc22
	v_rcp_f32_e32 v24, v24
	v_rcp_f32_e32 v25, v25
	v_mov_b64_e32 v[28:29], s[10:11]
	v_pk_mul_f32 v[26:27], v[26:27], s[2:3] op_sel_hi:[1,0]
	s_mov_b32 s10, 0x3fb5f0e3
	v_pk_fma_f32 v[30:31], v[24:25], s[6:7], v[28:29] op_sel_hi:[1,0,0]
	v_exp_f32_e32 v26, v26
	v_exp_f32_e32 v27, v27
	v_pk_fma_f32 v[30:31], v[24:25], v[30:31], s[10:11] op_sel_hi:[1,1,0]
	s_mov_b32 s12, 0xbe91a98e
	v_pk_fma_f32 v[30:31], v[24:25], v[30:31], s[12:13] op_sel_hi:[1,1,0]
	s_mov_b32 s14, 0x3e827906
	v_pk_fma_f32 v[30:31], v[24:25], v[30:31], s[14:15] op_sel_hi:[1,1,0]
	v_pk_add_f32 v[14:15], v[4:5], v[14:15]
	v_pk_mul_f32 v[24:25], v[24:25], v[30:31]
	s_waitcnt vmcnt(0) lgkmcnt(0)
	v_pk_add_f32 v[18:19], v[0:1], v[18:19]
	v_pk_fma_f32 v[24:25], v[26:27], v[24:25], 1.0 op_sel_hi:[1,1,0] neg_lo:[1,0,0] neg_hi:[1,0,0]
	s_nop 0
	v_bfi_b32 v17, s3, v25, v17
	v_bfi_b32 v16, s3, v24, v16
	v_pk_add_f32 v[16:17], v[16:17], 1.0 op_sel_hi:[1,0]
	s_nop 0
	v_pk_mul_f32 v[16:17], v[22:23], v[16:17]
	v_pk_mul_f32 v[22:23], v[14:15], 0.5 op_sel_hi:[1,0]
	v_pk_mul_f32 v[14:15], v[14:15], s[4:5] op_sel_hi:[1,0]
	v_cvt_pk_f16_f32 v17, v16, v17
	v_and_b32_e32 v24, 0x7fffffff, v14
	v_and_b32_e32 v25, 0x7fffffff, v15
	v_pk_mul_f32 v[26:27], v[24:25], v[24:25]
	v_pk_fma_f32 v[24:25], v[24:25], s[8:9], 1.0 op_sel_hi:[1,0,0]
	v_pk_mul_f32 v[26:27], v[26:27], s[2:3] op_sel_hi:[1,0]
	v_rcp_f32_e32 v24, v24
	v_rcp_f32_e32 v25, v25
	v_exp_f32_e32 v26, v26
	v_exp_f32_e32 v27, v27
	v_pk_fma_f32 v[30:31], v[24:25], s[6:7], v[28:29] op_sel_hi:[1,0,0]
	s_nop 0
	v_pk_fma_f32 v[30:31], v[24:25], v[30:31], s[10:11] op_sel_hi:[1,1,0]
	s_nop 0
	v_pk_fma_f32 v[30:31], v[24:25], v[30:31], s[12:13] op_sel_hi:[1,1,0]
	s_nop 0
	v_pk_fma_f32 v[30:31], v[24:25], v[30:31], s[14:15] op_sel_hi:[1,1,0]
	s_nop 0
	v_pk_mul_f32 v[24:25], v[24:25], v[30:31]
	s_nop 0
	v_pk_fma_f32 v[24:25], v[26:27], v[24:25], 1.0 op_sel_hi:[1,1,0] neg_lo:[1,0,0] neg_hi:[1,0,0]
	s_nop 0
	v_bfi_b32 v15, s3, v25, v15
	v_bfi_b32 v14, s3, v24, v14
	v_pk_add_f32 v[14:15], v[14:15], 1.0 op_sel_hi:[1,0]
	s_nop 0
	v_pk_mul_f32 v[22:23], v[22:23], v[14:15]
	v_pk_add_f32 v[14:15], v[2:3], v[20:21]
	v_cvt_pk_f16_f32 v16, v22, v23
	v_pk_mul_f32 v[20:21], v[14:15], 0.5 op_sel_hi:[1,0]
	v_pk_mul_f32 v[14:15], v[14:15], s[4:5] op_sel_hi:[1,0]
	s_nop 0
	v_and_b32_e32 v24, 0x7fffffff, v14
	v_and_b32_e32 v25, 0x7fffffff, v15
	v_pk_mul_f32 v[26:27], v[24:25], v[24:25]
	v_pk_fma_f32 v[24:25], v[24:25], s[8:9], 1.0 op_sel_hi:[1,0,0]
	v_pk_mul_f32 v[26:27], v[26:27], s[2:3] op_sel_hi:[1,0]
	v_rcp_f32_e32 v24, v24
	v_rcp_f32_e32 v25, v25
	v_exp_f32_e32 v26, v26
	v_exp_f32_e32 v27, v27
	v_pk_fma_f32 v[30:31], v[24:25], s[6:7], v[28:29] op_sel_hi:[1,0,0]
	s_nop 0
	v_pk_fma_f32 v[30:31], v[24:25], v[30:31], s[10:11] op_sel_hi:[1,1,0]
	s_nop 0
	v_pk_fma_f32 v[30:31], v[24:25], v[30:31], s[12:13] op_sel_hi:[1,1,0]
	s_nop 0
	v_pk_fma_f32 v[30:31], v[24:25], v[30:31], s[14:15] op_sel_hi:[1,1,0]
	s_nop 0
	v_pk_mul_f32 v[24:25], v[24:25], v[30:31]
	s_nop 0
	v_pk_fma_f32 v[24:25], v[26:27], v[24:25], 1.0 op_sel_hi:[1,1,0] neg_lo:[1,0,0] neg_hi:[1,0,0]
	s_nop 0
	v_bfi_b32 v15, s3, v25, v15
	v_bfi_b32 v14, s3, v24, v14
	v_pk_add_f32 v[14:15], v[14:15], 1.0 op_sel_hi:[1,0]
	s_nop 0
	v_pk_mul_f32 v[14:15], v[20:21], v[14:15]
	v_pk_mul_f32 v[20:21], v[18:19], 0.5 op_sel_hi:[1,0]
	v_pk_mul_f32 v[18:19], v[18:19], s[4:5] op_sel_hi:[1,0]
	v_cvt_pk_f16_f32 v15, v14, v15
	v_and_b32_e32 v24, 0x7fffffff, v18
	v_and_b32_e32 v25, 0x7fffffff, v19
	v_pk_mul_f32 v[26:27], v[24:25], v[24:25]
	v_pk_fma_f32 v[24:25], v[24:25], s[8:9], 1.0 op_sel_hi:[1,0,0]
	v_pk_mul_f32 v[26:27], v[26:27], s[2:3] op_sel_hi:[1,0]
	v_rcp_f32_e32 v24, v24
	v_rcp_f32_e32 v25, v25
	v_exp_f32_e32 v26, v26
	v_exp_f32_e32 v27, v27
	s_movk_i32 s2, 0x1880
	v_pk_fma_f32 v[28:29], v[24:25], s[6:7], v[28:29] op_sel_hi:[1,0,0]
	s_nop 0
	v_pk_fma_f32 v[28:29], v[24:25], v[28:29], s[10:11] op_sel_hi:[1,1,0]
	s_nop 0
	v_pk_fma_f32 v[28:29], v[24:25], v[28:29], s[12:13] op_sel_hi:[1,1,0]
	s_nop 0
	v_pk_fma_f32 v[28:29], v[24:25], v[28:29], s[14:15] op_sel_hi:[1,1,0]
	s_nop 0
	v_pk_mul_f32 v[24:25], v[24:25], v[28:29]
	s_nop 0
	v_pk_fma_f32 v[24:25], v[26:27], v[24:25], 1.0 op_sel_hi:[1,1,0] neg_lo:[1,0,0] neg_hi:[1,0,0]
	s_nop 0
	v_bfi_b32 v19, s3, v25, v19
	v_bfi_b32 v18, s3, v24, v18
	v_pk_add_f32 v[18:19], v[18:19], 1.0 op_sel_hi:[1,0]
	v_mad_i64_i32 v[12:13], s[2:3], v12, s2, v[8:9]
	v_pk_mul_f32 v[18:19], v[20:21], v[18:19]
	s_nop 0
	v_cvt_pk_f16_f32 v14, v18, v19
	global_store_dwordx4 v[12:13], v[14:17], off sc1
.LBB13_6:
	s_or_b64 exec, exec, s[0:1]
	v_or_b32_e32 v13, 8, v76
	v_add_u32_e32 v12, v10, v13
	v_cmp_gt_i32_e32 vcc, s9, v12
	s_and_saveexec_b64 s[0:1], vcc
	s_cbranch_execz .LBB13_8
	s_movk_i32 s2, 0x110
	v_mad_u32_u24 v13, v13, s2, v11
	ds_read_b128 v[14:17], v13 offset:16
	ds_read_b128 v[18:21], v13
	s_mov_b32 s4, 0x3f3504f3
	s_mov_b32 s8, 0x3ea7ba05
	s_mov_b32 s10, 0xbfba00e3
	s_waitcnt vmcnt(1) lgkmcnt(1)
	v_pk_add_f32 v[16:17], v[6:7], v[16:17]
	s_brev_b32 s3, -2
	v_pk_mul_f32 v[22:23], v[16:17], 0.5 op_sel_hi:[1,0]
	v_pk_mul_f32 v[16:17], v[16:17], s[4:5] op_sel_hi:[1,0]
	s_mov_b32 s2, 0xbfb8aa3b
	v_and_b32_e32 v24, 0x7fffffff, v16
	v_and_b32_e32 v25, 0x7fffffff, v17
	v_pk_mul_f32 v[26:27], v[24:25], v[24:25]
	v_pk_fma_f32 v[24:25], v[24:25], s[8:9], 1.0 op_sel_hi:[1,0,0]
	s_mov_b32 s6, 0x3f87dc22
	v_rcp_f32_e32 v24, v24
	v_rcp_f32_e32 v25, v25
	v_mov_b64_e32 v[28:29], s[10:11]
	v_pk_mul_f32 v[26:27], v[26:27], s[2:3] op_sel_hi:[1,0]
	s_mov_b32 s10, 0x3fb5f0e3
	v_pk_fma_f32 v[30:31], v[24:25], s[6:7], v[28:29] op_sel_hi:[1,0,0]
	v_exp_f32_e32 v26, v26
	v_exp_f32_e32 v27, v27
	v_pk_fma_f32 v[30:31], v[24:25], v[30:31], s[10:11] op_sel_hi:[1,1,0]
	s_mov_b32 s12, 0xbe91a98e
	v_pk_fma_f32 v[30:31], v[24:25], v[30:31], s[12:13] op_sel_hi:[1,1,0]
	s_mov_b32 s14, 0x3e827906
	v_pk_fma_f32 v[30:31], v[24:25], v[30:31], s[14:15] op_sel_hi:[1,1,0]
	v_pk_add_f32 v[14:15], v[4:5], v[14:15]
	v_pk_mul_f32 v[24:25], v[24:25], v[30:31]
	s_waitcnt vmcnt(0) lgkmcnt(0)
	v_pk_add_f32 v[18:19], v[0:1], v[18:19]
	v_pk_fma_f32 v[24:25], v[26:27], v[24:25], 1.0 op_sel_hi:[1,1,0] neg_lo:[1,0,0] neg_hi:[1,0,0]
	s_nop 0
	v_bfi_b32 v17, s3, v25, v17
	v_bfi_b32 v16, s3, v24, v16
	v_pk_add_f32 v[16:17], v[16:17], 1.0 op_sel_hi:[1,0]
	s_nop 0
	v_pk_mul_f32 v[16:17], v[22:23], v[16:17]
	v_pk_mul_f32 v[22:23], v[14:15], 0.5 op_sel_hi:[1,0]
	v_pk_mul_f32 v[14:15], v[14:15], s[4:5] op_sel_hi:[1,0]
	v_cvt_pk_f16_f32 v17, v16, v17
	v_and_b32_e32 v24, 0x7fffffff, v14
	v_and_b32_e32 v25, 0x7fffffff, v15
	v_pk_mul_f32 v[26:27], v[24:25], v[24:25]
	v_pk_fma_f32 v[24:25], v[24:25], s[8:9], 1.0 op_sel_hi:[1,0,0]
	v_pk_mul_f32 v[26:27], v[26:27], s[2:3] op_sel_hi:[1,0]
	v_rcp_f32_e32 v24, v24
	v_rcp_f32_e32 v25, v25
	v_exp_f32_e32 v26, v26
	v_exp_f32_e32 v27, v27
	v_pk_fma_f32 v[30:31], v[24:25], s[6:7], v[28:29] op_sel_hi:[1,0,0]
	s_nop 0
	v_pk_fma_f32 v[30:31], v[24:25], v[30:31], s[10:11] op_sel_hi:[1,1,0]
	s_nop 0
	v_pk_fma_f32 v[30:31], v[24:25], v[30:31], s[12:13] op_sel_hi:[1,1,0]
	s_nop 0
	v_pk_fma_f32 v[30:31], v[24:25], v[30:31], s[14:15] op_sel_hi:[1,1,0]
	s_nop 0
	v_pk_mul_f32 v[24:25], v[24:25], v[30:31]
	s_nop 0
	v_pk_fma_f32 v[24:25], v[26:27], v[24:25], 1.0 op_sel_hi:[1,1,0] neg_lo:[1,0,0] neg_hi:[1,0,0]
	s_nop 0
	v_bfi_b32 v15, s3, v25, v15
	v_bfi_b32 v14, s3, v24, v14
	v_pk_add_f32 v[14:15], v[14:15], 1.0 op_sel_hi:[1,0]
	s_nop 0
	v_pk_mul_f32 v[22:23], v[22:23], v[14:15]
	v_pk_add_f32 v[14:15], v[2:3], v[20:21]
	v_cvt_pk_f16_f32 v16, v22, v23
	v_pk_mul_f32 v[20:21], v[14:15], 0.5 op_sel_hi:[1,0]
	v_pk_mul_f32 v[14:15], v[14:15], s[4:5] op_sel_hi:[1,0]
	s_nop 0
	v_and_b32_e32 v24, 0x7fffffff, v14
	v_and_b32_e32 v25, 0x7fffffff, v15
	v_pk_mul_f32 v[26:27], v[24:25], v[24:25]
	v_pk_fma_f32 v[24:25], v[24:25], s[8:9], 1.0 op_sel_hi:[1,0,0]
	v_pk_mul_f32 v[26:27], v[26:27], s[2:3] op_sel_hi:[1,0]
	v_rcp_f32_e32 v24, v24
	v_rcp_f32_e32 v25, v25
	v_exp_f32_e32 v26, v26
	v_exp_f32_e32 v27, v27
	v_pk_fma_f32 v[30:31], v[24:25], s[6:7], v[28:29] op_sel_hi:[1,0,0]
	s_nop 0
	v_pk_fma_f32 v[30:31], v[24:25], v[30:31], s[10:11] op_sel_hi:[1,1,0]
	s_nop 0
	v_pk_fma_f32 v[30:31], v[24:25], v[30:31], s[12:13] op_sel_hi:[1,1,0]
	s_nop 0
	v_pk_fma_f32 v[30:31], v[24:25], v[30:31], s[14:15] op_sel_hi:[1,1,0]
	s_nop 0
	v_pk_mul_f32 v[24:25], v[24:25], v[30:31]
	s_nop 0
	v_pk_fma_f32 v[24:25], v[26:27], v[24:25], 1.0 op_sel_hi:[1,1,0] neg_lo:[1,0,0] neg_hi:[1,0,0]
	s_nop 0
	v_bfi_b32 v15, s3, v25, v15
	v_bfi_b32 v14, s3, v24, v14
	v_pk_add_f32 v[14:15], v[14:15], 1.0 op_sel_hi:[1,0]
	s_nop 0
	v_pk_mul_f32 v[14:15], v[20:21], v[14:15]
	v_pk_mul_f32 v[20:21], v[18:19], 0.5 op_sel_hi:[1,0]
	v_pk_mul_f32 v[18:19], v[18:19], s[4:5] op_sel_hi:[1,0]
	v_cvt_pk_f16_f32 v15, v14, v15
	v_and_b32_e32 v24, 0x7fffffff, v18
	v_and_b32_e32 v25, 0x7fffffff, v19
	v_pk_mul_f32 v[26:27], v[24:25], v[24:25]
	v_pk_fma_f32 v[24:25], v[24:25], s[8:9], 1.0 op_sel_hi:[1,0,0]
	v_pk_mul_f32 v[26:27], v[26:27], s[2:3] op_sel_hi:[1,0]
	v_rcp_f32_e32 v24, v24
	v_rcp_f32_e32 v25, v25
	v_exp_f32_e32 v26, v26
	v_exp_f32_e32 v27, v27
	s_movk_i32 s2, 0x1880
	v_pk_fma_f32 v[28:29], v[24:25], s[6:7], v[28:29] op_sel_hi:[1,0,0]
	s_nop 0
	v_pk_fma_f32 v[28:29], v[24:25], v[28:29], s[10:11] op_sel_hi:[1,1,0]
	s_nop 0
	v_pk_fma_f32 v[28:29], v[24:25], v[28:29], s[12:13] op_sel_hi:[1,1,0]
	s_nop 0
	v_pk_fma_f32 v[28:29], v[24:25], v[28:29], s[14:15] op_sel_hi:[1,1,0]
	s_nop 0
	v_pk_mul_f32 v[24:25], v[24:25], v[28:29]
	s_nop 0
	v_pk_fma_f32 v[24:25], v[26:27], v[24:25], 1.0 op_sel_hi:[1,1,0] neg_lo:[1,0,0] neg_hi:[1,0,0]
	s_nop 0
	v_bfi_b32 v19, s3, v25, v19
	v_bfi_b32 v18, s3, v24, v18
	v_pk_add_f32 v[18:19], v[18:19], 1.0 op_sel_hi:[1,0]
	v_mad_i64_i32 v[12:13], s[2:3], v12, s2, v[8:9]
	v_pk_mul_f32 v[18:19], v[20:21], v[18:19]
	s_nop 0
	v_cvt_pk_f16_f32 v14, v18, v19
	global_store_dwordx4 v[12:13], v[14:17], off sc1
.LBB13_8:
	s_or_b64 exec, exec, s[0:1]
	v_or_b32_e32 v13, 16, v76
	v_add_u32_e32 v12, v10, v13
	v_cmp_gt_i32_e32 vcc, s9, v12
	s_and_saveexec_b64 s[0:1], vcc
	s_cbranch_execz .LBB13_10
	s_movk_i32 s2, 0x110
	v_mad_u32_u24 v13, v13, s2, v11
	ds_read_b128 v[14:17], v13 offset:16
	ds_read_b128 v[18:21], v13
	s_mov_b32 s4, 0x3f3504f3
	s_mov_b32 s8, 0x3ea7ba05
	s_mov_b32 s10, 0xbfba00e3
	s_waitcnt vmcnt(1) lgkmcnt(1)
	v_pk_add_f32 v[16:17], v[6:7], v[16:17]
	s_brev_b32 s3, -2
	v_pk_mul_f32 v[22:23], v[16:17], 0.5 op_sel_hi:[1,0]
	v_pk_mul_f32 v[16:17], v[16:17], s[4:5] op_sel_hi:[1,0]
	s_mov_b32 s2, 0xbfb8aa3b
	v_and_b32_e32 v24, 0x7fffffff, v16
	v_and_b32_e32 v25, 0x7fffffff, v17
	v_pk_mul_f32 v[26:27], v[24:25], v[24:25]
	v_pk_fma_f32 v[24:25], v[24:25], s[8:9], 1.0 op_sel_hi:[1,0,0]
	s_mov_b32 s6, 0x3f87dc22
	v_rcp_f32_e32 v24, v24
	v_rcp_f32_e32 v25, v25
	v_mov_b64_e32 v[28:29], s[10:11]
	v_pk_mul_f32 v[26:27], v[26:27], s[2:3] op_sel_hi:[1,0]
	s_mov_b32 s10, 0x3fb5f0e3
	v_pk_fma_f32 v[30:31], v[24:25], s[6:7], v[28:29] op_sel_hi:[1,0,0]
	v_exp_f32_e32 v26, v26
	v_exp_f32_e32 v27, v27
	v_pk_fma_f32 v[30:31], v[24:25], v[30:31], s[10:11] op_sel_hi:[1,1,0]
	s_mov_b32 s12, 0xbe91a98e
	v_pk_fma_f32 v[30:31], v[24:25], v[30:31], s[12:13] op_sel_hi:[1,1,0]
	s_mov_b32 s14, 0x3e827906
	v_pk_fma_f32 v[30:31], v[24:25], v[30:31], s[14:15] op_sel_hi:[1,1,0]
	v_pk_add_f32 v[14:15], v[4:5], v[14:15]
	v_pk_mul_f32 v[24:25], v[24:25], v[30:31]
	s_waitcnt vmcnt(0) lgkmcnt(0)
	v_pk_add_f32 v[18:19], v[0:1], v[18:19]
	v_pk_fma_f32 v[24:25], v[26:27], v[24:25], 1.0 op_sel_hi:[1,1,0] neg_lo:[1,0,0] neg_hi:[1,0,0]
	s_nop 0
	v_bfi_b32 v17, s3, v25, v17
	v_bfi_b32 v16, s3, v24, v16
	v_pk_add_f32 v[16:17], v[16:17], 1.0 op_sel_hi:[1,0]
	s_nop 0
	v_pk_mul_f32 v[16:17], v[22:23], v[16:17]
	v_pk_mul_f32 v[22:23], v[14:15], 0.5 op_sel_hi:[1,0]
	v_pk_mul_f32 v[14:15], v[14:15], s[4:5] op_sel_hi:[1,0]
	v_cvt_pk_f16_f32 v17, v16, v17
	v_and_b32_e32 v24, 0x7fffffff, v14
	v_and_b32_e32 v25, 0x7fffffff, v15
	v_pk_mul_f32 v[26:27], v[24:25], v[24:25]
	v_pk_fma_f32 v[24:25], v[24:25], s[8:9], 1.0 op_sel_hi:[1,0,0]
	v_pk_mul_f32 v[26:27], v[26:27], s[2:3] op_sel_hi:[1,0]
	v_rcp_f32_e32 v24, v24
	v_rcp_f32_e32 v25, v25
	v_exp_f32_e32 v26, v26
	v_exp_f32_e32 v27, v27
	v_pk_fma_f32 v[30:31], v[24:25], s[6:7], v[28:29] op_sel_hi:[1,0,0]
	s_nop 0
	v_pk_fma_f32 v[30:31], v[24:25], v[30:31], s[10:11] op_sel_hi:[1,1,0]
	s_nop 0
	v_pk_fma_f32 v[30:31], v[24:25], v[30:31], s[12:13] op_sel_hi:[1,1,0]
	s_nop 0
	v_pk_fma_f32 v[30:31], v[24:25], v[30:31], s[14:15] op_sel_hi:[1,1,0]
	s_nop 0
	v_pk_mul_f32 v[24:25], v[24:25], v[30:31]
	s_nop 0
	v_pk_fma_f32 v[24:25], v[26:27], v[24:25], 1.0 op_sel_hi:[1,1,0] neg_lo:[1,0,0] neg_hi:[1,0,0]
	s_nop 0
	v_bfi_b32 v15, s3, v25, v15
	v_bfi_b32 v14, s3, v24, v14
	v_pk_add_f32 v[14:15], v[14:15], 1.0 op_sel_hi:[1,0]
	s_nop 0
	v_pk_mul_f32 v[22:23], v[22:23], v[14:15]
	v_pk_add_f32 v[14:15], v[2:3], v[20:21]
	v_cvt_pk_f16_f32 v16, v22, v23
	v_pk_mul_f32 v[20:21], v[14:15], 0.5 op_sel_hi:[1,0]
	v_pk_mul_f32 v[14:15], v[14:15], s[4:5] op_sel_hi:[1,0]
	s_nop 0
	v_and_b32_e32 v24, 0x7fffffff, v14
	v_and_b32_e32 v25, 0x7fffffff, v15
	v_pk_mul_f32 v[26:27], v[24:25], v[24:25]
	v_pk_fma_f32 v[24:25], v[24:25], s[8:9], 1.0 op_sel_hi:[1,0,0]
	v_pk_mul_f32 v[26:27], v[26:27], s[2:3] op_sel_hi:[1,0]
	v_rcp_f32_e32 v24, v24
	v_rcp_f32_e32 v25, v25
	v_exp_f32_e32 v26, v26
	v_exp_f32_e32 v27, v27
	v_pk_fma_f32 v[30:31], v[24:25], s[6:7], v[28:29] op_sel_hi:[1,0,0]
	s_nop 0
	v_pk_fma_f32 v[30:31], v[24:25], v[30:31], s[10:11] op_sel_hi:[1,1,0]
	s_nop 0
	v_pk_fma_f32 v[30:31], v[24:25], v[30:31], s[12:13] op_sel_hi:[1,1,0]
	s_nop 0
	v_pk_fma_f32 v[30:31], v[24:25], v[30:31], s[14:15] op_sel_hi:[1,1,0]
	s_nop 0
	v_pk_mul_f32 v[24:25], v[24:25], v[30:31]
	s_nop 0
	v_pk_fma_f32 v[24:25], v[26:27], v[24:25], 1.0 op_sel_hi:[1,1,0] neg_lo:[1,0,0] neg_hi:[1,0,0]
	s_nop 0
	v_bfi_b32 v15, s3, v25, v15
	v_bfi_b32 v14, s3, v24, v14
	v_pk_add_f32 v[14:15], v[14:15], 1.0 op_sel_hi:[1,0]
	s_nop 0
	v_pk_mul_f32 v[14:15], v[20:21], v[14:15]
	v_pk_mul_f32 v[20:21], v[18:19], 0.5 op_sel_hi:[1,0]
	v_pk_mul_f32 v[18:19], v[18:19], s[4:5] op_sel_hi:[1,0]
	v_cvt_pk_f16_f32 v15, v14, v15
	v_and_b32_e32 v24, 0x7fffffff, v18
	v_and_b32_e32 v25, 0x7fffffff, v19
	v_pk_mul_f32 v[26:27], v[24:25], v[24:25]
	v_pk_fma_f32 v[24:25], v[24:25], s[8:9], 1.0 op_sel_hi:[1,0,0]
	v_pk_mul_f32 v[26:27], v[26:27], s[2:3] op_sel_hi:[1,0]
	v_rcp_f32_e32 v24, v24
	v_rcp_f32_e32 v25, v25
	v_exp_f32_e32 v26, v26
	v_exp_f32_e32 v27, v27
	s_movk_i32 s2, 0x1880
	v_pk_fma_f32 v[28:29], v[24:25], s[6:7], v[28:29] op_sel_hi:[1,0,0]
	s_nop 0
	v_pk_fma_f32 v[28:29], v[24:25], v[28:29], s[10:11] op_sel_hi:[1,1,0]
	s_nop 0
	v_pk_fma_f32 v[28:29], v[24:25], v[28:29], s[12:13] op_sel_hi:[1,1,0]
	s_nop 0
	v_pk_fma_f32 v[28:29], v[24:25], v[28:29], s[14:15] op_sel_hi:[1,1,0]
	s_nop 0
	v_pk_mul_f32 v[24:25], v[24:25], v[28:29]
	s_nop 0
	v_pk_fma_f32 v[24:25], v[26:27], v[24:25], 1.0 op_sel_hi:[1,1,0] neg_lo:[1,0,0] neg_hi:[1,0,0]
	s_nop 0
	v_bfi_b32 v19, s3, v25, v19
	v_bfi_b32 v18, s3, v24, v18
	v_pk_add_f32 v[18:19], v[18:19], 1.0 op_sel_hi:[1,0]
	v_mad_i64_i32 v[12:13], s[2:3], v12, s2, v[8:9]
	v_pk_mul_f32 v[18:19], v[20:21], v[18:19]
	s_nop 0
	v_cvt_pk_f16_f32 v14, v18, v19
	global_store_dwordx4 v[12:13], v[14:17], off sc1
.LBB13_10:
	s_or_b64 exec, exec, s[0:1]
	v_or_b32_e32 v13, 24, v76
	v_add_u32_e32 v12, v10, v13
	v_cmp_gt_i32_e32 vcc, s9, v12
	s_and_saveexec_b64 s[0:1], vcc
	s_cbranch_execz .LBB13_12
	s_movk_i32 s2, 0x110
	v_mad_u32_u24 v13, v13, s2, v11
	ds_read_b128 v[14:17], v13 offset:16
	ds_read_b128 v[18:21], v13
	s_mov_b32 s4, 0x3f3504f3
	s_mov_b32 s8, 0x3ea7ba05
	s_mov_b32 s10, 0xbfba00e3
	s_waitcnt vmcnt(1) lgkmcnt(1)
	v_pk_add_f32 v[16:17], v[6:7], v[16:17]
	s_brev_b32 s3, -2
	v_pk_mul_f32 v[22:23], v[16:17], 0.5 op_sel_hi:[1,0]
	v_pk_mul_f32 v[16:17], v[16:17], s[4:5] op_sel_hi:[1,0]
	s_mov_b32 s2, 0xbfb8aa3b
	v_and_b32_e32 v24, 0x7fffffff, v16
	v_and_b32_e32 v25, 0x7fffffff, v17
	v_pk_mul_f32 v[26:27], v[24:25], v[24:25]
	v_pk_fma_f32 v[24:25], v[24:25], s[8:9], 1.0 op_sel_hi:[1,0,0]
	s_mov_b32 s6, 0x3f87dc22
	v_rcp_f32_e32 v24, v24
	v_rcp_f32_e32 v25, v25
	v_mov_b64_e32 v[28:29], s[10:11]
	v_pk_mul_f32 v[26:27], v[26:27], s[2:3] op_sel_hi:[1,0]
	s_mov_b32 s10, 0x3fb5f0e3
	v_pk_fma_f32 v[30:31], v[24:25], s[6:7], v[28:29] op_sel_hi:[1,0,0]
	v_exp_f32_e32 v26, v26
	v_exp_f32_e32 v27, v27
	v_pk_fma_f32 v[30:31], v[24:25], v[30:31], s[10:11] op_sel_hi:[1,1,0]
	s_mov_b32 s12, 0xbe91a98e
	v_pk_fma_f32 v[30:31], v[24:25], v[30:31], s[12:13] op_sel_hi:[1,1,0]
	s_mov_b32 s14, 0x3e827906
	v_pk_fma_f32 v[30:31], v[24:25], v[30:31], s[14:15] op_sel_hi:[1,1,0]
	v_pk_add_f32 v[14:15], v[4:5], v[14:15]
	v_pk_mul_f32 v[24:25], v[24:25], v[30:31]
	s_waitcnt vmcnt(0) lgkmcnt(0)
	v_pk_add_f32 v[18:19], v[0:1], v[18:19]
	v_pk_fma_f32 v[24:25], v[26:27], v[24:25], 1.0 op_sel_hi:[1,1,0] neg_lo:[1,0,0] neg_hi:[1,0,0]
	s_nop 0
	v_bfi_b32 v17, s3, v25, v17
	v_bfi_b32 v16, s3, v24, v16
	v_pk_add_f32 v[16:17], v[16:17], 1.0 op_sel_hi:[1,0]
	s_nop 0
	v_pk_mul_f32 v[16:17], v[22:23], v[16:17]
	v_pk_mul_f32 v[22:23], v[14:15], 0.5 op_sel_hi:[1,0]
	v_pk_mul_f32 v[14:15], v[14:15], s[4:5] op_sel_hi:[1,0]
	v_cvt_pk_f16_f32 v17, v16, v17
	v_and_b32_e32 v24, 0x7fffffff, v14
	v_and_b32_e32 v25, 0x7fffffff, v15
	v_pk_mul_f32 v[26:27], v[24:25], v[24:25]
	v_pk_fma_f32 v[24:25], v[24:25], s[8:9], 1.0 op_sel_hi:[1,0,0]
	v_pk_mul_f32 v[26:27], v[26:27], s[2:3] op_sel_hi:[1,0]
	v_rcp_f32_e32 v24, v24
	v_rcp_f32_e32 v25, v25
	v_exp_f32_e32 v26, v26
	v_exp_f32_e32 v27, v27
	v_pk_fma_f32 v[30:31], v[24:25], s[6:7], v[28:29] op_sel_hi:[1,0,0]
	s_nop 0
	v_pk_fma_f32 v[30:31], v[24:25], v[30:31], s[10:11] op_sel_hi:[1,1,0]
	s_nop 0
	v_pk_fma_f32 v[30:31], v[24:25], v[30:31], s[12:13] op_sel_hi:[1,1,0]
	s_nop 0
	v_pk_fma_f32 v[30:31], v[24:25], v[30:31], s[14:15] op_sel_hi:[1,1,0]
	s_nop 0
	v_pk_mul_f32 v[24:25], v[24:25], v[30:31]
	s_nop 0
	v_pk_fma_f32 v[24:25], v[26:27], v[24:25], 1.0 op_sel_hi:[1,1,0] neg_lo:[1,0,0] neg_hi:[1,0,0]
	s_nop 0
	v_bfi_b32 v15, s3, v25, v15
	v_bfi_b32 v14, s3, v24, v14
	v_pk_add_f32 v[14:15], v[14:15], 1.0 op_sel_hi:[1,0]
	s_nop 0
	v_pk_mul_f32 v[22:23], v[22:23], v[14:15]
	v_pk_add_f32 v[14:15], v[2:3], v[20:21]
	v_cvt_pk_f16_f32 v16, v22, v23
	v_pk_mul_f32 v[20:21], v[14:15], 0.5 op_sel_hi:[1,0]
	v_pk_mul_f32 v[14:15], v[14:15], s[4:5] op_sel_hi:[1,0]
	s_nop 0
	v_and_b32_e32 v24, 0x7fffffff, v14
	v_and_b32_e32 v25, 0x7fffffff, v15
	v_pk_mul_f32 v[26:27], v[24:25], v[24:25]
	v_pk_fma_f32 v[24:25], v[24:25], s[8:9], 1.0 op_sel_hi:[1,0,0]
	v_pk_mul_f32 v[26:27], v[26:27], s[2:3] op_sel_hi:[1,0]
	v_rcp_f32_e32 v24, v24
	v_rcp_f32_e32 v25, v25
	v_exp_f32_e32 v26, v26
	v_exp_f32_e32 v27, v27
	v_pk_fma_f32 v[30:31], v[24:25], s[6:7], v[28:29] op_sel_hi:[1,0,0]
	s_nop 0
	v_pk_fma_f32 v[30:31], v[24:25], v[30:31], s[10:11] op_sel_hi:[1,1,0]
	s_nop 0
	v_pk_fma_f32 v[30:31], v[24:25], v[30:31], s[12:13] op_sel_hi:[1,1,0]
	s_nop 0
	v_pk_fma_f32 v[30:31], v[24:25], v[30:31], s[14:15] op_sel_hi:[1,1,0]
	s_nop 0
	v_pk_mul_f32 v[24:25], v[24:25], v[30:31]
	s_nop 0
	v_pk_fma_f32 v[24:25], v[26:27], v[24:25], 1.0 op_sel_hi:[1,1,0] neg_lo:[1,0,0] neg_hi:[1,0,0]
	s_nop 0
	v_bfi_b32 v15, s3, v25, v15
	v_bfi_b32 v14, s3, v24, v14
	v_pk_add_f32 v[14:15], v[14:15], 1.0 op_sel_hi:[1,0]
	s_nop 0
	v_pk_mul_f32 v[14:15], v[20:21], v[14:15]
	v_pk_mul_f32 v[20:21], v[18:19], 0.5 op_sel_hi:[1,0]
	v_pk_mul_f32 v[18:19], v[18:19], s[4:5] op_sel_hi:[1,0]
	v_cvt_pk_f16_f32 v15, v14, v15
	v_and_b32_e32 v24, 0x7fffffff, v18
	v_and_b32_e32 v25, 0x7fffffff, v19
	v_pk_mul_f32 v[26:27], v[24:25], v[24:25]
	v_pk_fma_f32 v[24:25], v[24:25], s[8:9], 1.0 op_sel_hi:[1,0,0]
	v_pk_mul_f32 v[26:27], v[26:27], s[2:3] op_sel_hi:[1,0]
	v_rcp_f32_e32 v24, v24
	v_rcp_f32_e32 v25, v25
	v_exp_f32_e32 v26, v26
	v_exp_f32_e32 v27, v27
	s_movk_i32 s2, 0x1880
	v_pk_fma_f32 v[28:29], v[24:25], s[6:7], v[28:29] op_sel_hi:[1,0,0]
	s_nop 0
	v_pk_fma_f32 v[28:29], v[24:25], v[28:29], s[10:11] op_sel_hi:[1,1,0]
	s_nop 0
	v_pk_fma_f32 v[28:29], v[24:25], v[28:29], s[12:13] op_sel_hi:[1,1,0]
	s_nop 0
	v_pk_fma_f32 v[28:29], v[24:25], v[28:29], s[14:15] op_sel_hi:[1,1,0]
	s_nop 0
	v_pk_mul_f32 v[24:25], v[24:25], v[28:29]
	s_nop 0
	v_pk_fma_f32 v[24:25], v[26:27], v[24:25], 1.0 op_sel_hi:[1,1,0] neg_lo:[1,0,0] neg_hi:[1,0,0]
	s_nop 0
	v_bfi_b32 v19, s3, v25, v19
	v_bfi_b32 v18, s3, v24, v18
	v_pk_add_f32 v[18:19], v[18:19], 1.0 op_sel_hi:[1,0]
	v_mad_i64_i32 v[12:13], s[2:3], v12, s2, v[8:9]
	v_pk_mul_f32 v[18:19], v[20:21], v[18:19]
	s_nop 0
	v_cvt_pk_f16_f32 v14, v18, v19
	global_store_dwordx4 v[12:13], v[14:17], off sc1
.LBB13_12:
	s_or_b64 exec, exec, s[0:1]
	v_or_b32_e32 v13, 32, v76
	v_add_u32_e32 v12, v10, v13
	v_cmp_gt_i32_e32 vcc, s9, v12
	s_and_saveexec_b64 s[0:1], vcc
	s_cbranch_execz .LBB13_14
	s_movk_i32 s2, 0x110
	v_mad_u32_u24 v13, v13, s2, v11
	ds_read_b128 v[14:17], v13 offset:16
	ds_read_b128 v[18:21], v13
	s_mov_b32 s4, 0x3f3504f3
	s_mov_b32 s8, 0x3ea7ba05
	s_mov_b32 s10, 0xbfba00e3
	s_waitcnt vmcnt(1) lgkmcnt(1)
	v_pk_add_f32 v[16:17], v[6:7], v[16:17]
	s_brev_b32 s3, -2
	v_pk_mul_f32 v[22:23], v[16:17], 0.5 op_sel_hi:[1,0]
	v_pk_mul_f32 v[16:17], v[16:17], s[4:5] op_sel_hi:[1,0]
	s_mov_b32 s2, 0xbfb8aa3b
	v_and_b32_e32 v24, 0x7fffffff, v16
	v_and_b32_e32 v25, 0x7fffffff, v17
	v_pk_mul_f32 v[26:27], v[24:25], v[24:25]
	v_pk_fma_f32 v[24:25], v[24:25], s[8:9], 1.0 op_sel_hi:[1,0,0]
	s_mov_b32 s6, 0x3f87dc22
	v_rcp_f32_e32 v24, v24
	v_rcp_f32_e32 v25, v25
	v_mov_b64_e32 v[28:29], s[10:11]
	v_pk_mul_f32 v[26:27], v[26:27], s[2:3] op_sel_hi:[1,0]
	s_mov_b32 s10, 0x3fb5f0e3
	v_pk_fma_f32 v[30:31], v[24:25], s[6:7], v[28:29] op_sel_hi:[1,0,0]
	v_exp_f32_e32 v26, v26
	v_exp_f32_e32 v27, v27
	v_pk_fma_f32 v[30:31], v[24:25], v[30:31], s[10:11] op_sel_hi:[1,1,0]
	s_mov_b32 s12, 0xbe91a98e
	v_pk_fma_f32 v[30:31], v[24:25], v[30:31], s[12:13] op_sel_hi:[1,1,0]
	s_mov_b32 s14, 0x3e827906
	v_pk_fma_f32 v[30:31], v[24:25], v[30:31], s[14:15] op_sel_hi:[1,1,0]
	v_pk_add_f32 v[14:15], v[4:5], v[14:15]
	v_pk_mul_f32 v[24:25], v[24:25], v[30:31]
	s_waitcnt vmcnt(0) lgkmcnt(0)
	v_pk_add_f32 v[18:19], v[0:1], v[18:19]
	v_pk_fma_f32 v[24:25], v[26:27], v[24:25], 1.0 op_sel_hi:[1,1,0] neg_lo:[1,0,0] neg_hi:[1,0,0]
	s_nop 0
	v_bfi_b32 v17, s3, v25, v17
	v_bfi_b32 v16, s3, v24, v16
	v_pk_add_f32 v[16:17], v[16:17], 1.0 op_sel_hi:[1,0]
	s_nop 0
	v_pk_mul_f32 v[16:17], v[22:23], v[16:17]
	v_pk_mul_f32 v[22:23], v[14:15], 0.5 op_sel_hi:[1,0]
	v_pk_mul_f32 v[14:15], v[14:15], s[4:5] op_sel_hi:[1,0]
	v_cvt_pk_f16_f32 v17, v16, v17
	v_and_b32_e32 v24, 0x7fffffff, v14
	v_and_b32_e32 v25, 0x7fffffff, v15
	v_pk_mul_f32 v[26:27], v[24:25], v[24:25]
	v_pk_fma_f32 v[24:25], v[24:25], s[8:9], 1.0 op_sel_hi:[1,0,0]
	v_pk_mul_f32 v[26:27], v[26:27], s[2:3] op_sel_hi:[1,0]
	v_rcp_f32_e32 v24, v24
	v_rcp_f32_e32 v25, v25
	v_exp_f32_e32 v26, v26
	v_exp_f32_e32 v27, v27
	v_pk_fma_f32 v[30:31], v[24:25], s[6:7], v[28:29] op_sel_hi:[1,0,0]
	s_nop 0
	v_pk_fma_f32 v[30:31], v[24:25], v[30:31], s[10:11] op_sel_hi:[1,1,0]
	s_nop 0
	v_pk_fma_f32 v[30:31], v[24:25], v[30:31], s[12:13] op_sel_hi:[1,1,0]
	s_nop 0
	v_pk_fma_f32 v[30:31], v[24:25], v[30:31], s[14:15] op_sel_hi:[1,1,0]
	s_nop 0
	v_pk_mul_f32 v[24:25], v[24:25], v[30:31]
	s_nop 0
	v_pk_fma_f32 v[24:25], v[26:27], v[24:25], 1.0 op_sel_hi:[1,1,0] neg_lo:[1,0,0] neg_hi:[1,0,0]
	s_nop 0
	v_bfi_b32 v15, s3, v25, v15
	v_bfi_b32 v14, s3, v24, v14
	v_pk_add_f32 v[14:15], v[14:15], 1.0 op_sel_hi:[1,0]
	s_nop 0
	v_pk_mul_f32 v[22:23], v[22:23], v[14:15]
	v_pk_add_f32 v[14:15], v[2:3], v[20:21]
	v_cvt_pk_f16_f32 v16, v22, v23
	v_pk_mul_f32 v[20:21], v[14:15], 0.5 op_sel_hi:[1,0]
	v_pk_mul_f32 v[14:15], v[14:15], s[4:5] op_sel_hi:[1,0]
	s_nop 0
	v_and_b32_e32 v24, 0x7fffffff, v14
	v_and_b32_e32 v25, 0x7fffffff, v15
	v_pk_mul_f32 v[26:27], v[24:25], v[24:25]
	v_pk_fma_f32 v[24:25], v[24:25], s[8:9], 1.0 op_sel_hi:[1,0,0]
	v_pk_mul_f32 v[26:27], v[26:27], s[2:3] op_sel_hi:[1,0]
	v_rcp_f32_e32 v24, v24
	v_rcp_f32_e32 v25, v25
	v_exp_f32_e32 v26, v26
	v_exp_f32_e32 v27, v27
	v_pk_fma_f32 v[30:31], v[24:25], s[6:7], v[28:29] op_sel_hi:[1,0,0]
	s_nop 0
	v_pk_fma_f32 v[30:31], v[24:25], v[30:31], s[10:11] op_sel_hi:[1,1,0]
	s_nop 0
	v_pk_fma_f32 v[30:31], v[24:25], v[30:31], s[12:13] op_sel_hi:[1,1,0]
	s_nop 0
	v_pk_fma_f32 v[30:31], v[24:25], v[30:31], s[14:15] op_sel_hi:[1,1,0]
	s_nop 0
	v_pk_mul_f32 v[24:25], v[24:25], v[30:31]
	s_nop 0
	v_pk_fma_f32 v[24:25], v[26:27], v[24:25], 1.0 op_sel_hi:[1,1,0] neg_lo:[1,0,0] neg_hi:[1,0,0]
	s_nop 0
	v_bfi_b32 v15, s3, v25, v15
	v_bfi_b32 v14, s3, v24, v14
	v_pk_add_f32 v[14:15], v[14:15], 1.0 op_sel_hi:[1,0]
	s_nop 0
	v_pk_mul_f32 v[14:15], v[20:21], v[14:15]
	v_pk_mul_f32 v[20:21], v[18:19], 0.5 op_sel_hi:[1,0]
	v_pk_mul_f32 v[18:19], v[18:19], s[4:5] op_sel_hi:[1,0]
	v_cvt_pk_f16_f32 v15, v14, v15
	v_and_b32_e32 v24, 0x7fffffff, v18
	v_and_b32_e32 v25, 0x7fffffff, v19
	v_pk_mul_f32 v[26:27], v[24:25], v[24:25]
	v_pk_fma_f32 v[24:25], v[24:25], s[8:9], 1.0 op_sel_hi:[1,0,0]
	v_pk_mul_f32 v[26:27], v[26:27], s[2:3] op_sel_hi:[1,0]
	v_rcp_f32_e32 v24, v24
	v_rcp_f32_e32 v25, v25
	v_exp_f32_e32 v26, v26
	v_exp_f32_e32 v27, v27
	s_movk_i32 s2, 0x1880
	v_pk_fma_f32 v[28:29], v[24:25], s[6:7], v[28:29] op_sel_hi:[1,0,0]
	s_nop 0
	v_pk_fma_f32 v[28:29], v[24:25], v[28:29], s[10:11] op_sel_hi:[1,1,0]
	s_nop 0
	v_pk_fma_f32 v[28:29], v[24:25], v[28:29], s[12:13] op_sel_hi:[1,1,0]
	s_nop 0
	v_pk_fma_f32 v[28:29], v[24:25], v[28:29], s[14:15] op_sel_hi:[1,1,0]
	s_nop 0
	v_pk_mul_f32 v[24:25], v[24:25], v[28:29]
	s_nop 0
	v_pk_fma_f32 v[24:25], v[26:27], v[24:25], 1.0 op_sel_hi:[1,1,0] neg_lo:[1,0,0] neg_hi:[1,0,0]
	s_nop 0
	v_bfi_b32 v19, s3, v25, v19
	v_bfi_b32 v18, s3, v24, v18
	v_pk_add_f32 v[18:19], v[18:19], 1.0 op_sel_hi:[1,0]
	v_mad_i64_i32 v[12:13], s[2:3], v12, s2, v[8:9]
	v_pk_mul_f32 v[18:19], v[20:21], v[18:19]
	s_nop 0
	v_cvt_pk_f16_f32 v14, v18, v19
	global_store_dwordx4 v[12:13], v[14:17], off sc1
.LBB13_14:
	s_or_b64 exec, exec, s[0:1]
	v_or_b32_e32 v13, 40, v76
	v_add_u32_e32 v12, v10, v13
	v_cmp_gt_i32_e32 vcc, s9, v12
	s_and_saveexec_b64 s[0:1], vcc
	s_cbranch_execz .LBB13_16
	s_movk_i32 s2, 0x110
	v_mad_u32_u24 v13, v13, s2, v11
	ds_read_b128 v[14:17], v13 offset:16
	ds_read_b128 v[18:21], v13
	s_mov_b32 s4, 0x3f3504f3
	s_mov_b32 s8, 0x3ea7ba05
	s_mov_b32 s10, 0xbfba00e3
	s_waitcnt vmcnt(1) lgkmcnt(1)
	v_pk_add_f32 v[16:17], v[6:7], v[16:17]
	s_brev_b32 s3, -2
	v_pk_mul_f32 v[22:23], v[16:17], 0.5 op_sel_hi:[1,0]
	v_pk_mul_f32 v[16:17], v[16:17], s[4:5] op_sel_hi:[1,0]
	s_mov_b32 s2, 0xbfb8aa3b
	v_and_b32_e32 v24, 0x7fffffff, v16
	v_and_b32_e32 v25, 0x7fffffff, v17
	v_pk_mul_f32 v[26:27], v[24:25], v[24:25]
	v_pk_fma_f32 v[24:25], v[24:25], s[8:9], 1.0 op_sel_hi:[1,0,0]
	s_mov_b32 s6, 0x3f87dc22
	v_rcp_f32_e32 v24, v24
	v_rcp_f32_e32 v25, v25
	v_mov_b64_e32 v[28:29], s[10:11]
	v_pk_mul_f32 v[26:27], v[26:27], s[2:3] op_sel_hi:[1,0]
	s_mov_b32 s10, 0x3fb5f0e3
	v_pk_fma_f32 v[30:31], v[24:25], s[6:7], v[28:29] op_sel_hi:[1,0,0]
	v_exp_f32_e32 v26, v26
	v_exp_f32_e32 v27, v27
	v_pk_fma_f32 v[30:31], v[24:25], v[30:31], s[10:11] op_sel_hi:[1,1,0]
	s_mov_b32 s12, 0xbe91a98e
	v_pk_fma_f32 v[30:31], v[24:25], v[30:31], s[12:13] op_sel_hi:[1,1,0]
	s_mov_b32 s14, 0x3e827906
	v_pk_fma_f32 v[30:31], v[24:25], v[30:31], s[14:15] op_sel_hi:[1,1,0]
	v_pk_add_f32 v[14:15], v[4:5], v[14:15]
	v_pk_mul_f32 v[24:25], v[24:25], v[30:31]
	s_waitcnt vmcnt(0) lgkmcnt(0)
	v_pk_add_f32 v[18:19], v[0:1], v[18:19]
	v_pk_fma_f32 v[24:25], v[26:27], v[24:25], 1.0 op_sel_hi:[1,1,0] neg_lo:[1,0,0] neg_hi:[1,0,0]
	s_nop 0
	v_bfi_b32 v17, s3, v25, v17
	v_bfi_b32 v16, s3, v24, v16
	v_pk_add_f32 v[16:17], v[16:17], 1.0 op_sel_hi:[1,0]
	s_nop 0
	v_pk_mul_f32 v[16:17], v[22:23], v[16:17]
	v_pk_mul_f32 v[22:23], v[14:15], 0.5 op_sel_hi:[1,0]
	v_pk_mul_f32 v[14:15], v[14:15], s[4:5] op_sel_hi:[1,0]
	v_cvt_pk_f16_f32 v17, v16, v17
	v_and_b32_e32 v24, 0x7fffffff, v14
	v_and_b32_e32 v25, 0x7fffffff, v15
	v_pk_mul_f32 v[26:27], v[24:25], v[24:25]
	v_pk_fma_f32 v[24:25], v[24:25], s[8:9], 1.0 op_sel_hi:[1,0,0]
	v_pk_mul_f32 v[26:27], v[26:27], s[2:3] op_sel_hi:[1,0]
	v_rcp_f32_e32 v24, v24
	v_rcp_f32_e32 v25, v25
	v_exp_f32_e32 v26, v26
	v_exp_f32_e32 v27, v27
	v_pk_fma_f32 v[30:31], v[24:25], s[6:7], v[28:29] op_sel_hi:[1,0,0]
	s_nop 0
	v_pk_fma_f32 v[30:31], v[24:25], v[30:31], s[10:11] op_sel_hi:[1,1,0]
	s_nop 0
	v_pk_fma_f32 v[30:31], v[24:25], v[30:31], s[12:13] op_sel_hi:[1,1,0]
	s_nop 0
	v_pk_fma_f32 v[30:31], v[24:25], v[30:31], s[14:15] op_sel_hi:[1,1,0]
	s_nop 0
	v_pk_mul_f32 v[24:25], v[24:25], v[30:31]
	s_nop 0
	v_pk_fma_f32 v[24:25], v[26:27], v[24:25], 1.0 op_sel_hi:[1,1,0] neg_lo:[1,0,0] neg_hi:[1,0,0]
	s_nop 0
	v_bfi_b32 v15, s3, v25, v15
	v_bfi_b32 v14, s3, v24, v14
	v_pk_add_f32 v[14:15], v[14:15], 1.0 op_sel_hi:[1,0]
	s_nop 0
	v_pk_mul_f32 v[22:23], v[22:23], v[14:15]
	v_pk_add_f32 v[14:15], v[2:3], v[20:21]
	v_cvt_pk_f16_f32 v16, v22, v23
	v_pk_mul_f32 v[20:21], v[14:15], 0.5 op_sel_hi:[1,0]
	v_pk_mul_f32 v[14:15], v[14:15], s[4:5] op_sel_hi:[1,0]
	s_nop 0
	v_and_b32_e32 v24, 0x7fffffff, v14
	v_and_b32_e32 v25, 0x7fffffff, v15
	v_pk_mul_f32 v[26:27], v[24:25], v[24:25]
	v_pk_fma_f32 v[24:25], v[24:25], s[8:9], 1.0 op_sel_hi:[1,0,0]
	v_pk_mul_f32 v[26:27], v[26:27], s[2:3] op_sel_hi:[1,0]
	v_rcp_f32_e32 v24, v24
	v_rcp_f32_e32 v25, v25
	v_exp_f32_e32 v26, v26
	v_exp_f32_e32 v27, v27
	v_pk_fma_f32 v[30:31], v[24:25], s[6:7], v[28:29] op_sel_hi:[1,0,0]
	s_nop 0
	v_pk_fma_f32 v[30:31], v[24:25], v[30:31], s[10:11] op_sel_hi:[1,1,0]
	s_nop 0
	v_pk_fma_f32 v[30:31], v[24:25], v[30:31], s[12:13] op_sel_hi:[1,1,0]
	s_nop 0
	v_pk_fma_f32 v[30:31], v[24:25], v[30:31], s[14:15] op_sel_hi:[1,1,0]
	s_nop 0
	v_pk_mul_f32 v[24:25], v[24:25], v[30:31]
	s_nop 0
	v_pk_fma_f32 v[24:25], v[26:27], v[24:25], 1.0 op_sel_hi:[1,1,0] neg_lo:[1,0,0] neg_hi:[1,0,0]
	s_nop 0
	v_bfi_b32 v15, s3, v25, v15
	v_bfi_b32 v14, s3, v24, v14
	v_pk_add_f32 v[14:15], v[14:15], 1.0 op_sel_hi:[1,0]
	s_nop 0
	v_pk_mul_f32 v[14:15], v[20:21], v[14:15]
	v_pk_mul_f32 v[20:21], v[18:19], 0.5 op_sel_hi:[1,0]
	v_pk_mul_f32 v[18:19], v[18:19], s[4:5] op_sel_hi:[1,0]
	v_cvt_pk_f16_f32 v15, v14, v15
	v_and_b32_e32 v24, 0x7fffffff, v18
	v_and_b32_e32 v25, 0x7fffffff, v19
	v_pk_mul_f32 v[26:27], v[24:25], v[24:25]
	v_pk_fma_f32 v[24:25], v[24:25], s[8:9], 1.0 op_sel_hi:[1,0,0]
	v_pk_mul_f32 v[26:27], v[26:27], s[2:3] op_sel_hi:[1,0]
	v_rcp_f32_e32 v24, v24
	v_rcp_f32_e32 v25, v25
	v_exp_f32_e32 v26, v26
	v_exp_f32_e32 v27, v27
	s_movk_i32 s2, 0x1880
	v_pk_fma_f32 v[28:29], v[24:25], s[6:7], v[28:29] op_sel_hi:[1,0,0]
	s_nop 0
	v_pk_fma_f32 v[28:29], v[24:25], v[28:29], s[10:11] op_sel_hi:[1,1,0]
	s_nop 0
	v_pk_fma_f32 v[28:29], v[24:25], v[28:29], s[12:13] op_sel_hi:[1,1,0]
	s_nop 0
	v_pk_fma_f32 v[28:29], v[24:25], v[28:29], s[14:15] op_sel_hi:[1,1,0]
	s_nop 0
	v_pk_mul_f32 v[24:25], v[24:25], v[28:29]
	s_nop 0
	v_pk_fma_f32 v[24:25], v[26:27], v[24:25], 1.0 op_sel_hi:[1,1,0] neg_lo:[1,0,0] neg_hi:[1,0,0]
	s_nop 0
	v_bfi_b32 v19, s3, v25, v19
	v_bfi_b32 v18, s3, v24, v18
	v_pk_add_f32 v[18:19], v[18:19], 1.0 op_sel_hi:[1,0]
	v_mad_i64_i32 v[12:13], s[2:3], v12, s2, v[8:9]
	v_pk_mul_f32 v[18:19], v[20:21], v[18:19]
	s_nop 0
	v_cvt_pk_f16_f32 v14, v18, v19
	global_store_dwordx4 v[12:13], v[14:17], off sc1
.LBB13_16:
	s_or_b64 exec, exec, s[0:1]
	v_or_b32_e32 v13, 48, v76
	v_add_u32_e32 v12, v10, v13
	v_cmp_gt_i32_e32 vcc, s9, v12
	s_and_saveexec_b64 s[0:1], vcc
	s_cbranch_execz .LBB13_18
	s_movk_i32 s2, 0x110
	v_mad_u32_u24 v13, v13, s2, v11
	ds_read_b128 v[14:17], v13 offset:16
	ds_read_b128 v[18:21], v13
	s_mov_b32 s4, 0x3f3504f3
	s_mov_b32 s8, 0x3ea7ba05
	s_mov_b32 s10, 0xbfba00e3
	s_waitcnt vmcnt(1) lgkmcnt(1)
	v_pk_add_f32 v[16:17], v[6:7], v[16:17]
	s_brev_b32 s3, -2
	v_pk_mul_f32 v[22:23], v[16:17], 0.5 op_sel_hi:[1,0]
	v_pk_mul_f32 v[16:17], v[16:17], s[4:5] op_sel_hi:[1,0]
	s_mov_b32 s2, 0xbfb8aa3b
	v_and_b32_e32 v24, 0x7fffffff, v16
	v_and_b32_e32 v25, 0x7fffffff, v17
	v_pk_mul_f32 v[26:27], v[24:25], v[24:25]
	v_pk_fma_f32 v[24:25], v[24:25], s[8:9], 1.0 op_sel_hi:[1,0,0]
	s_mov_b32 s6, 0x3f87dc22
	v_rcp_f32_e32 v24, v24
	v_rcp_f32_e32 v25, v25
	v_mov_b64_e32 v[28:29], s[10:11]
	v_pk_mul_f32 v[26:27], v[26:27], s[2:3] op_sel_hi:[1,0]
	s_mov_b32 s10, 0x3fb5f0e3
	v_pk_fma_f32 v[30:31], v[24:25], s[6:7], v[28:29] op_sel_hi:[1,0,0]
	v_exp_f32_e32 v26, v26
	v_exp_f32_e32 v27, v27
	v_pk_fma_f32 v[30:31], v[24:25], v[30:31], s[10:11] op_sel_hi:[1,1,0]
	s_mov_b32 s12, 0xbe91a98e
	v_pk_fma_f32 v[30:31], v[24:25], v[30:31], s[12:13] op_sel_hi:[1,1,0]
	s_mov_b32 s14, 0x3e827906
	v_pk_fma_f32 v[30:31], v[24:25], v[30:31], s[14:15] op_sel_hi:[1,1,0]
	v_pk_add_f32 v[14:15], v[4:5], v[14:15]
	v_pk_mul_f32 v[24:25], v[24:25], v[30:31]
	s_waitcnt vmcnt(0) lgkmcnt(0)
	v_pk_add_f32 v[18:19], v[0:1], v[18:19]
	v_pk_fma_f32 v[24:25], v[26:27], v[24:25], 1.0 op_sel_hi:[1,1,0] neg_lo:[1,0,0] neg_hi:[1,0,0]
	s_nop 0
	v_bfi_b32 v17, s3, v25, v17
	v_bfi_b32 v16, s3, v24, v16
	v_pk_add_f32 v[16:17], v[16:17], 1.0 op_sel_hi:[1,0]
	s_nop 0
	v_pk_mul_f32 v[16:17], v[22:23], v[16:17]
	v_pk_mul_f32 v[22:23], v[14:15], 0.5 op_sel_hi:[1,0]
	v_pk_mul_f32 v[14:15], v[14:15], s[4:5] op_sel_hi:[1,0]
	v_cvt_pk_f16_f32 v17, v16, v17
	v_and_b32_e32 v24, 0x7fffffff, v14
	v_and_b32_e32 v25, 0x7fffffff, v15
	v_pk_mul_f32 v[26:27], v[24:25], v[24:25]
	v_pk_fma_f32 v[24:25], v[24:25], s[8:9], 1.0 op_sel_hi:[1,0,0]
	v_pk_mul_f32 v[26:27], v[26:27], s[2:3] op_sel_hi:[1,0]
	v_rcp_f32_e32 v24, v24
	v_rcp_f32_e32 v25, v25
	v_exp_f32_e32 v26, v26
	v_exp_f32_e32 v27, v27
	v_pk_fma_f32 v[30:31], v[24:25], s[6:7], v[28:29] op_sel_hi:[1,0,0]
	s_nop 0
	v_pk_fma_f32 v[30:31], v[24:25], v[30:31], s[10:11] op_sel_hi:[1,1,0]
	s_nop 0
	v_pk_fma_f32 v[30:31], v[24:25], v[30:31], s[12:13] op_sel_hi:[1,1,0]
	s_nop 0
	v_pk_fma_f32 v[30:31], v[24:25], v[30:31], s[14:15] op_sel_hi:[1,1,0]
	s_nop 0
	v_pk_mul_f32 v[24:25], v[24:25], v[30:31]
	s_nop 0
	v_pk_fma_f32 v[24:25], v[26:27], v[24:25], 1.0 op_sel_hi:[1,1,0] neg_lo:[1,0,0] neg_hi:[1,0,0]
	s_nop 0
	v_bfi_b32 v15, s3, v25, v15
	v_bfi_b32 v14, s3, v24, v14
	v_pk_add_f32 v[14:15], v[14:15], 1.0 op_sel_hi:[1,0]
	s_nop 0
	v_pk_mul_f32 v[22:23], v[22:23], v[14:15]
	v_pk_add_f32 v[14:15], v[2:3], v[20:21]
	v_cvt_pk_f16_f32 v16, v22, v23
	v_pk_mul_f32 v[20:21], v[14:15], 0.5 op_sel_hi:[1,0]
	v_pk_mul_f32 v[14:15], v[14:15], s[4:5] op_sel_hi:[1,0]
	s_nop 0
	v_and_b32_e32 v24, 0x7fffffff, v14
	v_and_b32_e32 v25, 0x7fffffff, v15
	v_pk_mul_f32 v[26:27], v[24:25], v[24:25]
	v_pk_fma_f32 v[24:25], v[24:25], s[8:9], 1.0 op_sel_hi:[1,0,0]
	v_pk_mul_f32 v[26:27], v[26:27], s[2:3] op_sel_hi:[1,0]
	v_rcp_f32_e32 v24, v24
	v_rcp_f32_e32 v25, v25
	v_exp_f32_e32 v26, v26
	v_exp_f32_e32 v27, v27
	v_pk_fma_f32 v[30:31], v[24:25], s[6:7], v[28:29] op_sel_hi:[1,0,0]
	s_nop 0
	v_pk_fma_f32 v[30:31], v[24:25], v[30:31], s[10:11] op_sel_hi:[1,1,0]
	s_nop 0
	v_pk_fma_f32 v[30:31], v[24:25], v[30:31], s[12:13] op_sel_hi:[1,1,0]
	s_nop 0
	v_pk_fma_f32 v[30:31], v[24:25], v[30:31], s[14:15] op_sel_hi:[1,1,0]
	s_nop 0
	v_pk_mul_f32 v[24:25], v[24:25], v[30:31]
	s_nop 0
	v_pk_fma_f32 v[24:25], v[26:27], v[24:25], 1.0 op_sel_hi:[1,1,0] neg_lo:[1,0,0] neg_hi:[1,0,0]
	s_nop 0
	v_bfi_b32 v15, s3, v25, v15
	v_bfi_b32 v14, s3, v24, v14
	v_pk_add_f32 v[14:15], v[14:15], 1.0 op_sel_hi:[1,0]
	s_nop 0
	v_pk_mul_f32 v[14:15], v[20:21], v[14:15]
	v_pk_mul_f32 v[20:21], v[18:19], 0.5 op_sel_hi:[1,0]
	v_pk_mul_f32 v[18:19], v[18:19], s[4:5] op_sel_hi:[1,0]
	v_cvt_pk_f16_f32 v15, v14, v15
	v_and_b32_e32 v24, 0x7fffffff, v18
	v_and_b32_e32 v25, 0x7fffffff, v19
	v_pk_mul_f32 v[26:27], v[24:25], v[24:25]
	v_pk_fma_f32 v[24:25], v[24:25], s[8:9], 1.0 op_sel_hi:[1,0,0]
	v_pk_mul_f32 v[26:27], v[26:27], s[2:3] op_sel_hi:[1,0]
	v_rcp_f32_e32 v24, v24
	v_rcp_f32_e32 v25, v25
	v_exp_f32_e32 v26, v26
	v_exp_f32_e32 v27, v27
	s_movk_i32 s2, 0x1880
	v_pk_fma_f32 v[28:29], v[24:25], s[6:7], v[28:29] op_sel_hi:[1,0,0]
	s_nop 0
	v_pk_fma_f32 v[28:29], v[24:25], v[28:29], s[10:11] op_sel_hi:[1,1,0]
	s_nop 0
	v_pk_fma_f32 v[28:29], v[24:25], v[28:29], s[12:13] op_sel_hi:[1,1,0]
	s_nop 0
	v_pk_fma_f32 v[28:29], v[24:25], v[28:29], s[14:15] op_sel_hi:[1,1,0]
	s_nop 0
	v_pk_mul_f32 v[24:25], v[24:25], v[28:29]
	s_nop 0
	v_pk_fma_f32 v[24:25], v[26:27], v[24:25], 1.0 op_sel_hi:[1,1,0] neg_lo:[1,0,0] neg_hi:[1,0,0]
	s_nop 0
	v_bfi_b32 v19, s3, v25, v19
	v_bfi_b32 v18, s3, v24, v18
	v_pk_add_f32 v[18:19], v[18:19], 1.0 op_sel_hi:[1,0]
	v_mad_i64_i32 v[12:13], s[2:3], v12, s2, v[8:9]
	v_pk_mul_f32 v[18:19], v[20:21], v[18:19]
	s_nop 0
	v_cvt_pk_f16_f32 v14, v18, v19
	global_store_dwordx4 v[12:13], v[14:17], off sc1
.LBB13_18:
	s_or_b64 exec, exec, s[0:1]
	v_or_b32_e32 v12, 56, v76
	v_add_u32_e32 v10, v10, v12
	v_cmp_gt_i32_e32 vcc, s9, v10
	s_and_saveexec_b64 s[0:1], vcc
	s_cbranch_execz .LBB13_20
	s_movk_i32 s0, 0x110
	v_mad_u32_u24 v11, v12, s0, v11
	ds_read_b128 v[12:15], v11 offset:16
	ds_read_b128 v[16:19], v11
	s_mov_b32 s2, 0x3f3504f3
	s_mov_b32 s6, 0x3ea7ba05
	s_mov_b32 s8, 0xbfba00e3
	s_waitcnt vmcnt(1) lgkmcnt(1)
	v_pk_add_f32 v[6:7], v[6:7], v[14:15]
	s_brev_b32 s1, -2
	v_pk_mul_f32 v[14:15], v[6:7], 0.5 op_sel_hi:[1,0]
	v_pk_mul_f32 v[6:7], v[6:7], s[2:3] op_sel_hi:[1,0]
	s_mov_b32 s0, 0xbfb8aa3b
	v_and_b32_e32 v20, 0x7fffffff, v6
	v_and_b32_e32 v21, 0x7fffffff, v7
	v_pk_mul_f32 v[22:23], v[20:21], v[20:21]
	v_pk_fma_f32 v[20:21], v[20:21], s[6:7], 1.0 op_sel_hi:[1,0,0]
	s_mov_b32 s4, 0x3f87dc22
	v_rcp_f32_e32 v20, v20
	v_rcp_f32_e32 v21, v21
	v_mov_b64_e32 v[24:25], s[8:9]
	v_pk_mul_f32 v[22:23], v[22:23], s[0:1] op_sel_hi:[1,0]
	s_mov_b32 s8, 0x3fb5f0e3
	v_pk_fma_f32 v[26:27], v[20:21], s[4:5], v[24:25] op_sel_hi:[1,0,0]
	v_exp_f32_e32 v22, v22
	v_exp_f32_e32 v23, v23
	v_pk_fma_f32 v[26:27], v[20:21], v[26:27], s[8:9] op_sel_hi:[1,1,0]
	s_mov_b32 s10, 0xbe91a98e
	v_pk_fma_f32 v[26:27], v[20:21], v[26:27], s[10:11] op_sel_hi:[1,1,0]
	s_mov_b32 s12, 0x3e827906
	v_pk_fma_f32 v[26:27], v[20:21], v[26:27], s[12:13] op_sel_hi:[1,1,0]
	v_pk_add_f32 v[4:5], v[4:5], v[12:13]
	v_pk_mul_f32 v[20:21], v[20:21], v[26:27]
	v_pk_mul_f32 v[12:13], v[4:5], 0.5 op_sel_hi:[1,0]
	v_pk_fma_f32 v[20:21], v[22:23], v[20:21], 1.0 op_sel_hi:[1,1,0] neg_lo:[1,0,0] neg_hi:[1,0,0]
	v_pk_mul_f32 v[4:5], v[4:5], s[2:3] op_sel_hi:[1,0]
	v_bfi_b32 v7, s1, v21, v7
	v_bfi_b32 v6, s1, v20, v6
	v_pk_add_f32 v[6:7], v[6:7], 1.0 op_sel_hi:[1,0]
	s_waitcnt vmcnt(0) lgkmcnt(0)
	v_pk_add_f32 v[2:3], v[2:3], v[18:19]
	v_pk_mul_f32 v[6:7], v[14:15], v[6:7]
	v_and_b32_e32 v14, 0x7fffffff, v4
	v_and_b32_e32 v15, 0x7fffffff, v5
	v_pk_mul_f32 v[20:21], v[14:15], v[14:15]
	v_pk_fma_f32 v[14:15], v[14:15], s[6:7], 1.0 op_sel_hi:[1,0,0]
	v_pk_mul_f32 v[20:21], v[20:21], s[0:1] op_sel_hi:[1,0]
	v_rcp_f32_e32 v14, v14
	v_rcp_f32_e32 v15, v15
	v_exp_f32_e32 v20, v20
	v_exp_f32_e32 v21, v21
	v_pk_add_f32 v[0:1], v[0:1], v[16:17]
	v_pk_fma_f32 v[22:23], v[14:15], s[4:5], v[24:25] op_sel_hi:[1,0,0]
	s_nop 0
	v_pk_fma_f32 v[22:23], v[14:15], v[22:23], s[8:9] op_sel_hi:[1,1,0]
	s_nop 0
	v_pk_fma_f32 v[22:23], v[14:15], v[22:23], s[10:11] op_sel_hi:[1,1,0]
	s_nop 0
	v_pk_fma_f32 v[22:23], v[14:15], v[22:23], s[12:13] op_sel_hi:[1,1,0]
	s_nop 0
	v_pk_mul_f32 v[14:15], v[14:15], v[22:23]
	s_nop 0
	v_pk_fma_f32 v[14:15], v[20:21], v[14:15], 1.0 op_sel_hi:[1,1,0] neg_lo:[1,0,0] neg_hi:[1,0,0]
	s_nop 0
	v_bfi_b32 v5, s1, v15, v5
	v_bfi_b32 v4, s1, v14, v4
	v_pk_add_f32 v[4:5], v[4:5], 1.0 op_sel_hi:[1,0]
	s_nop 0
	v_pk_mul_f32 v[4:5], v[12:13], v[4:5]
	v_pk_mul_f32 v[12:13], v[2:3], 0.5 op_sel_hi:[1,0]
	v_pk_mul_f32 v[2:3], v[2:3], s[2:3] op_sel_hi:[1,0]
	s_nop 0
	v_and_b32_e32 v14, 0x7fffffff, v2
	v_and_b32_e32 v15, 0x7fffffff, v3
	v_pk_mul_f32 v[18:19], v[14:15], v[14:15]
	v_pk_fma_f32 v[14:15], v[14:15], s[6:7], 1.0 op_sel_hi:[1,0,0]
	v_pk_mul_f32 v[18:19], v[18:19], s[0:1] op_sel_hi:[1,0]
	v_rcp_f32_e32 v14, v14
	v_rcp_f32_e32 v15, v15
	v_exp_f32_e32 v18, v18
	v_exp_f32_e32 v19, v19
	v_pk_fma_f32 v[20:21], v[14:15], s[4:5], v[24:25] op_sel_hi:[1,0,0]
	s_nop 0
	v_pk_fma_f32 v[20:21], v[14:15], v[20:21], s[8:9] op_sel_hi:[1,1,0]
	s_nop 0
	v_pk_fma_f32 v[20:21], v[14:15], v[20:21], s[10:11] op_sel_hi:[1,1,0]
	s_nop 0
	v_pk_fma_f32 v[20:21], v[14:15], v[20:21], s[12:13] op_sel_hi:[1,1,0]
	s_nop 0
	v_pk_mul_f32 v[14:15], v[14:15], v[20:21]
	s_nop 0
	v_pk_fma_f32 v[14:15], v[18:19], v[14:15], 1.0 op_sel_hi:[1,1,0] neg_lo:[1,0,0] neg_hi:[1,0,0]
	s_nop 0
	v_bfi_b32 v3, s1, v15, v3
	v_bfi_b32 v2, s1, v14, v2
	v_pk_add_f32 v[2:3], v[2:3], 1.0 op_sel_hi:[1,0]
	s_nop 0
	v_pk_mul_f32 v[12:13], v[12:13], v[2:3]
	v_pk_mul_f32 v[2:3], v[0:1], 0.5 op_sel_hi:[1,0]
	v_pk_mul_f32 v[0:1], v[0:1], s[2:3] op_sel_hi:[1,0]
	s_nop 0
	v_and_b32_e32 v14, 0x7fffffff, v0
	v_and_b32_e32 v15, 0x7fffffff, v1
	v_pk_mul_f32 v[16:17], v[14:15], v[14:15]
	v_pk_fma_f32 v[14:15], v[14:15], s[6:7], 1.0 op_sel_hi:[1,0,0]
	v_pk_mul_f32 v[16:17], v[16:17], s[0:1] op_sel_hi:[1,0]
	v_rcp_f32_e32 v14, v14
	v_rcp_f32_e32 v15, v15
	v_exp_f32_e32 v16, v16
	v_exp_f32_e32 v17, v17
	s_movk_i32 s0, 0x1880
	v_pk_fma_f32 v[18:19], v[14:15], s[4:5], v[24:25] op_sel_hi:[1,0,0]
	s_nop 0
	v_pk_fma_f32 v[18:19], v[14:15], v[18:19], s[8:9] op_sel_hi:[1,1,0]
	s_nop 0
	v_pk_fma_f32 v[18:19], v[14:15], v[18:19], s[10:11] op_sel_hi:[1,1,0]
	s_nop 0
	v_pk_fma_f32 v[18:19], v[14:15], v[18:19], s[12:13] op_sel_hi:[1,1,0]
	s_nop 0
	v_pk_mul_f32 v[14:15], v[14:15], v[18:19]
	s_nop 0
	v_pk_fma_f32 v[14:15], v[16:17], v[14:15], 1.0 op_sel_hi:[1,1,0] neg_lo:[1,0,0] neg_hi:[1,0,0]
	s_nop 0
	v_bfi_b32 v1, s1, v15, v1
	v_bfi_b32 v0, s1, v14, v0
	v_pk_add_f32 v[0:1], v[0:1], 1.0 op_sel_hi:[1,0]
	s_nop 0
	v_pk_mul_f32 v[14:15], v[2:3], v[0:1]
	v_cvt_pk_f16_f32 v3, v6, v7
	v_cvt_pk_f16_f32 v1, v12, v13
	v_cvt_pk_f16_f32 v2, v4, v5
	v_cvt_pk_f16_f32 v0, v14, v15
	v_mad_i64_i32 v[4:5], s[0:1], v10, s0, v[8:9]
	global_store_dwordx4 v[4:5], v[0:3], off sc1
